# FFT: waves 4-7 start each LDS pass 512 cycles later (s_sleep 8 after the pass barrier) so LDS traffic of one half overlaps the VALU work of the other
# baseline (speedup 1.0000x reference)
.LBB0_755:
	s_waitcnt vmcnt(58)
	v_pk_add_f32 v[2:3], v[10:11], v[42:43] neg_lo:[0,1] neg_hi:[0,1]
	v_mov_b64_e32 v[102:103], s[4:5]
	v_pk_mul_f32 v[4:5], v[2:3], v[102:103] op_sel_hi:[1,0]
	v_mov_b32_e32 v148, v204
	v_pk_fma_f32 v[116:117], v[2:3], v[102:103], v[4:5] op_sel:[1,1,0] op_sel_hi:[0,1,1] neg_hi:[1,0,0]
	s_waitcnt vmcnt(54)
	v_pk_add_f32 v[4:5], v[14:15], v[46:47] neg_lo:[0,1] neg_hi:[0,1]
	v_mov_b64_e32 v[2:3], s[6:7]
	v_pk_mul_f32 v[104:105], v[4:5], v[2:3] op_sel_hi:[1,0]
	v_pk_add_f32 v[114:115], v[42:43], v[10:11]
	v_pk_fma_f32 v[120:121], v[4:5], v[2:3], v[104:105] op_sel:[1,1,0] op_sel_hi:[0,1,1] neg_hi:[1,0,0]
	s_waitcnt vmcnt(50)
	v_pk_add_f32 v[4:5], v[18:19], v[50:51] neg_lo:[0,1] neg_hi:[0,1]
	v_mov_b64_e32 v[104:105], s[10:11]
	v_pk_mul_f32 v[106:107], v[4:5], v[104:105] op_sel_hi:[1,0]
	v_cmp_ne_u32_e32 vcc, 0, v148
	v_pk_fma_f32 v[124:125], v[4:5], v[104:105], v[106:107] op_sel:[1,1,0] op_sel_hi:[0,1,1] neg_hi:[1,0,0]
	s_waitcnt vmcnt(42)
	v_pk_add_f32 v[4:5], v[26:27], v[58:59] neg_lo:[0,1] neg_hi:[0,1]
	v_mov_b64_e32 v[106:107], s[12:13]
	v_pk_mul_f32 v[108:109], v[4:5], v[106:107] op_sel_hi:[1,0]
	v_cndmask_b32_e32 v38, 0, v205, vcc
	v_pk_fma_f32 v[132:133], v[4:5], v[106:107], v[108:109] op_sel:[1,1,0] op_sel_hi:[0,1,1] neg_hi:[1,0,0]
	s_waitcnt vmcnt(38)
	v_pk_add_f32 v[108:109], v[30:31], v[62:63] neg_lo:[0,1] neg_hi:[0,1]
	v_mov_b64_e32 v[4:5], s[14:15]
	v_pk_mul_f32 v[136:137], v[108:109], v[4:5] op_sel_hi:[1,0]
	v_pk_add_f32 v[110:111], v[6:7], v[38:39]
	v_pk_add_f32 v[126:127], v[54:55], v[22:23]
	v_pk_add_f32 v[130:131], v[58:59], v[26:27]
	v_pk_fma_f32 v[136:137], v[108:109], v[4:5], v[136:137] op_sel:[1,1,0] op_sel_hi:[0,1,1] neg_hi:[1,0,0]
	s_waitcnt vmcnt(34)
	v_pk_add_f32 v[140:141], v[34:35], v[66:67] neg_lo:[0,1] neg_hi:[0,1]
	v_mov_b64_e32 v[108:109], s[16:17]
	v_pk_mul_f32 v[142:143], v[140:141], v[108:109] op_sel_hi:[1,0]
	v_pk_add_f32 v[112:113], v[6:7], v[38:39] neg_lo:[0,1] neg_hi:[0,1]
	v_pk_add_f32 v[118:119], v[46:47], v[14:15]
	v_pk_add_f32 v[122:123], v[50:51], v[18:19]
	v_pk_add_f32 v[134:135], v[62:63], v[30:31]
	v_pk_add_f32 v[138:139], v[66:67], v[34:35]
	v_pk_fma_f32 v[140:141], v[140:141], v[108:109], v[142:143] op_sel:[1,1,0] op_sel_hi:[0,1,1] neg_hi:[1,0,0]
	v_pk_add_f32 v[142:143], v[126:127], v[110:111]
	v_pk_add_f32 v[110:111], v[110:111], v[126:127] neg_lo:[0,1] neg_hi:[0,1]
	v_pk_add_f32 v[126:127], v[114:115], v[130:131]
	v_pk_add_f32 v[114:115], v[114:115], v[130:131] neg_lo:[0,1] neg_hi:[0,1]
	v_cvt_f32_i32_e32 v38, v148
	v_pk_mul_f32 v[130:131], v[114:115], v[2:3] op_sel_hi:[1,0]
	v_pk_add_f32 v[128:129], v[22:23], v[54:55] op_sel:[1,1] op_sel_hi:[0,0] neg_lo:[0,1] neg_hi:[1,0]
	v_and_b32_e32 v149, -8, v148
	v_pk_fma_f32 v[114:115], v[114:115], v[2:3], v[130:131] op_sel:[1,1,0] op_sel_hi:[0,1,1] neg_hi:[1,0,0]
	v_pk_add_f32 v[130:131], v[118:119], v[134:135]
	v_pk_add_f32 v[118:119], v[118:119], v[134:135] op_sel:[1,1] op_sel_hi:[0,0] neg_lo:[0,1] neg_hi:[1,0]
	v_pk_add_f32 v[134:135], v[122:123], v[138:139]
	v_pk_add_f32 v[122:123], v[122:123], v[138:139] neg_lo:[0,1] neg_hi:[0,1]
	v_mul_f32_e32 v38, 0x38800000, v38
	v_pk_mul_f32 v[138:139], v[122:123], v[4:5] op_sel_hi:[1,0]
	v_cos_f32_e32 v144, v38
	v_pk_fma_f32 v[122:123], v[122:123], v[4:5], v[138:139] op_sel:[1,1,0] op_sel_hi:[0,1,1] neg_hi:[1,0,0]
	v_pk_add_f32 v[138:139], v[112:113], v[128:129]
	v_pk_add_f32 v[112:113], v[112:113], v[128:129] neg_lo:[0,1] neg_hi:[0,1]
	v_pk_add_f32 v[128:129], v[116:117], v[132:133]
	v_pk_add_f32 v[116:117], v[116:117], v[132:133] neg_lo:[0,1] neg_hi:[0,1]
	v_sin_f32_e32 v145, v38
	v_pk_mul_f32 v[132:133], v[116:117], v[2:3] op_sel_hi:[1,0]
	v_lshlrev_b32_e32 v38, 3, v148
	v_pk_fma_f32 v[116:117], v[116:117], v[2:3], v[132:133] op_sel:[1,1,0] op_sel_hi:[0,1,1] neg_hi:[1,0,0]
	v_pk_add_f32 v[132:133], v[120:121], v[136:137]
	v_pk_add_f32 v[120:121], v[120:121], v[136:137] op_sel:[1,1] op_sel_hi:[0,0] neg_lo:[0,1] neg_hi:[1,0]
	v_pk_add_f32 v[136:137], v[124:125], v[140:141]
	v_pk_add_f32 v[124:125], v[124:125], v[140:141] neg_lo:[0,1] neg_hi:[0,1]
	s_mov_b64 s[84:85], -1
	v_pk_mul_f32 v[140:141], v[124:125], v[4:5] op_sel_hi:[1,0]
	s_mov_b32 s86, 0
	v_pk_fma_f32 v[124:125], v[124:125], v[4:5], v[140:141] op_sel:[1,1,0] op_sel_hi:[0,1,1] neg_hi:[1,0,0]
	v_pk_add_f32 v[140:141], v[130:131], v[142:143]
	v_pk_add_f32 v[130:131], v[142:143], v[130:131] neg_lo:[0,1] neg_hi:[0,1]
	v_pk_add_f32 v[142:143], v[126:127], v[134:135]
	v_pk_add_f32 v[126:127], v[126:127], v[134:135] op_sel:[1,1] op_sel_hi:[0,0] neg_lo:[0,1] neg_hi:[1,0]
	v_pk_add_f32 v[134:135], v[110:111], v[118:119]
	v_pk_add_f32 v[110:111], v[110:111], v[118:119] neg_lo:[0,1] neg_hi:[0,1]
	v_pk_add_f32 v[118:119], v[114:115], v[122:123]
	v_pk_add_f32 v[114:115], v[114:115], v[122:123] op_sel:[1,1] op_sel_hi:[0,0] neg_lo:[0,1] neg_hi:[1,0]
	v_pk_add_f32 v[122:123], v[138:139], v[132:133]
	v_pk_add_f32 v[132:133], v[138:139], v[132:133] neg_lo:[0,1] neg_hi:[0,1]
	v_pk_add_f32 v[138:139], v[128:129], v[136:137]
	v_pk_add_f32 v[128:129], v[128:129], v[136:137] op_sel:[1,1] op_sel_hi:[0,0] neg_lo:[0,1] neg_hi:[1,0]
	v_pk_add_f32 v[136:137], v[112:113], v[120:121]
	v_pk_add_f32 v[112:113], v[112:113], v[120:121] neg_lo:[0,1] neg_hi:[0,1]
	v_pk_add_f32 v[120:121], v[116:117], v[124:125]
	v_pk_add_f32 v[116:117], v[116:117], v[124:125] op_sel:[1,1] op_sel_hi:[0,0] neg_lo:[0,1] neg_hi:[1,0]
	v_pk_add_f32 v[124:125], v[142:143], v[140:141]
	v_pk_add_f32 v[140:141], v[140:141], v[142:143] neg_lo:[0,1] neg_hi:[0,1]
	v_pk_add_f32 v[142:143], v[130:131], v[126:127]
	v_pk_add_f32 v[126:127], v[130:131], v[126:127] neg_lo:[0,1] neg_hi:[0,1]
	v_pk_add_f32 v[130:131], v[134:135], v[118:119]
	v_pk_add_f32 v[118:119], v[134:135], v[118:119] neg_lo:[0,1] neg_hi:[0,1]
	v_pk_add_f32 v[134:135], v[110:111], v[114:115]
	v_pk_add_f32 v[110:111], v[110:111], v[114:115] neg_lo:[0,1] neg_hi:[0,1]
	v_pk_add_f32 v[114:115], v[122:123], v[138:139]
	v_pk_add_f32 v[122:123], v[122:123], v[138:139] neg_lo:[0,1] neg_hi:[0,1]
	v_pk_add_f32 v[138:139], v[132:133], v[128:129]
	v_pk_add_f32 v[128:129], v[132:133], v[128:129] neg_lo:[0,1] neg_hi:[0,1]
	v_pk_add_f32 v[132:133], v[136:137], v[120:121]
	v_pk_add_f32 v[120:121], v[136:137], v[120:121] neg_lo:[0,1] neg_hi:[0,1]
	v_pk_add_f32 v[136:137], v[112:113], v[116:117]
	v_pk_add_f32 v[112:113], v[112:113], v[116:117] neg_lo:[0,1] neg_hi:[0,1]
	v_pk_mul_f32 v[116:117], v[114:115], v[144:145] op_sel_hi:[1,0]
	s_nop 0
	v_pk_fma_f32 v[114:115], v[114:115], v[144:145], v[116:117] op_sel:[1,1,0] op_sel_hi:[0,1,1] neg_hi:[1,0,0]
	v_pk_mul_f32 v[116:117], v[144:145], v[144:145] op_sel_hi:[1,0]
	s_nop 0
	v_pk_fma_f32 v[116:117], v[144:145], v[144:145], v[116:117] op_sel:[1,1,0] op_sel_hi:[0,1,1] neg_lo:[1,0,0]
	s_nop 0
	v_pk_mul_f32 v[146:147], v[130:131], v[116:117] op_sel_hi:[1,0]
	s_nop 0
	v_pk_fma_f32 v[130:131], v[130:131], v[116:117], v[146:147] op_sel:[1,1,0] op_sel_hi:[0,1,1] neg_hi:[1,0,0]
	v_pk_mul_f32 v[146:147], v[116:117], v[144:145] op_sel_hi:[1,0]
	s_nop 0
	v_pk_fma_f32 v[116:117], v[116:117], v[144:145], v[146:147] op_sel:[1,1,0] op_sel_hi:[0,1,1] neg_lo:[1,0,0]
	s_nop 0
	v_pk_mul_f32 v[146:147], v[132:133], v[116:117] op_sel_hi:[1,0]
	s_nop 0
	v_pk_fma_f32 v[132:133], v[132:133], v[116:117], v[146:147] op_sel:[1,1,0] op_sel_hi:[0,1,1] neg_hi:[1,0,0]
	v_pk_mul_f32 v[146:147], v[116:117], v[144:145] op_sel_hi:[1,0]
	s_nop 0
	v_pk_fma_f32 v[116:117], v[116:117], v[144:145], v[146:147] op_sel:[1,1,0] op_sel_hi:[0,1,1] neg_lo:[1,0,0]
	s_nop 0
	v_pk_mul_f32 v[146:147], v[142:143], v[116:117] op_sel_hi:[1,0]
	s_nop 0
	v_pk_fma_f32 v[142:143], v[142:143], v[116:117], v[146:147] op_sel:[1,1,0] op_sel_hi:[0,1,1] neg_hi:[1,0,0]
	v_pk_mul_f32 v[146:147], v[116:117], v[144:145] op_sel_hi:[1,0]
	s_nop 0
	v_pk_fma_f32 v[116:117], v[116:117], v[144:145], v[146:147] op_sel:[1,1,0] op_sel_hi:[0,1,1] neg_lo:[1,0,0]
	s_nop 0
	v_pk_mul_f32 v[146:147], v[138:139], v[116:117] op_sel_hi:[1,0]
	s_nop 0
	v_pk_fma_f32 v[138:139], v[138:139], v[116:117], v[146:147] op_sel:[1,1,0] op_sel_hi:[0,1,1] neg_hi:[1,0,0]
	v_pk_mul_f32 v[146:147], v[116:117], v[144:145] op_sel_hi:[1,0]
	s_nop 0
	v_pk_fma_f32 v[116:117], v[116:117], v[144:145], v[146:147] op_sel:[1,1,0] op_sel_hi:[0,1,1] neg_lo:[1,0,0]
	s_nop 0
	v_pk_mul_f32 v[146:147], v[134:135], v[116:117] op_sel_hi:[1,0]
	s_nop 0
	v_pk_fma_f32 v[134:135], v[134:135], v[116:117], v[146:147] op_sel:[1,1,0] op_sel_hi:[0,1,1] neg_hi:[1,0,0]
	v_pk_mul_f32 v[146:147], v[116:117], v[144:145] op_sel_hi:[1,0]
	s_nop 0
	v_pk_fma_f32 v[116:117], v[116:117], v[144:145], v[146:147] op_sel:[1,1,0] op_sel_hi:[0,1,1] neg_lo:[1,0,0]
	s_nop 0
	v_pk_mul_f32 v[146:147], v[136:137], v[116:117] op_sel_hi:[1,0]
	s_nop 0
	v_pk_fma_f32 v[136:137], v[136:137], v[116:117], v[146:147] op_sel:[1,1,0] op_sel_hi:[0,1,1] neg_hi:[1,0,0]
	v_pk_mul_f32 v[146:147], v[116:117], v[144:145] op_sel_hi:[1,0]
	s_nop 0
	v_pk_fma_f32 v[116:117], v[116:117], v[144:145], v[146:147] op_sel:[1,1,0] op_sel_hi:[0,1,1] neg_lo:[1,0,0]
	s_nop 0
	v_pk_mul_f32 v[146:147], v[140:141], v[116:117] op_sel_hi:[1,0]
	s_nop 0
	v_pk_fma_f32 v[140:141], v[140:141], v[116:117], v[146:147] op_sel:[1,1,0] op_sel_hi:[0,1,1] neg_hi:[1,0,0]
	v_pk_mul_f32 v[146:147], v[116:117], v[144:145] op_sel_hi:[1,0]
	s_nop 0
	v_pk_fma_f32 v[116:117], v[116:117], v[144:145], v[146:147] op_sel:[1,1,0] op_sel_hi:[0,1,1] neg_lo:[1,0,0]
	s_nop 0
	v_pk_mul_f32 v[146:147], v[122:123], v[116:117] op_sel_hi:[1,0]
	s_nop 0
	v_pk_fma_f32 v[122:123], v[122:123], v[116:117], v[146:147] op_sel:[1,1,0] op_sel_hi:[0,1,1] neg_hi:[1,0,0]
	v_pk_mul_f32 v[146:147], v[116:117], v[144:145] op_sel_hi:[1,0]
	s_nop 0
	v_pk_fma_f32 v[116:117], v[116:117], v[144:145], v[146:147] op_sel:[1,1,0] op_sel_hi:[0,1,1] neg_lo:[1,0,0]
	s_nop 0
	v_pk_mul_f32 v[146:147], v[118:119], v[116:117] op_sel_hi:[1,0]
	s_nop 0
	v_pk_fma_f32 v[118:119], v[118:119], v[116:117], v[146:147] op_sel:[1,1,0] op_sel_hi:[0,1,1] neg_hi:[1,0,0]
	v_pk_mul_f32 v[146:147], v[116:117], v[144:145] op_sel_hi:[1,0]
	s_nop 0
	v_pk_fma_f32 v[116:117], v[116:117], v[144:145], v[146:147] op_sel:[1,1,0] op_sel_hi:[0,1,1] neg_lo:[1,0,0]
	s_nop 0
	v_pk_mul_f32 v[146:147], v[120:121], v[116:117] op_sel_hi:[1,0]
	s_nop 0
	v_pk_fma_f32 v[120:121], v[120:121], v[116:117], v[146:147] op_sel:[1,1,0] op_sel_hi:[0,1,1] neg_hi:[1,0,0]
	v_pk_mul_f32 v[146:147], v[116:117], v[144:145] op_sel_hi:[1,0]
	s_nop 0
	v_pk_fma_f32 v[116:117], v[116:117], v[144:145], v[146:147] op_sel:[1,1,0] op_sel_hi:[0,1,1] neg_lo:[1,0,0]
	s_nop 0
	v_pk_mul_f32 v[146:147], v[126:127], v[116:117] op_sel_hi:[1,0]
	s_nop 0
	v_pk_fma_f32 v[126:127], v[126:127], v[116:117], v[146:147] op_sel:[1,1,0] op_sel_hi:[0,1,1] neg_hi:[1,0,0]
	v_pk_mul_f32 v[146:147], v[116:117], v[144:145] op_sel_hi:[1,0]
	s_nop 0
	v_pk_fma_f32 v[116:117], v[116:117], v[144:145], v[146:147] op_sel:[1,1,0] op_sel_hi:[0,1,1] neg_lo:[1,0,0]
	s_nop 0
	v_pk_mul_f32 v[146:147], v[128:129], v[116:117] op_sel_hi:[1,0]
	s_nop 0
	v_pk_fma_f32 v[128:129], v[128:129], v[116:117], v[146:147] op_sel:[1,1,0] op_sel_hi:[0,1,1] neg_hi:[1,0,0]
	v_pk_mul_f32 v[146:147], v[116:117], v[144:145] op_sel_hi:[1,0]
	s_nop 0
	v_pk_fma_f32 v[116:117], v[116:117], v[144:145], v[146:147] op_sel:[1,1,0] op_sel_hi:[0,1,1] neg_lo:[1,0,0]
	s_nop 0
	v_pk_mul_f32 v[146:147], v[110:111], v[116:117] op_sel_hi:[1,0]
	s_nop 0
	v_pk_fma_f32 v[110:111], v[110:111], v[116:117], v[146:147] op_sel:[1,1,0] op_sel_hi:[0,1,1] neg_hi:[1,0,0]
	v_pk_mul_f32 v[146:147], v[116:117], v[144:145] op_sel_hi:[1,0]
	s_nop 0
	v_pk_fma_f32 v[116:117], v[116:117], v[144:145], v[146:147] op_sel:[1,1,0] op_sel_hi:[0,1,1] neg_lo:[1,0,0]
	s_nop 0
	v_pk_mul_f32 v[144:145], v[112:113], v[116:117] op_sel_hi:[1,0]
	s_nop 0
	v_pk_fma_f32 v[112:113], v[112:113], v[116:117], v[144:145] op_sel:[1,1,0] op_sel_hi:[0,1,1] neg_hi:[1,0,0]
	v_add3_u32 v116, 0, v149, v38
	ds_write2st64_b64 v116, v[124:125], v[114:115] offset1:18
	ds_write2st64_b64 v116, v[130:131], v[132:133] offset0:36 offset1:54
	ds_write2st64_b64 v116, v[142:143], v[138:139] offset0:72 offset1:90
	ds_write2st64_b64 v116, v[134:135], v[136:137] offset0:108 offset1:126
	v_add_u32_e32 v114, 0x12000, v116
	ds_write_b64 v114, v[140:141]
	v_add_u32_e32 v114, 0x14400, v116
	ds_write_b64 v114, v[122:123]
	v_add_u32_e32 v114, 0x16800, v116
	ds_write_b64 v114, v[118:119]
	v_add_u32_e32 v114, 0x18c00, v116
	ds_write_b64 v114, v[120:121]
	v_add_u32_e32 v114, 0x1b000, v116
	ds_write_b64 v114, v[126:127]
	v_add_u32_e32 v114, 0x1d400, v116
	ds_write_b64 v114, v[128:129]
	v_add_u32_e32 v114, 0x1f800, v116
	ds_write_b64 v114, v[110:111]
	v_add_u32_e32 v110, 0x21c00, v116
	v_pk_add_f32 v[116:117], v[12:13], v[44:45] neg_lo:[0,1] neg_hi:[0,1]
	v_pk_add_f32 v[122:123], v[20:21], v[52:53] neg_lo:[0,1] neg_hi:[0,1]
	v_pk_mul_f32 v[118:119], v[116:117], v[102:103] op_sel_hi:[1,0]
	v_pk_add_f32 v[128:129], v[28:29], v[60:61] neg_lo:[0,1] neg_hi:[0,1]
	ds_write_b64 v110, v[112:113]
	v_pk_mul_f32 v[130:131], v[128:129], v[106:107] op_sel_hi:[1,0]
	v_pk_add_f32 v[110:111], v[40:41], v[8:9]
	v_pk_add_f32 v[114:115], v[44:45], v[12:13]
	v_pk_fma_f32 v[102:103], v[116:117], v[102:103], v[118:119] op_sel:[1,1,0] op_sel_hi:[0,1,1] neg_hi:[1,0,0]
	v_pk_add_f32 v[118:119], v[16:17], v[48:49] neg_lo:[0,1] neg_hi:[0,1]
	v_pk_mul_f32 v[124:125], v[122:123], v[104:105] op_sel_hi:[1,0]
	v_pk_add_f32 v[126:127], v[60:61], v[28:29]
	v_pk_mul_f32 v[120:121], v[118:119], v[2:3] op_sel_hi:[1,0]
	v_pk_fma_f32 v[104:105], v[122:123], v[104:105], v[124:125] op_sel:[1,1,0] op_sel_hi:[0,1,1] neg_hi:[1,0,0]
	v_pk_add_f32 v[122:123], v[56:57], v[24:25]
	v_pk_fma_f32 v[106:107], v[128:129], v[106:107], v[130:131] op_sel:[1,1,0] op_sel_hi:[0,1,1] neg_hi:[1,0,0]
	v_pk_add_f32 v[130:131], v[32:33], v[64:65] neg_lo:[0,1] neg_hi:[0,1]
	s_waitcnt vmcnt(32)
	v_pk_add_f32 v[134:135], v[36:37], v[68:69] neg_lo:[0,1] neg_hi:[0,1]
	v_pk_mul_f32 v[132:133], v[130:131], v[4:5] op_sel_hi:[1,0]
	v_pk_add_f32 v[116:117], v[48:49], v[16:17]
	v_pk_fma_f32 v[118:119], v[118:119], v[2:3], v[120:121] op_sel:[1,1,0] op_sel_hi:[0,1,1] neg_hi:[1,0,0]
	v_pk_add_f32 v[120:121], v[52:53], v[20:21]
	v_pk_add_f32 v[128:129], v[64:65], v[32:33]
	v_pk_fma_f32 v[130:131], v[130:131], v[4:5], v[132:133] op_sel:[1,1,0] op_sel_hi:[0,1,1] neg_hi:[1,0,0]
	v_pk_add_f32 v[132:133], v[68:69], v[36:37]
	v_pk_mul_f32 v[136:137], v[134:135], v[108:109] op_sel_hi:[1,0]
	v_pk_add_f32 v[112:113], v[8:9], v[40:41] neg_lo:[0,1] neg_hi:[0,1]
	v_pk_fma_f32 v[108:109], v[134:135], v[108:109], v[136:137] op_sel:[1,1,0] op_sel_hi:[0,1,1] neg_hi:[1,0,0]
	v_pk_add_f32 v[134:135], v[110:111], v[122:123]
	v_pk_add_f32 v[110:111], v[110:111], v[122:123] neg_lo:[0,1] neg_hi:[0,1]
	v_pk_add_f32 v[122:123], v[114:115], v[126:127]
	v_pk_add_f32 v[114:115], v[114:115], v[126:127] neg_lo:[0,1] neg_hi:[0,1]
	v_pk_add_f32 v[124:125], v[24:25], v[56:57] op_sel:[1,1] op_sel_hi:[0,0] neg_lo:[0,1] neg_hi:[1,0]
	v_add_u32_e32 v138, 0x200, v148
	v_pk_mul_f32 v[126:127], v[114:115], v[2:3] op_sel_hi:[1,0]
	v_and_b32_e32 v139, -8, v138
	v_pk_fma_f32 v[114:115], v[114:115], v[2:3], v[126:127] op_sel:[1,1,0] op_sel_hi:[0,1,1] neg_hi:[1,0,0]
	v_pk_add_f32 v[126:127], v[116:117], v[128:129]
	v_pk_add_f32 v[116:117], v[116:117], v[128:129] op_sel:[1,1] op_sel_hi:[0,0] neg_lo:[0,1] neg_hi:[1,0]
	v_pk_add_f32 v[128:129], v[120:121], v[132:133]
	v_pk_add_f32 v[120:121], v[120:121], v[132:133] neg_lo:[0,1] neg_hi:[0,1]
	v_add3_u32 v38, 0, v139, v38
	v_pk_mul_f32 v[132:133], v[120:121], v[4:5] op_sel_hi:[1,0]
	s_nop 0
	v_pk_fma_f32 v[120:121], v[120:121], v[4:5], v[132:133] op_sel:[1,1,0] op_sel_hi:[0,1,1] neg_hi:[1,0,0]
	v_pk_add_f32 v[132:133], v[112:113], v[124:125]
	v_pk_add_f32 v[112:113], v[112:113], v[124:125] neg_lo:[0,1] neg_hi:[0,1]
	v_pk_add_f32 v[124:125], v[102:103], v[106:107]
	v_pk_add_f32 v[102:103], v[102:103], v[106:107] neg_lo:[0,1] neg_hi:[0,1]
	s_nop 0
	v_pk_mul_f32 v[106:107], v[102:103], v[2:3] op_sel_hi:[1,0]
	s_nop 0
	v_pk_fma_f32 v[2:3], v[102:103], v[2:3], v[106:107] op_sel:[1,1,0] op_sel_hi:[0,1,1] neg_hi:[1,0,0]
	v_pk_add_f32 v[102:103], v[118:119], v[130:131]
	v_pk_add_f32 v[106:107], v[118:119], v[130:131] op_sel:[1,1] op_sel_hi:[0,0] neg_lo:[0,1] neg_hi:[1,0]
	v_pk_add_f32 v[118:119], v[104:105], v[108:109]
	v_pk_add_f32 v[104:105], v[104:105], v[108:109] neg_lo:[0,1] neg_hi:[0,1]
	v_pk_add_f32 v[130:131], v[124:125], v[118:119]
	v_pk_mul_f32 v[108:109], v[104:105], v[4:5] op_sel_hi:[1,0]
	v_pk_add_f32 v[118:119], v[124:125], v[118:119] op_sel:[1,1] op_sel_hi:[0,0] neg_lo:[0,1] neg_hi:[1,0]
	v_pk_add_f32 v[124:125], v[112:113], v[106:107]
	v_pk_fma_f32 v[4:5], v[104:105], v[4:5], v[108:109] op_sel:[1,1,0] op_sel_hi:[0,1,1] neg_hi:[1,0,0]
	v_pk_add_f32 v[104:105], v[134:135], v[126:127]
	v_pk_add_f32 v[108:109], v[134:135], v[126:127] neg_lo:[0,1] neg_hi:[0,1]
	v_pk_add_f32 v[126:127], v[122:123], v[128:129]
	v_pk_add_f32 v[122:123], v[122:123], v[128:129] op_sel:[1,1] op_sel_hi:[0,0] neg_lo:[0,1] neg_hi:[1,0]
	v_pk_add_f32 v[128:129], v[110:111], v[116:117]
	v_pk_add_f32 v[110:111], v[110:111], v[116:117] neg_lo:[0,1] neg_hi:[0,1]
	v_pk_add_f32 v[116:117], v[114:115], v[120:121]
	v_pk_add_f32 v[114:115], v[114:115], v[120:121] op_sel:[1,1] op_sel_hi:[0,0] neg_lo:[0,1] neg_hi:[1,0]
	v_pk_add_f32 v[120:121], v[132:133], v[102:103]
	v_pk_add_f32 v[102:103], v[132:133], v[102:103] neg_lo:[0,1] neg_hi:[0,1]
	v_cvt_f32_i32_e32 v132, v138
	v_pk_add_f32 v[106:107], v[112:113], v[106:107] neg_lo:[0,1] neg_hi:[0,1]
	v_pk_add_f32 v[112:113], v[2:3], v[4:5]
	v_pk_add_f32 v[2:3], v[2:3], v[4:5] op_sel:[1,1] op_sel_hi:[0,0] neg_lo:[0,1] neg_hi:[1,0]
	v_mul_f32_e32 v133, 0x38800000, v132
	v_pk_add_f32 v[4:5], v[104:105], v[126:127]
	v_pk_add_f32 v[104:105], v[104:105], v[126:127] neg_lo:[0,1] neg_hi:[0,1]
	v_pk_add_f32 v[126:127], v[108:109], v[122:123]
	v_pk_add_f32 v[108:109], v[108:109], v[122:123] neg_lo:[0,1] neg_hi:[0,1]
	v_pk_add_f32 v[122:123], v[128:129], v[116:117]
	v_pk_add_f32 v[116:117], v[128:129], v[116:117] neg_lo:[0,1] neg_hi:[0,1]
	v_pk_add_f32 v[128:129], v[110:111], v[114:115]
	v_pk_add_f32 v[110:111], v[110:111], v[114:115] neg_lo:[0,1] neg_hi:[0,1]
	v_pk_add_f32 v[114:115], v[120:121], v[130:131]
	v_pk_add_f32 v[120:121], v[120:121], v[130:131] neg_lo:[0,1] neg_hi:[0,1]
	v_pk_add_f32 v[130:131], v[102:103], v[118:119]
	v_pk_add_f32 v[102:103], v[102:103], v[118:119] neg_lo:[0,1] neg_hi:[0,1]
	v_pk_add_f32 v[118:119], v[124:125], v[112:113]
	v_cos_f32_e32 v132, v133
	v_sin_f32_e32 v133, v133
	v_pk_add_f32 v[112:113], v[124:125], v[112:113] neg_lo:[0,1] neg_hi:[0,1]
	v_pk_add_f32 v[124:125], v[106:107], v[2:3]
	v_pk_add_f32 v[2:3], v[106:107], v[2:3] neg_lo:[0,1] neg_hi:[0,1]
	v_pk_mul_f32 v[106:107], v[114:115], v[132:133] op_sel_hi:[1,0]
	s_nop 0
	v_pk_fma_f32 v[106:107], v[114:115], v[132:133], v[106:107] op_sel:[1,1,0] op_sel_hi:[0,1,1] neg_hi:[1,0,0]
	v_pk_mul_f32 v[114:115], v[132:133], v[132:133] op_sel_hi:[1,0]
	s_nop 0
	v_pk_fma_f32 v[114:115], v[132:133], v[132:133], v[114:115] op_sel:[1,1,0] op_sel_hi:[0,1,1] neg_lo:[1,0,0]
	s_nop 0
	v_pk_mul_f32 v[134:135], v[122:123], v[114:115] op_sel_hi:[1,0]
	s_nop 0
	v_pk_fma_f32 v[122:123], v[122:123], v[114:115], v[134:135] op_sel:[1,1,0] op_sel_hi:[0,1,1] neg_hi:[1,0,0]
	v_pk_mul_f32 v[134:135], v[114:115], v[132:133] op_sel_hi:[1,0]
	s_nop 0
	v_pk_fma_f32 v[114:115], v[114:115], v[132:133], v[134:135] op_sel:[1,1,0] op_sel_hi:[0,1,1] neg_lo:[1,0,0]
	s_nop 0
	v_pk_mul_f32 v[134:135], v[118:119], v[114:115] op_sel_hi:[1,0]
	s_nop 0
	v_pk_fma_f32 v[118:119], v[118:119], v[114:115], v[134:135] op_sel:[1,1,0] op_sel_hi:[0,1,1] neg_hi:[1,0,0]
	v_pk_mul_f32 v[134:135], v[114:115], v[132:133] op_sel_hi:[1,0]
	s_nop 0
	v_pk_fma_f32 v[114:115], v[114:115], v[132:133], v[134:135] op_sel:[1,1,0] op_sel_hi:[0,1,1] neg_lo:[1,0,0]
	s_nop 0
	v_pk_mul_f32 v[134:135], v[126:127], v[114:115] op_sel_hi:[1,0]
	s_nop 0
	v_pk_fma_f32 v[126:127], v[126:127], v[114:115], v[134:135] op_sel:[1,1,0] op_sel_hi:[0,1,1] neg_hi:[1,0,0]
	v_pk_mul_f32 v[134:135], v[114:115], v[132:133] op_sel_hi:[1,0]
	s_nop 0
	v_pk_fma_f32 v[114:115], v[114:115], v[132:133], v[134:135] op_sel:[1,1,0] op_sel_hi:[0,1,1] neg_lo:[1,0,0]
	s_nop 0
	v_pk_mul_f32 v[134:135], v[130:131], v[114:115] op_sel_hi:[1,0]
	s_nop 0
	v_pk_fma_f32 v[130:131], v[130:131], v[114:115], v[134:135] op_sel:[1,1,0] op_sel_hi:[0,1,1] neg_hi:[1,0,0]
	v_pk_mul_f32 v[134:135], v[114:115], v[132:133] op_sel_hi:[1,0]
	s_nop 0
	v_pk_fma_f32 v[114:115], v[114:115], v[132:133], v[134:135] op_sel:[1,1,0] op_sel_hi:[0,1,1] neg_lo:[1,0,0]
	s_nop 0
	v_pk_mul_f32 v[134:135], v[128:129], v[114:115] op_sel_hi:[1,0]
	s_nop 0
	v_pk_fma_f32 v[128:129], v[128:129], v[114:115], v[134:135] op_sel:[1,1,0] op_sel_hi:[0,1,1] neg_hi:[1,0,0]
	v_pk_mul_f32 v[134:135], v[114:115], v[132:133] op_sel_hi:[1,0]
	s_nop 0
	v_pk_fma_f32 v[114:115], v[114:115], v[132:133], v[134:135] op_sel:[1,1,0] op_sel_hi:[0,1,1] neg_lo:[1,0,0]
	s_nop 0
	v_pk_mul_f32 v[134:135], v[124:125], v[114:115] op_sel_hi:[1,0]
	s_nop 0
	v_pk_fma_f32 v[124:125], v[124:125], v[114:115], v[134:135] op_sel:[1,1,0] op_sel_hi:[0,1,1] neg_hi:[1,0,0]
	v_pk_mul_f32 v[134:135], v[114:115], v[132:133] op_sel_hi:[1,0]
	s_nop 0
	v_pk_fma_f32 v[114:115], v[114:115], v[132:133], v[134:135] op_sel:[1,1,0] op_sel_hi:[0,1,1] neg_lo:[1,0,0]
	s_nop 0
	v_pk_mul_f32 v[134:135], v[104:105], v[114:115] op_sel_hi:[1,0]
	s_nop 0
	v_pk_fma_f32 v[104:105], v[104:105], v[114:115], v[134:135] op_sel:[1,1,0] op_sel_hi:[0,1,1] neg_hi:[1,0,0]
	v_pk_mul_f32 v[134:135], v[114:115], v[132:133] op_sel_hi:[1,0]
	s_nop 0
	v_pk_fma_f32 v[114:115], v[114:115], v[132:133], v[134:135] op_sel:[1,1,0] op_sel_hi:[0,1,1] neg_lo:[1,0,0]
	s_nop 0
	v_pk_mul_f32 v[134:135], v[120:121], v[114:115] op_sel_hi:[1,0]
	s_nop 0
	v_pk_fma_f32 v[120:121], v[120:121], v[114:115], v[134:135] op_sel:[1,1,0] op_sel_hi:[0,1,1] neg_hi:[1,0,0]
	v_pk_mul_f32 v[134:135], v[114:115], v[132:133] op_sel_hi:[1,0]
	s_nop 0
	v_pk_fma_f32 v[114:115], v[114:115], v[132:133], v[134:135] op_sel:[1,1,0] op_sel_hi:[0,1,1] neg_lo:[1,0,0]
	s_nop 0
	v_pk_mul_f32 v[134:135], v[116:117], v[114:115] op_sel_hi:[1,0]
	s_nop 0
	v_pk_fma_f32 v[116:117], v[116:117], v[114:115], v[134:135] op_sel:[1,1,0] op_sel_hi:[0,1,1] neg_hi:[1,0,0]
	v_pk_mul_f32 v[134:135], v[114:115], v[132:133] op_sel_hi:[1,0]
	s_nop 0
	v_pk_fma_f32 v[114:115], v[114:115], v[132:133], v[134:135] op_sel:[1,1,0] op_sel_hi:[0,1,1] neg_lo:[1,0,0]
	s_nop 0
	v_pk_mul_f32 v[134:135], v[112:113], v[114:115] op_sel_hi:[1,0]
	s_nop 0
	v_pk_fma_f32 v[112:113], v[112:113], v[114:115], v[134:135] op_sel:[1,1,0] op_sel_hi:[0,1,1] neg_hi:[1,0,0]
	v_pk_mul_f32 v[134:135], v[114:115], v[132:133] op_sel_hi:[1,0]
	s_nop 0
	v_pk_fma_f32 v[114:115], v[114:115], v[132:133], v[134:135] op_sel:[1,1,0] op_sel_hi:[0,1,1] neg_lo:[1,0,0]
	s_nop 0
	v_pk_mul_f32 v[134:135], v[108:109], v[114:115] op_sel_hi:[1,0]
	s_nop 0
	v_pk_fma_f32 v[108:109], v[108:109], v[114:115], v[134:135] op_sel:[1,1,0] op_sel_hi:[0,1,1] neg_hi:[1,0,0]
	v_pk_mul_f32 v[134:135], v[114:115], v[132:133] op_sel_hi:[1,0]
	s_nop 0
	v_pk_fma_f32 v[114:115], v[114:115], v[132:133], v[134:135] op_sel:[1,1,0] op_sel_hi:[0,1,1] neg_lo:[1,0,0]
	s_nop 0
	v_pk_mul_f32 v[134:135], v[102:103], v[114:115] op_sel_hi:[1,0]
	s_nop 0
	v_pk_fma_f32 v[102:103], v[102:103], v[114:115], v[134:135] op_sel:[1,1,0] op_sel_hi:[0,1,1] neg_hi:[1,0,0]
	v_pk_mul_f32 v[134:135], v[114:115], v[132:133] op_sel_hi:[1,0]
	s_nop 0
	v_pk_fma_f32 v[114:115], v[114:115], v[132:133], v[134:135] op_sel:[1,1,0] op_sel_hi:[0,1,1] neg_lo:[1,0,0]
	s_nop 0
	v_pk_mul_f32 v[134:135], v[110:111], v[114:115] op_sel_hi:[1,0]
	s_nop 0
	v_pk_fma_f32 v[110:111], v[110:111], v[114:115], v[134:135] op_sel:[1,1,0] op_sel_hi:[0,1,1] neg_hi:[1,0,0]
	v_pk_mul_f32 v[134:135], v[114:115], v[132:133] op_sel_hi:[1,0]
	s_nop 0
	v_pk_fma_f32 v[114:115], v[114:115], v[132:133], v[134:135] op_sel:[1,1,0] op_sel_hi:[0,1,1] neg_lo:[1,0,0]
	s_nop 0
	v_pk_mul_f32 v[132:133], v[2:3], v[114:115] op_sel_hi:[1,0]
	s_nop 0
	v_pk_fma_f32 v[2:3], v[2:3], v[114:115], v[132:133] op_sel:[1,1,0] op_sel_hi:[0,1,1] neg_hi:[1,0,0]
	v_add_u32_e32 v114, 0x1000, v38
	ds_write2st64_b64 v38, v[4:5], v[106:107] offset0:8 offset1:26
	ds_write2st64_b64 v38, v[122:123], v[118:119] offset0:44 offset1:62
	ds_write2st64_b64 v38, v[126:127], v[130:131] offset0:80 offset1:98
	ds_write_b64 v38, v[128:129] offset:59392
	ds_write_b64 v114, v[124:125] offset:64512
	v_add_u32_e32 v4, 0x13000, v38
	ds_write_b64 v4, v[104:105]
	v_add_u32_e32 v4, 0x15400, v38
	ds_write_b64 v4, v[120:121]
	v_add_u32_e32 v4, 0x17800, v38
	ds_write_b64 v4, v[116:117]
	v_add_u32_e32 v4, 0x19c00, v38
	ds_write_b64 v4, v[112:113]
	v_add_u32_e32 v4, 0x1c000, v38
	ds_write_b64 v4, v[108:109]
	v_add_u32_e32 v4, 0x1e400, v38
	ds_write_b64 v4, v[102:103]
	v_add_u32_e32 v4, 0x20800, v38
	ds_write_b64 v4, v[110:111]
	v_add_u32_e32 v4, 0x22c00, v38
	ds_write_b64 v4, v[2:3]
	v_mov_b32_e32 v4, v204
	s_waitcnt lgkmcnt(0)
	s_barrier
	s_cselect_b32 s99, 1, 0
	v_readfirstlane_b32 s98, v0
	s_cmp_lt_u32 s98, 0x100
	s_cbranch_scc1 .Lfft_stg_17796
	s_sleep 8
.Lfft_stg_17796:
	s_cmp_lg_u32 s99, 0
	s_nop 0
	v_and_b32_e32 v38, 63, v4
	v_cvt_f32_ubyte0_e32 v2, v38
	v_mul_f32_e32 v3, 0x3a800000, v2
	v_cos_f32_e32 v2, v3
	v_sin_f32_e32 v3, v3
	v_lshlrev_b32_e32 v132, 4, v4
.LBB0_756:
	v_add_u32_e32 v4, s86, v132
	v_and_b32_e32 v4, 0xfffffc00, v4
	v_or_b32_e32 v5, v4, v38
	v_bitop3_b32 v4, v4, s97, v38 bitop3:0xc8
	v_lshlrev_b32_e32 v5, 3, v5
	v_add3_u32 v133, 0, v4, v5
	v_add_u32_e32 v134, 0x800, v133
	v_add_u32_e32 v135, 0x1000, v133
	ds_read2_b64 v[102:105], v133 offset1:72
	ds_read2_b64 v[106:109], v133 offset0:144 offset1:216
	ds_read2_b64 v[110:113], v134 offset0:32 offset1:104
	ds_read2_b64 v[114:117], v134 offset0:176 offset1:248
	ds_read2_b64 v[118:121], v135 offset0:64 offset1:136
	v_add_u32_e32 v136, 0x1400, v133
	ds_read2_b64 v[122:125], v136 offset0:80 offset1:152
	v_add_u32_e32 v137, 0x1800, v133
	ds_read2_b64 v[126:129], v137 offset0:96 offset1:168
	v_add_u32_e32 v138, 0x1c00, v133
	ds_read2_b64 v[140:143], v138 offset0:112 offset1:184
	s_waitcnt lgkmcnt(3)
	v_pk_add_f32 v[4:5], v[102:103], v[118:119]
	v_pk_add_f32 v[102:103], v[102:103], v[118:119] neg_lo:[0,1] neg_hi:[0,1]
	v_pk_add_f32 v[118:119], v[104:105], v[120:121]
	v_pk_add_f32 v[104:105], v[104:105], v[120:121] neg_lo:[0,1] neg_hi:[0,1]
	v_mov_b64_e32 v[120:121], s[4:5]
	v_pk_mul_f32 v[130:131], v[104:105], v[120:121] op_sel_hi:[1,0]
	s_movk_i32 s86, 0x2000
	v_pk_fma_f32 v[104:105], v[104:105], v[120:121], v[130:131] op_sel:[1,1,0] op_sel_hi:[0,1,1] neg_hi:[1,0,0]
	s_waitcnt lgkmcnt(2)
	v_pk_add_f32 v[120:121], v[106:107], v[122:123]
	v_pk_add_f32 v[106:107], v[106:107], v[122:123] neg_lo:[0,1] neg_hi:[0,1]
	v_mov_b64_e32 v[122:123], s[6:7]
	v_pk_mul_f32 v[130:131], v[106:107], v[122:123] op_sel_hi:[1,0]
	s_and_b64 vcc, exec, s[84:85]
	v_pk_fma_f32 v[106:107], v[106:107], v[122:123], v[130:131] op_sel:[1,1,0] op_sel_hi:[0,1,1] neg_hi:[1,0,0]
	v_pk_add_f32 v[130:131], v[108:109], v[124:125]
	v_pk_add_f32 v[108:109], v[108:109], v[124:125] neg_lo:[0,1] neg_hi:[0,1]
	v_mov_b64_e32 v[124:125], s[10:11]
	v_pk_mul_f32 v[144:145], v[108:109], v[124:125] op_sel_hi:[1,0]
	s_mov_b64 s[84:85], 0
	v_pk_fma_f32 v[108:109], v[108:109], v[124:125], v[144:145] op_sel:[1,1,0] op_sel_hi:[0,1,1] neg_hi:[1,0,0]
	s_waitcnt lgkmcnt(1)
	v_pk_add_f32 v[124:125], v[110:111], v[126:127]
	v_pk_add_f32 v[110:111], v[110:111], v[126:127] op_sel:[1,1] op_sel_hi:[0,0] neg_lo:[0,1] neg_hi:[1,0]
	v_pk_add_f32 v[126:127], v[112:113], v[128:129]
	v_pk_add_f32 v[112:113], v[112:113], v[128:129] neg_lo:[0,1] neg_hi:[0,1]
	v_mov_b64_e32 v[128:129], s[12:13]
	v_pk_mul_f32 v[144:145], v[112:113], v[128:129] op_sel_hi:[1,0]
	s_nop 0
	v_pk_fma_f32 v[112:113], v[112:113], v[128:129], v[144:145] op_sel:[1,1,0] op_sel_hi:[0,1,1] neg_hi:[1,0,0]
	s_waitcnt lgkmcnt(0)
	v_pk_add_f32 v[128:129], v[114:115], v[140:141]
	v_pk_add_f32 v[114:115], v[114:115], v[140:141] neg_lo:[0,1] neg_hi:[0,1]
	v_mov_b64_e32 v[140:141], s[14:15]
	v_pk_mul_f32 v[144:145], v[114:115], v[140:141] op_sel_hi:[1,0]
	s_nop 0
	v_pk_fma_f32 v[114:115], v[114:115], v[140:141], v[144:145] op_sel:[1,1,0] op_sel_hi:[0,1,1] neg_hi:[1,0,0]
	v_pk_add_f32 v[144:145], v[116:117], v[142:143]
	v_pk_add_f32 v[116:117], v[116:117], v[142:143] neg_lo:[0,1] neg_hi:[0,1]
	v_mov_b64_e32 v[142:143], s[16:17]
	v_pk_mul_f32 v[146:147], v[116:117], v[142:143] op_sel_hi:[1,0]
	s_nop 0
	v_pk_fma_f32 v[116:117], v[116:117], v[142:143], v[146:147] op_sel:[1,1,0] op_sel_hi:[0,1,1] neg_hi:[1,0,0]
	v_pk_add_f32 v[142:143], v[4:5], v[124:125]
	v_pk_add_f32 v[4:5], v[4:5], v[124:125] neg_lo:[0,1] neg_hi:[0,1]
	v_pk_add_f32 v[124:125], v[118:119], v[126:127]
	v_pk_add_f32 v[118:119], v[118:119], v[126:127] neg_lo:[0,1] neg_hi:[0,1]
	s_nop 0
	v_pk_mul_f32 v[126:127], v[118:119], v[122:123] op_sel_hi:[1,0]
	s_nop 0
	v_pk_fma_f32 v[118:119], v[118:119], v[122:123], v[126:127] op_sel:[1,1,0] op_sel_hi:[0,1,1] neg_hi:[1,0,0]
	v_pk_add_f32 v[126:127], v[120:121], v[128:129]
	v_pk_add_f32 v[120:121], v[120:121], v[128:129] op_sel:[1,1] op_sel_hi:[0,0] neg_lo:[0,1] neg_hi:[1,0]
	v_pk_add_f32 v[128:129], v[130:131], v[144:145]
	v_pk_add_f32 v[130:131], v[130:131], v[144:145] neg_lo:[0,1] neg_hi:[0,1]
	s_nop 0
	v_pk_mul_f32 v[144:145], v[130:131], v[140:141] op_sel_hi:[1,0]
	s_nop 0
	v_pk_fma_f32 v[130:131], v[130:131], v[140:141], v[144:145] op_sel:[1,1,0] op_sel_hi:[0,1,1] neg_hi:[1,0,0]
	v_pk_add_f32 v[144:145], v[102:103], v[110:111]
	v_pk_add_f32 v[102:103], v[102:103], v[110:111] neg_lo:[0,1] neg_hi:[0,1]
	v_pk_add_f32 v[110:111], v[104:105], v[112:113]
	v_pk_add_f32 v[104:105], v[104:105], v[112:113] neg_lo:[0,1] neg_hi:[0,1]
	s_nop 0
	v_pk_mul_f32 v[112:113], v[104:105], v[122:123] op_sel_hi:[1,0]
	s_nop 0
	v_pk_fma_f32 v[104:105], v[104:105], v[122:123], v[112:113] op_sel:[1,1,0] op_sel_hi:[0,1,1] neg_hi:[1,0,0]
	v_pk_add_f32 v[112:113], v[106:107], v[114:115]
	v_pk_add_f32 v[106:107], v[106:107], v[114:115] op_sel:[1,1] op_sel_hi:[0,0] neg_lo:[0,1] neg_hi:[1,0]
	v_pk_add_f32 v[114:115], v[108:109], v[116:117]
	v_pk_add_f32 v[108:109], v[108:109], v[116:117] neg_lo:[0,1] neg_hi:[0,1]
	v_pk_add_f32 v[122:123], v[124:125], v[128:129]
	v_pk_mul_f32 v[116:117], v[108:109], v[140:141] op_sel_hi:[1,0]
	v_pk_add_f32 v[124:125], v[124:125], v[128:129] op_sel:[1,1] op_sel_hi:[0,0] neg_lo:[0,1] neg_hi:[1,0]
	v_pk_add_f32 v[146:147], v[110:111], v[114:115]
	v_pk_fma_f32 v[108:109], v[108:109], v[140:141], v[116:117] op_sel:[1,1,0] op_sel_hi:[0,1,1] neg_hi:[1,0,0]
	v_pk_add_f32 v[116:117], v[142:143], v[126:127]
	v_pk_add_f32 v[126:127], v[142:143], v[126:127] neg_lo:[0,1] neg_hi:[0,1]
	v_pk_add_f32 v[140:141], v[4:5], v[120:121]
	v_pk_add_f32 v[142:143], v[4:5], v[120:121] neg_lo:[0,1] neg_hi:[0,1]
	v_pk_add_f32 v[120:121], v[118:119], v[130:131]
	v_pk_add_f32 v[118:119], v[118:119], v[130:131] op_sel:[1,1] op_sel_hi:[0,0] neg_lo:[0,1] neg_hi:[1,0]
	v_pk_add_f32 v[130:131], v[144:145], v[112:113]
	v_pk_add_f32 v[148:149], v[102:103], v[106:107]
	v_pk_add_f32 v[106:107], v[102:103], v[106:107] neg_lo:[0,1] neg_hi:[0,1]
	v_pk_add_f32 v[150:151], v[104:105], v[108:109]
	v_pk_add_f32 v[108:109], v[104:105], v[108:109] op_sel:[1,1] op_sel_hi:[0,0] neg_lo:[0,1] neg_hi:[1,0]
	v_pk_add_f32 v[144:145], v[144:145], v[112:113] neg_lo:[0,1] neg_hi:[0,1]
	v_pk_add_f32 v[110:111], v[110:111], v[114:115] op_sel:[1,1] op_sel_hi:[0,0] neg_lo:[0,1] neg_hi:[1,0]
	v_pk_add_f32 v[4:5], v[116:117], v[122:123]
	v_pk_add_f32 v[114:115], v[116:117], v[122:123] neg_lo:[0,1] neg_hi:[0,1]
	v_pk_add_f32 v[122:123], v[126:127], v[124:125]
	v_pk_add_f32 v[104:105], v[126:127], v[124:125] neg_lo:[0,1] neg_hi:[0,1]
	v_pk_add_f32 v[128:129], v[140:141], v[120:121]
	v_pk_add_f32 v[112:113], v[140:141], v[120:121] neg_lo:[0,1] neg_hi:[0,1]
	v_pk_add_f32 v[140:141], v[130:131], v[146:147]
	v_pk_add_f32 v[124:125], v[106:107], v[108:109]
	v_pk_add_f32 v[106:107], v[106:107], v[108:109] neg_lo:[0,1] neg_hi:[0,1]
	v_pk_mul_f32 v[108:109], v[140:141], v[2:3] op_sel_hi:[1,0]
	v_pk_add_f32 v[120:121], v[142:143], v[118:119]
	v_pk_fma_f32 v[108:109], v[140:141], v[2:3], v[108:109] op_sel:[1,1,0] op_sel_hi:[0,1,1] neg_hi:[1,0,0]
	v_pk_mul_f32 v[140:141], v[2:3], v[2:3] op_sel_hi:[1,0]
	v_pk_add_f32 v[102:103], v[142:143], v[118:119] neg_lo:[0,1] neg_hi:[0,1]
	v_pk_fma_f32 v[140:141], v[2:3], v[2:3], v[140:141] op_sel:[1,1,0] op_sel_hi:[0,1,1] neg_lo:[1,0,0]
	v_pk_add_f32 v[118:119], v[130:131], v[146:147] neg_lo:[0,1] neg_hi:[0,1]
	v_pk_mul_f32 v[142:143], v[128:129], v[140:141] op_sel_hi:[1,0]
	v_pk_add_f32 v[130:131], v[148:149], v[150:151]
	v_pk_fma_f32 v[128:129], v[128:129], v[140:141], v[142:143] op_sel:[1,1,0] op_sel_hi:[0,1,1] neg_hi:[1,0,0]
	v_pk_mul_f32 v[142:143], v[140:141], v[2:3] op_sel_hi:[1,0]
	v_pk_add_f32 v[126:127], v[144:145], v[110:111]
	v_pk_fma_f32 v[140:141], v[140:141], v[2:3], v[142:143] op_sel:[1,1,0] op_sel_hi:[0,1,1] neg_lo:[1,0,0]
	v_pk_add_f32 v[116:117], v[148:149], v[150:151] neg_lo:[0,1] neg_hi:[0,1]
	v_pk_mul_f32 v[142:143], v[130:131], v[140:141] op_sel_hi:[1,0]
	v_pk_add_f32 v[110:111], v[144:145], v[110:111] neg_lo:[0,1] neg_hi:[0,1]
	v_pk_fma_f32 v[130:131], v[130:131], v[140:141], v[142:143] op_sel:[1,1,0] op_sel_hi:[0,1,1] neg_hi:[1,0,0]
	v_pk_mul_f32 v[142:143], v[140:141], v[2:3] op_sel_hi:[1,0]
	s_nop 0
	v_pk_fma_f32 v[140:141], v[140:141], v[2:3], v[142:143] op_sel:[1,1,0] op_sel_hi:[0,1,1] neg_lo:[1,0,0]
	s_nop 0
	v_pk_mul_f32 v[142:143], v[122:123], v[140:141] op_sel_hi:[1,0]
	s_nop 0
	v_pk_fma_f32 v[122:123], v[122:123], v[140:141], v[142:143] op_sel:[1,1,0] op_sel_hi:[0,1,1] neg_hi:[1,0,0]
	v_pk_mul_f32 v[142:143], v[140:141], v[2:3] op_sel_hi:[1,0]
	s_nop 0
	v_pk_fma_f32 v[140:141], v[140:141], v[2:3], v[142:143] op_sel:[1,1,0] op_sel_hi:[0,1,1] neg_lo:[1,0,0]
	s_nop 0
	v_pk_mul_f32 v[142:143], v[126:127], v[140:141] op_sel_hi:[1,0]
	s_nop 0
	v_pk_fma_f32 v[126:127], v[126:127], v[140:141], v[142:143] op_sel:[1,1,0] op_sel_hi:[0,1,1] neg_hi:[1,0,0]
	v_pk_mul_f32 v[142:143], v[140:141], v[2:3] op_sel_hi:[1,0]
	s_nop 0
	v_pk_fma_f32 v[140:141], v[140:141], v[2:3], v[142:143] op_sel:[1,1,0] op_sel_hi:[0,1,1] neg_lo:[1,0,0]
	s_nop 0
	v_pk_mul_f32 v[142:143], v[120:121], v[140:141] op_sel_hi:[1,0]
	s_nop 0
	v_pk_fma_f32 v[120:121], v[120:121], v[140:141], v[142:143] op_sel:[1,1,0] op_sel_hi:[0,1,1] neg_hi:[1,0,0]
	v_pk_mul_f32 v[142:143], v[140:141], v[2:3] op_sel_hi:[1,0]
	s_nop 0
	v_pk_fma_f32 v[140:141], v[140:141], v[2:3], v[142:143] op_sel:[1,1,0] op_sel_hi:[0,1,1] neg_lo:[1,0,0]
	s_nop 0
	v_pk_mul_f32 v[142:143], v[124:125], v[140:141] op_sel_hi:[1,0]
	s_nop 0
	v_pk_fma_f32 v[124:125], v[124:125], v[140:141], v[142:143] op_sel:[1,1,0] op_sel_hi:[0,1,1] neg_hi:[1,0,0]
	v_pk_mul_f32 v[142:143], v[140:141], v[2:3] op_sel_hi:[1,0]
	s_nop 0
	v_pk_fma_f32 v[140:141], v[140:141], v[2:3], v[142:143] op_sel:[1,1,0] op_sel_hi:[0,1,1] neg_lo:[1,0,0]
	s_nop 0
	v_pk_mul_f32 v[142:143], v[114:115], v[140:141] op_sel_hi:[1,0]
	s_nop 0
	v_pk_fma_f32 v[114:115], v[114:115], v[140:141], v[142:143] op_sel:[1,1,0] op_sel_hi:[0,1,1] neg_hi:[1,0,0]
	v_pk_mul_f32 v[142:143], v[140:141], v[2:3] op_sel_hi:[1,0]
	s_nop 0
	v_pk_fma_f32 v[140:141], v[140:141], v[2:3], v[142:143] op_sel:[1,1,0] op_sel_hi:[0,1,1] neg_lo:[1,0,0]
	s_nop 0
	v_pk_mul_f32 v[142:143], v[118:119], v[140:141] op_sel_hi:[1,0]
	s_nop 0
	v_pk_fma_f32 v[118:119], v[118:119], v[140:141], v[142:143] op_sel:[1,1,0] op_sel_hi:[0,1,1] neg_hi:[1,0,0]
	v_pk_mul_f32 v[142:143], v[140:141], v[2:3] op_sel_hi:[1,0]
	s_nop 0
	v_pk_fma_f32 v[140:141], v[140:141], v[2:3], v[142:143] op_sel:[1,1,0] op_sel_hi:[0,1,1] neg_lo:[1,0,0]
	s_nop 0
	v_pk_mul_f32 v[142:143], v[112:113], v[140:141] op_sel_hi:[1,0]
	s_nop 0
	v_pk_fma_f32 v[112:113], v[112:113], v[140:141], v[142:143] op_sel:[1,1,0] op_sel_hi:[0,1,1] neg_hi:[1,0,0]
	v_pk_mul_f32 v[142:143], v[140:141], v[2:3] op_sel_hi:[1,0]
	s_nop 0
	v_pk_fma_f32 v[140:141], v[140:141], v[2:3], v[142:143] op_sel:[1,1,0] op_sel_hi:[0,1,1] neg_lo:[1,0,0]
	s_nop 0
	v_pk_mul_f32 v[142:143], v[116:117], v[140:141] op_sel_hi:[1,0]
	s_nop 0
	v_pk_fma_f32 v[116:117], v[116:117], v[140:141], v[142:143] op_sel:[1,1,0] op_sel_hi:[0,1,1] neg_hi:[1,0,0]
	v_pk_mul_f32 v[142:143], v[140:141], v[2:3] op_sel_hi:[1,0]
	s_nop 0
	v_pk_fma_f32 v[140:141], v[140:141], v[2:3], v[142:143] op_sel:[1,1,0] op_sel_hi:[0,1,1] neg_lo:[1,0,0]
	s_nop 0
	v_pk_mul_f32 v[142:143], v[104:105], v[140:141] op_sel_hi:[1,0]
	s_nop 0
	v_pk_fma_f32 v[104:105], v[104:105], v[140:141], v[142:143] op_sel:[1,1,0] op_sel_hi:[0,1,1] neg_hi:[1,0,0]
	v_pk_mul_f32 v[142:143], v[140:141], v[2:3] op_sel_hi:[1,0]
	s_nop 0
	v_pk_fma_f32 v[140:141], v[140:141], v[2:3], v[142:143] op_sel:[1,1,0] op_sel_hi:[0,1,1] neg_lo:[1,0,0]
	s_nop 0
	v_pk_mul_f32 v[142:143], v[110:111], v[140:141] op_sel_hi:[1,0]
	s_nop 0
	v_pk_fma_f32 v[110:111], v[110:111], v[140:141], v[142:143] op_sel:[1,1,0] op_sel_hi:[0,1,1] neg_hi:[1,0,0]
	v_pk_mul_f32 v[142:143], v[140:141], v[2:3] op_sel_hi:[1,0]
	s_nop 0
	v_pk_fma_f32 v[140:141], v[140:141], v[2:3], v[142:143] op_sel:[1,1,0] op_sel_hi:[0,1,1] neg_lo:[1,0,0]
	s_nop 0
	v_pk_mul_f32 v[142:143], v[102:103], v[140:141] op_sel_hi:[1,0]
	s_nop 0
	v_pk_fma_f32 v[102:103], v[102:103], v[140:141], v[142:143] op_sel:[1,1,0] op_sel_hi:[0,1,1] neg_hi:[1,0,0]
	v_pk_mul_f32 v[142:143], v[140:141], v[2:3] op_sel_hi:[1,0]
	s_nop 0
	v_pk_fma_f32 v[140:141], v[140:141], v[2:3], v[142:143] op_sel:[1,1,0] op_sel_hi:[0,1,1] neg_lo:[1,0,0]
	s_nop 0
	v_pk_mul_f32 v[142:143], v[106:107], v[140:141] op_sel_hi:[1,0]
	s_nop 0
	v_pk_fma_f32 v[106:107], v[106:107], v[140:141], v[142:143] op_sel:[1,1,0] op_sel_hi:[0,1,1] neg_hi:[1,0,0]
	ds_write2_b64 v133, v[4:5], v[108:109] offset1:72
	ds_write2_b64 v133, v[128:129], v[130:131] offset0:144 offset1:216
	ds_write2_b64 v134, v[122:123], v[126:127] offset0:32 offset1:104
	ds_write2_b64 v134, v[120:121], v[124:125] offset0:176 offset1:248
	ds_write2_b64 v135, v[114:115], v[118:119] offset0:64 offset1:136
	ds_write2_b64 v136, v[112:113], v[116:117] offset0:80 offset1:152
	ds_write2_b64 v137, v[104:105], v[110:111] offset0:96 offset1:168
	ds_write2_b64 v138, v[102:103], v[106:107] offset0:112 offset1:184
	s_cbranch_vccnz .LBB0_756
	v_mov_b32_e32 v4, v204
	s_waitcnt lgkmcnt(0)
	s_barrier
	s_cselect_b32 s99, 1, 0
	v_readfirstlane_b32 s98, v0
	s_cmp_lt_u32 s98, 0x100
	s_cbranch_scc1 .Lfft_stg_18212
	s_sleep 8
.Lfft_stg_18212:
	s_cmp_lg_u32 s99, 0
	s_mov_b32 s84, 0
	v_and_b32_e32 v5, 7, v4
	v_cvt_f32_ubyte0_e32 v2, v5
	v_mul_f32_e32 v3, 0x3c800000, v2
	v_cos_f32_e32 v2, v3
	v_sin_f32_e32 v3, v3
	v_lshlrev_b32_e32 v4, 3, v4
	v_lshl_add_u32 v5, v5, 3, 0
.LBB0_758:
	v_add_u32_e32 v38, s84, v4
	v_and_b32_e32 v38, 0xffffffc0, v38
	v_lshlrev_b32_e32 v102, 3, v38
	v_add3_u32 v38, v5, v38, v102
	ds_read2_b64 v[102:105], v38 offset1:9
	ds_read2_b64 v[106:109], v38 offset0:18 offset1:27
	ds_read2_b64 v[110:113], v38 offset0:36 offset1:45
	ds_read2_b64 v[114:117], v38 offset0:54 offset1:63
	s_addk_i32 s84, 0x1000
	s_cmpk_lg_i32 s84, 0x4000
	s_waitcnt lgkmcnt(1)
	v_pk_add_f32 v[118:119], v[102:103], v[110:111]
	v_pk_add_f32 v[102:103], v[102:103], v[110:111] neg_lo:[0,1] neg_hi:[0,1]
	v_pk_add_f32 v[110:111], v[104:105], v[112:113]
	v_pk_add_f32 v[104:105], v[104:105], v[112:113] neg_lo:[0,1] neg_hi:[0,1]
	v_mov_b64_e32 v[112:113], s[6:7]
	v_pk_mul_f32 v[120:121], v[104:105], v[112:113] op_sel_hi:[1,0]
	s_nop 0
	v_pk_fma_f32 v[104:105], v[104:105], v[112:113], v[120:121] op_sel:[1,1,0] op_sel_hi:[0,1,1] neg_hi:[1,0,0]
	s_waitcnt lgkmcnt(0)
	v_pk_add_f32 v[112:113], v[106:107], v[114:115]
	v_pk_add_f32 v[106:107], v[106:107], v[114:115] op_sel:[1,1] op_sel_hi:[0,0] neg_lo:[0,1] neg_hi:[1,0]
	v_pk_add_f32 v[114:115], v[108:109], v[116:117]
	v_pk_add_f32 v[108:109], v[108:109], v[116:117] neg_lo:[0,1] neg_hi:[0,1]
	v_mov_b64_e32 v[116:117], s[14:15]
	v_pk_mul_f32 v[120:121], v[108:109], v[116:117] op_sel_hi:[1,0]
	s_nop 0
	v_pk_fma_f32 v[108:109], v[108:109], v[116:117], v[120:121] op_sel:[1,1,0] op_sel_hi:[0,1,1] neg_hi:[1,0,0]
	v_pk_add_f32 v[116:117], v[118:119], v[112:113]
	v_pk_add_f32 v[112:113], v[118:119], v[112:113] neg_lo:[0,1] neg_hi:[0,1]
	v_pk_add_f32 v[118:119], v[110:111], v[114:115]
	v_pk_add_f32 v[110:111], v[110:111], v[114:115] op_sel:[1,1] op_sel_hi:[0,0] neg_lo:[0,1] neg_hi:[1,0]
	v_pk_add_f32 v[114:115], v[102:103], v[106:107]
	v_pk_add_f32 v[102:103], v[102:103], v[106:107] neg_lo:[0,1] neg_hi:[0,1]
	v_pk_add_f32 v[106:107], v[104:105], v[108:109]
	v_pk_add_f32 v[104:105], v[104:105], v[108:109] op_sel:[1,1] op_sel_hi:[0,0] neg_lo:[0,1] neg_hi:[1,0]
	v_pk_add_f32 v[108:109], v[116:117], v[118:119]
	v_pk_add_f32 v[116:117], v[116:117], v[118:119] neg_lo:[0,1] neg_hi:[0,1]
	v_pk_add_f32 v[118:119], v[112:113], v[110:111]
	v_pk_add_f32 v[110:111], v[112:113], v[110:111] neg_lo:[0,1] neg_hi:[0,1]
	v_pk_add_f32 v[112:113], v[114:115], v[106:107]
	v_pk_add_f32 v[106:107], v[114:115], v[106:107] neg_lo:[0,1] neg_hi:[0,1]
	v_pk_add_f32 v[114:115], v[102:103], v[104:105]
	v_pk_add_f32 v[102:103], v[102:103], v[104:105] neg_lo:[0,1] neg_hi:[0,1]
	v_pk_mul_f32 v[104:105], v[112:113], v[2:3] op_sel_hi:[1,0]
	s_nop 0
	v_pk_fma_f32 v[104:105], v[112:113], v[2:3], v[104:105] op_sel:[1,1,0] op_sel_hi:[0,1,1] neg_hi:[1,0,0]
	v_pk_mul_f32 v[112:113], v[2:3], v[2:3] op_sel_hi:[1,0]
	s_nop 0
	v_pk_fma_f32 v[112:113], v[2:3], v[2:3], v[112:113] op_sel:[1,1,0] op_sel_hi:[0,1,1] neg_lo:[1,0,0]
	s_nop 0
	v_pk_mul_f32 v[120:121], v[118:119], v[112:113] op_sel_hi:[1,0]
	s_nop 0
	v_pk_fma_f32 v[118:119], v[118:119], v[112:113], v[120:121] op_sel:[1,1,0] op_sel_hi:[0,1,1] neg_hi:[1,0,0]
	v_pk_mul_f32 v[120:121], v[112:113], v[2:3] op_sel_hi:[1,0]
	s_nop 0
	v_pk_fma_f32 v[112:113], v[112:113], v[2:3], v[120:121] op_sel:[1,1,0] op_sel_hi:[0,1,1] neg_lo:[1,0,0]
	s_nop 0
	v_pk_mul_f32 v[120:121], v[114:115], v[112:113] op_sel_hi:[1,0]
	s_nop 0
	v_pk_fma_f32 v[114:115], v[114:115], v[112:113], v[120:121] op_sel:[1,1,0] op_sel_hi:[0,1,1] neg_hi:[1,0,0]
	v_pk_mul_f32 v[120:121], v[112:113], v[2:3] op_sel_hi:[1,0]
	s_nop 0
	v_pk_fma_f32 v[112:113], v[112:113], v[2:3], v[120:121] op_sel:[1,1,0] op_sel_hi:[0,1,1] neg_lo:[1,0,0]
	s_nop 0
	v_pk_mul_f32 v[120:121], v[116:117], v[112:113] op_sel_hi:[1,0]
	s_nop 0
	v_pk_fma_f32 v[116:117], v[116:117], v[112:113], v[120:121] op_sel:[1,1,0] op_sel_hi:[0,1,1] neg_hi:[1,0,0]
	v_pk_mul_f32 v[120:121], v[112:113], v[2:3] op_sel_hi:[1,0]
	s_nop 0
	v_pk_fma_f32 v[112:113], v[112:113], v[2:3], v[120:121] op_sel:[1,1,0] op_sel_hi:[0,1,1] neg_lo:[1,0,0]
	s_nop 0
	v_pk_mul_f32 v[120:121], v[106:107], v[112:113] op_sel_hi:[1,0]
	s_nop 0
	v_pk_fma_f32 v[106:107], v[106:107], v[112:113], v[120:121] op_sel:[1,1,0] op_sel_hi:[0,1,1] neg_hi:[1,0,0]
	v_pk_mul_f32 v[120:121], v[112:113], v[2:3] op_sel_hi:[1,0]
	s_nop 0
	v_pk_fma_f32 v[112:113], v[112:113], v[2:3], v[120:121] op_sel:[1,1,0] op_sel_hi:[0,1,1] neg_lo:[1,0,0]
	s_nop 0
	v_pk_mul_f32 v[120:121], v[110:111], v[112:113] op_sel_hi:[1,0]
	s_nop 0
	v_pk_fma_f32 v[110:111], v[110:111], v[112:113], v[120:121] op_sel:[1,1,0] op_sel_hi:[0,1,1] neg_hi:[1,0,0]
	v_pk_mul_f32 v[120:121], v[112:113], v[2:3] op_sel_hi:[1,0]
	s_nop 0
	v_pk_fma_f32 v[112:113], v[112:113], v[2:3], v[120:121] op_sel:[1,1,0] op_sel_hi:[0,1,1] neg_lo:[1,0,0]
	s_nop 0
	v_pk_mul_f32 v[120:121], v[102:103], v[112:113] op_sel_hi:[1,0]
	s_nop 0
	v_pk_fma_f32 v[102:103], v[102:103], v[112:113], v[120:121] op_sel:[1,1,0] op_sel_hi:[0,1,1] neg_hi:[1,0,0]
	ds_write2_b64 v38, v[108:109], v[104:105] offset1:9
	ds_write2_b64 v38, v[118:119], v[114:115] offset0:18 offset1:27
	ds_write2_b64 v38, v[116:117], v[106:107] offset0:36 offset1:45
	ds_write2_b64 v38, v[110:111], v[102:103] offset0:54 offset1:63
	s_cbranch_scc1 .LBB0_758
	v_mov_b32_e32 v2, v204
	s_waitcnt lgkmcnt(0)
	s_barrier
	s_cselect_b32 s99, 1, 0
	v_readfirstlane_b32 s98, v0
	s_cmp_lt_u32 s98, 0x100
	s_cbranch_scc1 .Lfft_stg_18391
	s_sleep 8
.Lfft_stg_18391:
	s_cmp_lg_u32 s99, 0
	s_mov_b32 s84, 0
	v_mul_lo_u32 v2, v2, s33
	v_add_u32_e32 v2, 0, v2

.LBB0_763:
	s_or_b64 exec, exec, s[84:85]
	v_mov_b64_e32 v[166:167], s[4:5]
	s_waitcnt vmcnt(29)
	v_pk_mul_f32 v[162:163], v[74:75], v[166:167] op_sel_hi:[1,0]
	v_mov_b64_e32 v[168:169], s[10:11]
	v_pk_fma_f32 v[180:181], v[74:75], v[166:167], v[162:163] op_sel:[1,1,0] op_sel_hi:[0,1,1] neg_hi:[1,0,0]
	v_mov_b64_e32 v[162:163], s[6:7]
	s_waitcnt vmcnt(27)
	v_pk_mul_f32 v[164:165], v[78:79], v[162:163] op_sel_hi:[1,0]
	v_mov_b32_e32 v38, v204
	v_pk_fma_f32 v[184:185], v[78:79], v[162:163], v[164:165] op_sel:[1,1,0] op_sel_hi:[0,1,1] neg_hi:[1,0,0]
	s_waitcnt vmcnt(25)
	v_pk_mul_f32 v[164:165], v[82:83], v[168:169] op_sel_hi:[1,0]
	v_mov_b64_e32 v[170:171], s[12:13]
	v_pk_fma_f32 v[188:189], v[82:83], v[168:169], v[164:165] op_sel:[1,1,0] op_sel_hi:[0,1,1] neg_hi:[1,0,0]
	s_waitcnt vmcnt(2)
	v_pk_mul_f32 v[164:165], v[90:91], v[170:171] op_sel_hi:[1,0]
	s_waitcnt lgkmcnt(0)
	s_barrier
	s_cselect_b32 s99, 1, 0
	v_readfirstlane_b32 s98, v0
	s_cmp_lt_u32 s98, 0x100
	s_cbranch_scc1 .Lfft_stg_18926
	s_sleep 8
.Lfft_stg_18926:
	s_cmp_lg_u32 s99, 0
	v_pk_add_f32 v[176:177], v[70:71], 0 op_sel_hi:[1,0]
	v_pk_add_f32 v[178:179], v[74:75], 0 op_sel_hi:[1,0]
	v_pk_add_f32 v[190:191], v[86:87], 0 op_sel_hi:[1,0]
	v_pk_add_f32 v[194:195], v[90:91], 0 op_sel_hi:[1,0]
	v_pk_fma_f32 v[210:211], v[90:91], v[170:171], v[164:165] op_sel:[1,1,0] op_sel_hi:[0,1,1] neg_hi:[1,0,0]
	v_mov_b64_e32 v[164:165], s[14:15]
	s_waitcnt vmcnt(0)
	v_pk_mul_f32 v[174:175], v[94:95], v[164:165] op_sel_hi:[1,0]
	v_cvt_f32_i32_e32 v224, v38
	v_pk_add_f32 v[182:183], v[78:79], 0 op_sel_hi:[1,0]
	v_pk_add_f32 v[186:187], v[82:83], 0 op_sel_hi:[1,0]
	v_pk_add_f32 v[212:213], v[94:95], 0 op_sel_hi:[1,0]
	v_pk_fma_f32 v[214:215], v[94:95], v[164:165], v[174:175] op_sel:[1,1,0] op_sel_hi:[0,1,1] neg_hi:[1,0,0]
	v_pk_add_f32 v[216:217], v[98:99], 0 op_sel_hi:[1,0]
	v_mov_b64_e32 v[174:175], s[16:17]
	v_pk_mul_f32 v[218:219], v[98:99], v[174:175] op_sel_hi:[1,0]
	v_pk_add_f32 v[220:221], v[190:191], v[176:177]
	v_pk_add_f32 v[176:177], v[176:177], v[190:191] neg_lo:[0,1] neg_hi:[0,1]
	v_pk_add_f32 v[190:191], v[194:195], v[178:179]
	v_pk_add_f32 v[178:179], v[178:179], v[194:195] neg_lo:[0,1] neg_hi:[0,1]
	v_mov_b64_e32 v[172:173], s[18:19]
	v_pk_mul_f32 v[194:195], v[178:179], v[162:163] op_sel_hi:[1,0]
	v_pk_add_f32 v[192:193], v[86:87], v[172:173] op_sel:[1,1] op_sel_hi:[0,0] neg_lo:[0,1] neg_hi:[1,0]
	v_pk_fma_f32 v[218:219], v[98:99], v[174:175], v[218:219] op_sel:[1,1,0] op_sel_hi:[0,1,1] neg_hi:[1,0,0]
	v_pk_add_f32 v[222:223], v[180:181], v[210:211]
	v_pk_fma_f32 v[178:179], v[178:179], v[162:163], v[194:195] op_sel:[1,1,0] op_sel_hi:[0,1,1] neg_hi:[1,0,0]
	v_pk_add_f32 v[194:195], v[212:213], v[182:183]
	v_pk_add_f32 v[182:183], v[182:183], v[212:213] op_sel:[1,1] op_sel_hi:[0,0] neg_lo:[0,1] neg_hi:[1,0]
	v_pk_add_f32 v[212:213], v[216:217], v[186:187]
	v_pk_add_f32 v[186:187], v[186:187], v[216:217] neg_lo:[0,1] neg_hi:[0,1]
	v_pk_add_f32 v[180:181], v[180:181], v[210:211] neg_lo:[0,1] neg_hi:[0,1]
	v_pk_mul_f32 v[216:217], v[186:187], v[164:165] op_sel_hi:[1,0]
	v_mul_f32_e32 v225, 0x38800000, v224
	v_pk_mul_f32 v[210:211], v[180:181], v[162:163] op_sel_hi:[1,0]
	v_pk_fma_f32 v[186:187], v[186:187], v[164:165], v[216:217] op_sel:[1,1,0] op_sel_hi:[0,1,1] neg_hi:[1,0,0]
	v_pk_add_f32 v[216:217], v[70:71], v[192:193]
	v_pk_add_f32 v[192:193], v[70:71], v[192:193] neg_lo:[0,1] neg_hi:[0,1]
	v_pk_fma_f32 v[180:181], v[180:181], v[162:163], v[210:211] op_sel:[1,1,0] op_sel_hi:[0,1,1] neg_hi:[1,0,0]
	v_pk_add_f32 v[210:211], v[184:185], v[214:215]
	v_pk_add_f32 v[184:185], v[184:185], v[214:215] op_sel:[1,1] op_sel_hi:[0,0] neg_lo:[0,1] neg_hi:[1,0]
	v_pk_add_f32 v[214:215], v[188:189], v[218:219]
	v_pk_add_f32 v[188:189], v[188:189], v[218:219] neg_lo:[0,1] neg_hi:[0,1]
	v_cos_f32_e32 v224, v225
	v_pk_mul_f32 v[218:219], v[188:189], v[164:165] op_sel_hi:[1,0]
	v_sin_f32_e32 v225, v225
	v_pk_fma_f32 v[188:189], v[188:189], v[164:165], v[218:219] op_sel:[1,1,0] op_sel_hi:[0,1,1] neg_hi:[1,0,0]
	v_pk_add_f32 v[218:219], v[194:195], v[220:221]
	v_pk_add_f32 v[194:195], v[220:221], v[194:195] neg_lo:[0,1] neg_hi:[0,1]
	v_pk_add_f32 v[220:221], v[212:213], v[190:191]
	v_pk_add_f32 v[190:191], v[190:191], v[212:213] op_sel:[1,1] op_sel_hi:[0,0] neg_lo:[0,1] neg_hi:[1,0]
	v_pk_add_f32 v[212:213], v[176:177], v[182:183]
	v_pk_add_f32 v[176:177], v[176:177], v[182:183] neg_lo:[0,1] neg_hi:[0,1]
	v_pk_add_f32 v[182:183], v[178:179], v[186:187]
	v_pk_add_f32 v[178:179], v[178:179], v[186:187] op_sel:[1,1] op_sel_hi:[0,0] neg_lo:[0,1] neg_hi:[1,0]
	v_pk_add_f32 v[186:187], v[216:217], v[210:211]
	v_pk_add_f32 v[210:211], v[216:217], v[210:211] neg_lo:[0,1] neg_hi:[0,1]
	v_pk_add_f32 v[216:217], v[222:223], v[214:215]
	v_pk_add_f32 v[214:215], v[222:223], v[214:215] op_sel:[1,1] op_sel_hi:[0,0] neg_lo:[0,1] neg_hi:[1,0]
	v_pk_add_f32 v[222:223], v[192:193], v[184:185]
	v_pk_add_f32 v[184:185], v[192:193], v[184:185] neg_lo:[0,1] neg_hi:[0,1]
	v_pk_add_f32 v[192:193], v[180:181], v[188:189]
	v_pk_add_f32 v[180:181], v[180:181], v[188:189] op_sel:[1,1] op_sel_hi:[0,0] neg_lo:[0,1] neg_hi:[1,0]
	v_pk_add_f32 v[188:189], v[220:221], v[218:219]
	v_pk_add_f32 v[218:219], v[218:219], v[220:221] neg_lo:[0,1] neg_hi:[0,1]
	v_pk_add_f32 v[220:221], v[194:195], v[190:191]
	v_pk_add_f32 v[190:191], v[194:195], v[190:191] neg_lo:[0,1] neg_hi:[0,1]
	v_pk_add_f32 v[194:195], v[212:213], v[182:183]
	v_pk_add_f32 v[182:183], v[212:213], v[182:183] neg_lo:[0,1] neg_hi:[0,1]
	v_pk_add_f32 v[212:213], v[176:177], v[178:179]
	v_pk_add_f32 v[176:177], v[176:177], v[178:179] neg_lo:[0,1] neg_hi:[0,1]
	v_pk_add_f32 v[178:179], v[186:187], v[216:217]
	v_pk_add_f32 v[186:187], v[186:187], v[216:217] neg_lo:[0,1] neg_hi:[0,1]
	v_pk_add_f32 v[216:217], v[210:211], v[214:215]
	v_pk_add_f32 v[210:211], v[210:211], v[214:215] neg_lo:[0,1] neg_hi:[0,1]
	v_pk_add_f32 v[214:215], v[222:223], v[192:193]
	v_pk_add_f32 v[192:193], v[222:223], v[192:193] neg_lo:[0,1] neg_hi:[0,1]
	v_pk_add_f32 v[222:223], v[184:185], v[180:181]
	v_pk_add_f32 v[180:181], v[184:185], v[180:181] neg_lo:[0,1] neg_hi:[0,1]
	v_pk_mul_f32 v[184:185], v[178:179], v[224:225] op_sel_hi:[1,0]
	v_and_b32_e32 v228, -8, v38
	v_pk_fma_f32 v[178:179], v[178:179], v[224:225], v[184:185] op_sel:[1,1,0] op_sel_hi:[0,1,1] neg_hi:[1,0,0]
	v_pk_mul_f32 v[184:185], v[224:225], v[224:225] op_sel_hi:[1,0]
	v_pk_add_f32 v[172:173], v[88:89], v[172:173] op_sel:[1,1] op_sel_hi:[0,0] neg_lo:[0,1] neg_hi:[1,0]
	s_mov_b32 s86, 0
	v_pk_fma_f32 v[184:185], v[224:225], v[224:225], v[184:185] op_sel:[1,1,0] op_sel_hi:[0,1,1] neg_lo:[1,0,0]
	s_mov_b64 s[84:85], -1
	v_pk_mul_f32 v[226:227], v[194:195], v[184:185] op_sel_hi:[1,0]
	s_nop 0
	v_pk_fma_f32 v[194:195], v[194:195], v[184:185], v[226:227] op_sel:[1,1,0] op_sel_hi:[0,1,1] neg_hi:[1,0,0]
	v_pk_mul_f32 v[226:227], v[184:185], v[224:225] op_sel_hi:[1,0]
	s_nop 0
	v_pk_fma_f32 v[184:185], v[184:185], v[224:225], v[226:227] op_sel:[1,1,0] op_sel_hi:[0,1,1] neg_lo:[1,0,0]
	s_nop 0
	v_pk_mul_f32 v[226:227], v[214:215], v[184:185] op_sel_hi:[1,0]
	s_nop 0
	v_pk_fma_f32 v[214:215], v[214:215], v[184:185], v[226:227] op_sel:[1,1,0] op_sel_hi:[0,1,1] neg_hi:[1,0,0]
	v_pk_mul_f32 v[226:227], v[184:185], v[224:225] op_sel_hi:[1,0]
	s_nop 0
	v_pk_fma_f32 v[184:185], v[184:185], v[224:225], v[226:227] op_sel:[1,1,0] op_sel_hi:[0,1,1] neg_lo:[1,0,0]
	s_nop 0
	v_pk_mul_f32 v[226:227], v[220:221], v[184:185] op_sel_hi:[1,0]
	s_nop 0
	v_pk_fma_f32 v[220:221], v[220:221], v[184:185], v[226:227] op_sel:[1,1,0] op_sel_hi:[0,1,1] neg_hi:[1,0,0]
	v_pk_mul_f32 v[226:227], v[184:185], v[224:225] op_sel_hi:[1,0]
	s_nop 0
	v_pk_fma_f32 v[184:185], v[184:185], v[224:225], v[226:227] op_sel:[1,1,0] op_sel_hi:[0,1,1] neg_lo:[1,0,0]
	s_nop 0
	v_pk_mul_f32 v[226:227], v[216:217], v[184:185] op_sel_hi:[1,0]
	s_nop 0
	v_pk_fma_f32 v[216:217], v[216:217], v[184:185], v[226:227] op_sel:[1,1,0] op_sel_hi:[0,1,1] neg_hi:[1,0,0]
	v_pk_mul_f32 v[226:227], v[184:185], v[224:225] op_sel_hi:[1,0]
	s_nop 0
	v_pk_fma_f32 v[184:185], v[184:185], v[224:225], v[226:227] op_sel:[1,1,0] op_sel_hi:[0,1,1] neg_lo:[1,0,0]
	s_nop 0
	v_pk_mul_f32 v[226:227], v[212:213], v[184:185] op_sel_hi:[1,0]
	s_nop 0
	v_pk_fma_f32 v[212:213], v[212:213], v[184:185], v[226:227] op_sel:[1,1,0] op_sel_hi:[0,1,1] neg_hi:[1,0,0]
	v_pk_mul_f32 v[226:227], v[184:185], v[224:225] op_sel_hi:[1,0]
	s_nop 0
	v_pk_fma_f32 v[184:185], v[184:185], v[224:225], v[226:227] op_sel:[1,1,0] op_sel_hi:[0,1,1] neg_lo:[1,0,0]
	s_nop 0
	v_pk_mul_f32 v[226:227], v[222:223], v[184:185] op_sel_hi:[1,0]
	s_nop 0
	v_pk_fma_f32 v[222:223], v[222:223], v[184:185], v[226:227] op_sel:[1,1,0] op_sel_hi:[0,1,1] neg_hi:[1,0,0]
	v_pk_mul_f32 v[226:227], v[184:185], v[224:225] op_sel_hi:[1,0]
	s_nop 0
	v_pk_fma_f32 v[184:185], v[184:185], v[224:225], v[226:227] op_sel:[1,1,0] op_sel_hi:[0,1,1] neg_lo:[1,0,0]
	s_nop 0
	v_pk_mul_f32 v[226:227], v[218:219], v[184:185] op_sel_hi:[1,0]
	s_nop 0
	v_pk_fma_f32 v[218:219], v[218:219], v[184:185], v[226:227] op_sel:[1,1,0] op_sel_hi:[0,1,1] neg_hi:[1,0,0]
	v_pk_mul_f32 v[226:227], v[184:185], v[224:225] op_sel_hi:[1,0]
	s_nop 0
	v_pk_fma_f32 v[184:185], v[184:185], v[224:225], v[226:227] op_sel:[1,1,0] op_sel_hi:[0,1,1] neg_lo:[1,0,0]
	s_nop 0
	v_pk_mul_f32 v[226:227], v[186:187], v[184:185] op_sel_hi:[1,0]
	s_nop 0
	v_pk_fma_f32 v[186:187], v[186:187], v[184:185], v[226:227] op_sel:[1,1,0] op_sel_hi:[0,1,1] neg_hi:[1,0,0]
	v_pk_mul_f32 v[226:227], v[184:185], v[224:225] op_sel_hi:[1,0]
	s_nop 0
	v_pk_fma_f32 v[184:185], v[184:185], v[224:225], v[226:227] op_sel:[1,1,0] op_sel_hi:[0,1,1] neg_lo:[1,0,0]
	s_nop 0
	v_pk_mul_f32 v[226:227], v[182:183], v[184:185] op_sel_hi:[1,0]
	s_nop 0
	v_pk_fma_f32 v[182:183], v[182:183], v[184:185], v[226:227] op_sel:[1,1,0] op_sel_hi:[0,1,1] neg_hi:[1,0,0]
	v_pk_mul_f32 v[226:227], v[184:185], v[224:225] op_sel_hi:[1,0]
	s_nop 0
	v_pk_fma_f32 v[184:185], v[184:185], v[224:225], v[226:227] op_sel:[1,1,0] op_sel_hi:[0,1,1] neg_lo:[1,0,0]
	s_nop 0
	v_pk_mul_f32 v[226:227], v[192:193], v[184:185] op_sel_hi:[1,0]
	s_nop 0
	v_pk_fma_f32 v[192:193], v[192:193], v[184:185], v[226:227] op_sel:[1,1,0] op_sel_hi:[0,1,1] neg_hi:[1,0,0]
	v_pk_mul_f32 v[226:227], v[184:185], v[224:225] op_sel_hi:[1,0]
	s_nop 0
	v_pk_fma_f32 v[184:185], v[184:185], v[224:225], v[226:227] op_sel:[1,1,0] op_sel_hi:[0,1,1] neg_lo:[1,0,0]
	s_nop 0
	v_pk_mul_f32 v[226:227], v[190:191], v[184:185] op_sel_hi:[1,0]
	s_nop 0
	v_pk_fma_f32 v[190:191], v[190:191], v[184:185], v[226:227] op_sel:[1,1,0] op_sel_hi:[0,1,1] neg_hi:[1,0,0]
	v_pk_mul_f32 v[226:227], v[184:185], v[224:225] op_sel_hi:[1,0]
	s_nop 0
	v_pk_fma_f32 v[184:185], v[184:185], v[224:225], v[226:227] op_sel:[1,1,0] op_sel_hi:[0,1,1] neg_lo:[1,0,0]
	s_nop 0
	v_pk_mul_f32 v[226:227], v[210:211], v[184:185] op_sel_hi:[1,0]
	s_nop 0
	v_pk_fma_f32 v[210:211], v[210:211], v[184:185], v[226:227] op_sel:[1,1,0] op_sel_hi:[0,1,1] neg_hi:[1,0,0]
	v_pk_mul_f32 v[226:227], v[184:185], v[224:225] op_sel_hi:[1,0]
	s_nop 0
	v_pk_fma_f32 v[184:185], v[184:185], v[224:225], v[226:227] op_sel:[1,1,0] op_sel_hi:[0,1,1] neg_lo:[1,0,0]
	s_nop 0
	v_pk_mul_f32 v[226:227], v[176:177], v[184:185] op_sel_hi:[1,0]
	s_nop 0
	v_pk_fma_f32 v[176:177], v[176:177], v[184:185], v[226:227] op_sel:[1,1,0] op_sel_hi:[0,1,1] neg_hi:[1,0,0]
	v_pk_mul_f32 v[226:227], v[184:185], v[224:225] op_sel_hi:[1,0]
	s_nop 0
	v_pk_fma_f32 v[184:185], v[184:185], v[224:225], v[226:227] op_sel:[1,1,0] op_sel_hi:[0,1,1] neg_lo:[1,0,0]
	s_nop 0
	v_pk_mul_f32 v[224:225], v[180:181], v[184:185] op_sel_hi:[1,0]
	s_nop 0
	v_pk_fma_f32 v[180:181], v[180:181], v[184:185], v[224:225] op_sel:[1,1,0] op_sel_hi:[0,1,1] neg_hi:[1,0,0]
	v_lshlrev_b32_e32 v224, 3, v38
	v_add3_u32 v184, 0, v228, v224
	ds_write2st64_b64 v184, v[188:189], v[178:179] offset1:18
	ds_write2st64_b64 v184, v[194:195], v[214:215] offset0:36 offset1:54
	ds_write2st64_b64 v184, v[220:221], v[216:217] offset0:72 offset1:90
	ds_write2st64_b64 v184, v[212:213], v[222:223] offset0:108 offset1:126
	v_add_u32_e32 v178, 0x12000, v184
	ds_write_b64 v178, v[218:219]
	v_add_u32_e32 v178, 0x14400, v184
	ds_write_b64 v178, v[186:187]
	v_add_u32_e32 v178, 0x16800, v184
	ds_write_b64 v178, v[182:183]
	v_add_u32_e32 v178, 0x18c00, v184
	ds_write_b64 v178, v[192:193]
	v_add_u32_e32 v178, 0x1b000, v184
	ds_write_b64 v178, v[190:191]
	v_add_u32_e32 v178, 0x1d400, v184
	ds_write_b64 v178, v[210:211]
	v_add_u32_e32 v178, 0x1f800, v184
	ds_write_b64 v178, v[176:177]
	v_add_u32_e32 v176, 0x21c00, v184
	v_add_u32_e32 v38, 0x200, v38
	v_pk_mul_f32 v[186:187], v[84:85], v[168:169] op_sel_hi:[1,0]
	ds_write_b64 v176, v[180:181]
	v_and_b32_e32 v214, -8, v38
	v_pk_add_f32 v[176:177], v[72:73], 0 op_sel_hi:[1,0]
	v_pk_add_f32 v[178:179], v[76:77], 0 op_sel_hi:[1,0]
	v_pk_mul_f32 v[180:181], v[76:77], v[166:167] op_sel_hi:[1,0]
	v_pk_fma_f32 v[168:169], v[84:85], v[168:169], v[186:187] op_sel:[1,1,0] op_sel_hi:[0,1,1] neg_hi:[1,0,0]
	v_pk_add_f32 v[186:187], v[88:89], 0 op_sel_hi:[1,0]
	v_pk_add_f32 v[188:189], v[92:93], 0 op_sel_hi:[1,0]
	v_pk_mul_f32 v[190:191], v[92:93], v[170:171] op_sel_hi:[1,0]
	v_pk_mul_f32 v[210:211], v[100:101], v[174:175] op_sel_hi:[1,0]
	v_cvt_f32_i32_e32 v38, v38
	v_pk_fma_f32 v[166:167], v[76:77], v[166:167], v[180:181] op_sel:[1,1,0] op_sel_hi:[0,1,1] neg_hi:[1,0,0]
	v_pk_add_f32 v[180:181], v[80:81], 0 op_sel_hi:[1,0]
	v_pk_mul_f32 v[182:183], v[80:81], v[162:163] op_sel_hi:[1,0]
	v_pk_add_f32 v[184:185], v[84:85], 0 op_sel_hi:[1,0]
	v_pk_fma_f32 v[170:171], v[92:93], v[170:171], v[190:191] op_sel:[1,1,0] op_sel_hi:[0,1,1] neg_hi:[1,0,0]
	v_pk_add_f32 v[190:191], v[96:97], 0 op_sel_hi:[1,0]
	v_pk_add_f32 v[194:195], v[100:101], 0 op_sel_hi:[1,0]
	v_pk_fma_f32 v[174:175], v[100:101], v[174:175], v[210:211] op_sel:[1,1,0] op_sel_hi:[0,1,1] neg_hi:[1,0,0]
	v_pk_add_f32 v[210:211], v[186:187], v[176:177]
	v_pk_add_f32 v[176:177], v[176:177], v[186:187] neg_lo:[0,1] neg_hi:[0,1]
	v_pk_add_f32 v[186:187], v[188:189], v[178:179]
	v_pk_add_f32 v[178:179], v[178:179], v[188:189] neg_lo:[0,1] neg_hi:[0,1]
	v_pk_fma_f32 v[182:183], v[80:81], v[162:163], v[182:183] op_sel:[1,1,0] op_sel_hi:[0,1,1] neg_hi:[1,0,0]
	v_pk_mul_f32 v[192:193], v[96:97], v[164:165] op_sel_hi:[1,0]
	v_pk_add_f32 v[212:213], v[166:167], v[170:171]
	v_pk_mul_f32 v[188:189], v[178:179], v[162:163] op_sel_hi:[1,0]
	v_pk_add_f32 v[166:167], v[166:167], v[170:171] neg_lo:[0,1] neg_hi:[0,1]
	v_pk_fma_f32 v[178:179], v[178:179], v[162:163], v[188:189] op_sel:[1,1,0] op_sel_hi:[0,1,1] neg_hi:[1,0,0]
	v_pk_add_f32 v[188:189], v[190:191], v[180:181]
	v_pk_add_f32 v[180:181], v[180:181], v[190:191] op_sel:[1,1] op_sel_hi:[0,0] neg_lo:[0,1] neg_hi:[1,0]
	v_pk_add_f32 v[190:191], v[194:195], v[184:185]
	v_pk_add_f32 v[184:185], v[184:185], v[194:195] neg_lo:[0,1] neg_hi:[0,1]
	v_pk_mul_f32 v[170:171], v[166:167], v[162:163] op_sel_hi:[1,0]
	v_pk_fma_f32 v[192:193], v[96:97], v[164:165], v[192:193] op_sel:[1,1,0] op_sel_hi:[0,1,1] neg_hi:[1,0,0]
	v_mul_f32_e32 v38, 0x38800000, v38
	v_pk_mul_f32 v[194:195], v[184:185], v[164:165] op_sel_hi:[1,0]
	v_pk_fma_f32 v[162:163], v[166:167], v[162:163], v[170:171] op_sel:[1,1,0] op_sel_hi:[0,1,1] neg_hi:[1,0,0]
	v_pk_add_f32 v[166:167], v[182:183], v[192:193]
	v_pk_fma_f32 v[184:185], v[184:185], v[164:165], v[194:195] op_sel:[1,1,0] op_sel_hi:[0,1,1] neg_hi:[1,0,0]
	v_pk_add_f32 v[194:195], v[72:73], v[172:173]
	v_pk_add_f32 v[172:173], v[72:73], v[172:173] neg_lo:[0,1] neg_hi:[0,1]
	v_pk_add_f32 v[170:171], v[182:183], v[192:193] op_sel:[1,1] op_sel_hi:[0,0] neg_lo:[0,1] neg_hi:[1,0]
	v_pk_add_f32 v[182:183], v[168:169], v[174:175]
	v_pk_add_f32 v[168:169], v[168:169], v[174:175] neg_lo:[0,1] neg_hi:[0,1]
	v_pk_add_f32 v[192:193], v[212:213], v[182:183]
	v_pk_mul_f32 v[174:175], v[168:169], v[164:165] op_sel_hi:[1,0]
	v_pk_add_f32 v[182:183], v[212:213], v[182:183] op_sel:[1,1] op_sel_hi:[0,0] neg_lo:[0,1] neg_hi:[1,0]
	s_nop 0
	v_pk_fma_f32 v[164:165], v[168:169], v[164:165], v[174:175] op_sel:[1,1,0] op_sel_hi:[0,1,1] neg_hi:[1,0,0]
	v_pk_add_f32 v[168:169], v[188:189], v[210:211]
	v_pk_add_f32 v[174:175], v[210:211], v[188:189] neg_lo:[0,1] neg_hi:[0,1]
	v_pk_add_f32 v[188:189], v[190:191], v[186:187]
	v_pk_add_f32 v[186:187], v[186:187], v[190:191] op_sel:[1,1] op_sel_hi:[0,0] neg_lo:[0,1] neg_hi:[1,0]
	v_pk_add_f32 v[190:191], v[176:177], v[180:181]
	v_pk_add_f32 v[176:177], v[176:177], v[180:181] neg_lo:[0,1] neg_hi:[0,1]
	v_pk_add_f32 v[180:181], v[178:179], v[184:185]
	v_pk_add_f32 v[178:179], v[178:179], v[184:185] op_sel:[1,1] op_sel_hi:[0,0] neg_lo:[0,1] neg_hi:[1,0]
	v_pk_add_f32 v[184:185], v[194:195], v[166:167]
	v_pk_add_f32 v[166:167], v[194:195], v[166:167] neg_lo:[0,1] neg_hi:[0,1]
	v_pk_add_f32 v[194:195], v[172:173], v[170:171]
	v_pk_add_f32 v[170:171], v[172:173], v[170:171] neg_lo:[0,1] neg_hi:[0,1]
	v_pk_add_f32 v[172:173], v[162:163], v[164:165]
	v_pk_add_f32 v[162:163], v[162:163], v[164:165] op_sel:[1,1] op_sel_hi:[0,0] neg_lo:[0,1] neg_hi:[1,0]
	v_pk_add_f32 v[164:165], v[188:189], v[168:169]
	v_pk_add_f32 v[168:169], v[168:169], v[188:189] neg_lo:[0,1] neg_hi:[0,1]
	v_pk_add_f32 v[188:189], v[174:175], v[186:187]
	v_pk_add_f32 v[174:175], v[174:175], v[186:187] neg_lo:[0,1] neg_hi:[0,1]
	v_pk_add_f32 v[186:187], v[190:191], v[180:181]
	v_pk_add_f32 v[180:181], v[190:191], v[180:181] neg_lo:[0,1] neg_hi:[0,1]
	v_pk_add_f32 v[190:191], v[176:177], v[178:179]
	v_pk_add_f32 v[176:177], v[176:177], v[178:179] neg_lo:[0,1] neg_hi:[0,1]
	v_pk_add_f32 v[178:179], v[184:185], v[192:193]
	v_pk_add_f32 v[184:185], v[184:185], v[192:193] neg_lo:[0,1] neg_hi:[0,1]
	v_pk_add_f32 v[192:193], v[166:167], v[182:183]
	v_pk_add_f32 v[166:167], v[166:167], v[182:183] neg_lo:[0,1] neg_hi:[0,1]
	v_pk_add_f32 v[182:183], v[194:195], v[172:173]
	v_cos_f32_e32 v210, v38
	v_sin_f32_e32 v211, v38
	v_pk_add_f32 v[172:173], v[194:195], v[172:173] neg_lo:[0,1] neg_hi:[0,1]
	v_pk_add_f32 v[194:195], v[170:171], v[162:163]
	v_pk_add_f32 v[162:163], v[170:171], v[162:163] neg_lo:[0,1] neg_hi:[0,1]
	v_pk_mul_f32 v[170:171], v[178:179], v[210:211] op_sel_hi:[1,0]
	v_add3_u32 v38, 0, v214, v224
	v_pk_fma_f32 v[170:171], v[178:179], v[210:211], v[170:171] op_sel:[1,1,0] op_sel_hi:[0,1,1] neg_hi:[1,0,0]
	v_pk_mul_f32 v[178:179], v[210:211], v[210:211] op_sel_hi:[1,0]
	s_nop 0
	v_pk_fma_f32 v[178:179], v[210:211], v[210:211], v[178:179] op_sel:[1,1,0] op_sel_hi:[0,1,1] neg_lo:[1,0,0]
	s_nop 0
	v_pk_mul_f32 v[212:213], v[186:187], v[178:179] op_sel_hi:[1,0]
	s_nop 0
	v_pk_fma_f32 v[186:187], v[186:187], v[178:179], v[212:213] op_sel:[1,1,0] op_sel_hi:[0,1,1] neg_hi:[1,0,0]
	v_pk_mul_f32 v[212:213], v[178:179], v[210:211] op_sel_hi:[1,0]
	s_nop 0
	v_pk_fma_f32 v[178:179], v[178:179], v[210:211], v[212:213] op_sel:[1,1,0] op_sel_hi:[0,1,1] neg_lo:[1,0,0]
	s_nop 0
	v_pk_mul_f32 v[212:213], v[182:183], v[178:179] op_sel_hi:[1,0]
	s_nop 0
	v_pk_fma_f32 v[182:183], v[182:183], v[178:179], v[212:213] op_sel:[1,1,0] op_sel_hi:[0,1,1] neg_hi:[1,0,0]
	v_pk_mul_f32 v[212:213], v[178:179], v[210:211] op_sel_hi:[1,0]
	s_nop 0
	v_pk_fma_f32 v[178:179], v[178:179], v[210:211], v[212:213] op_sel:[1,1,0] op_sel_hi:[0,1,1] neg_lo:[1,0,0]
	s_nop 0
	v_pk_mul_f32 v[212:213], v[188:189], v[178:179] op_sel_hi:[1,0]
	s_nop 0
	v_pk_fma_f32 v[188:189], v[188:189], v[178:179], v[212:213] op_sel:[1,1,0] op_sel_hi:[0,1,1] neg_hi:[1,0,0]
	v_pk_mul_f32 v[212:213], v[178:179], v[210:211] op_sel_hi:[1,0]
	s_nop 0
	v_pk_fma_f32 v[178:179], v[178:179], v[210:211], v[212:213] op_sel:[1,1,0] op_sel_hi:[0,1,1] neg_lo:[1,0,0]
	s_nop 0
	v_pk_mul_f32 v[212:213], v[192:193], v[178:179] op_sel_hi:[1,0]
	s_nop 0
	v_pk_fma_f32 v[192:193], v[192:193], v[178:179], v[212:213] op_sel:[1,1,0] op_sel_hi:[0,1,1] neg_hi:[1,0,0]
	v_pk_mul_f32 v[212:213], v[178:179], v[210:211] op_sel_hi:[1,0]
	s_nop 0
	v_pk_fma_f32 v[178:179], v[178:179], v[210:211], v[212:213] op_sel:[1,1,0] op_sel_hi:[0,1,1] neg_lo:[1,0,0]
	s_nop 0
	v_pk_mul_f32 v[212:213], v[190:191], v[178:179] op_sel_hi:[1,0]
	s_nop 0
	v_pk_fma_f32 v[190:191], v[190:191], v[178:179], v[212:213] op_sel:[1,1,0] op_sel_hi:[0,1,1] neg_hi:[1,0,0]
	v_pk_mul_f32 v[212:213], v[178:179], v[210:211] op_sel_hi:[1,0]
	s_nop 0
	v_pk_fma_f32 v[178:179], v[178:179], v[210:211], v[212:213] op_sel:[1,1,0] op_sel_hi:[0,1,1] neg_lo:[1,0,0]
	s_nop 0
	v_pk_mul_f32 v[212:213], v[194:195], v[178:179] op_sel_hi:[1,0]
	s_nop 0
	v_pk_fma_f32 v[194:195], v[194:195], v[178:179], v[212:213] op_sel:[1,1,0] op_sel_hi:[0,1,1] neg_hi:[1,0,0]
	v_pk_mul_f32 v[212:213], v[178:179], v[210:211] op_sel_hi:[1,0]
	s_nop 0
	v_pk_fma_f32 v[178:179], v[178:179], v[210:211], v[212:213] op_sel:[1,1,0] op_sel_hi:[0,1,1] neg_lo:[1,0,0]
	s_nop 0
	v_pk_mul_f32 v[212:213], v[168:169], v[178:179] op_sel_hi:[1,0]
	s_nop 0
	v_pk_fma_f32 v[168:169], v[168:169], v[178:179], v[212:213] op_sel:[1,1,0] op_sel_hi:[0,1,1] neg_hi:[1,0,0]
	v_pk_mul_f32 v[212:213], v[178:179], v[210:211] op_sel_hi:[1,0]
	s_nop 0
	v_pk_fma_f32 v[178:179], v[178:179], v[210:211], v[212:213] op_sel:[1,1,0] op_sel_hi:[0,1,1] neg_lo:[1,0,0]
	s_nop 0
	v_pk_mul_f32 v[212:213], v[184:185], v[178:179] op_sel_hi:[1,0]
	s_nop 0
	v_pk_fma_f32 v[184:185], v[184:185], v[178:179], v[212:213] op_sel:[1,1,0] op_sel_hi:[0,1,1] neg_hi:[1,0,0]
	v_pk_mul_f32 v[212:213], v[178:179], v[210:211] op_sel_hi:[1,0]
	s_nop 0
	v_pk_fma_f32 v[178:179], v[178:179], v[210:211], v[212:213] op_sel:[1,1,0] op_sel_hi:[0,1,1] neg_lo:[1,0,0]
	s_nop 0
	v_pk_mul_f32 v[212:213], v[180:181], v[178:179] op_sel_hi:[1,0]
	s_nop 0
	v_pk_fma_f32 v[180:181], v[180:181], v[178:179], v[212:213] op_sel:[1,1,0] op_sel_hi:[0,1,1] neg_hi:[1,0,0]
	v_pk_mul_f32 v[212:213], v[178:179], v[210:211] op_sel_hi:[1,0]
	s_nop 0
	v_pk_fma_f32 v[178:179], v[178:179], v[210:211], v[212:213] op_sel:[1,1,0] op_sel_hi:[0,1,1] neg_lo:[1,0,0]
	s_nop 0
	v_pk_mul_f32 v[212:213], v[172:173], v[178:179] op_sel_hi:[1,0]
	s_nop 0
	v_pk_fma_f32 v[172:173], v[172:173], v[178:179], v[212:213] op_sel:[1,1,0] op_sel_hi:[0,1,1] neg_hi:[1,0,0]
	v_pk_mul_f32 v[212:213], v[178:179], v[210:211] op_sel_hi:[1,0]
	s_nop 0
	v_pk_fma_f32 v[178:179], v[178:179], v[210:211], v[212:213] op_sel:[1,1,0] op_sel_hi:[0,1,1] neg_lo:[1,0,0]
	s_nop 0
	v_pk_mul_f32 v[212:213], v[174:175], v[178:179] op_sel_hi:[1,0]
	s_nop 0
	v_pk_fma_f32 v[174:175], v[174:175], v[178:179], v[212:213] op_sel:[1,1,0] op_sel_hi:[0,1,1] neg_hi:[1,0,0]
	v_pk_mul_f32 v[212:213], v[178:179], v[210:211] op_sel_hi:[1,0]
	s_nop 0
	v_pk_fma_f32 v[178:179], v[178:179], v[210:211], v[212:213] op_sel:[1,1,0] op_sel_hi:[0,1,1] neg_lo:[1,0,0]
	s_nop 0
	v_pk_mul_f32 v[212:213], v[166:167], v[178:179] op_sel_hi:[1,0]
	s_nop 0
	v_pk_fma_f32 v[166:167], v[166:167], v[178:179], v[212:213] op_sel:[1,1,0] op_sel_hi:[0,1,1] neg_hi:[1,0,0]
	v_pk_mul_f32 v[212:213], v[178:179], v[210:211] op_sel_hi:[1,0]
	s_nop 0
	v_pk_fma_f32 v[178:179], v[178:179], v[210:211], v[212:213] op_sel:[1,1,0] op_sel_hi:[0,1,1] neg_lo:[1,0,0]
	s_nop 0
	v_pk_mul_f32 v[212:213], v[176:177], v[178:179] op_sel_hi:[1,0]
	s_nop 0
	v_pk_fma_f32 v[176:177], v[176:177], v[178:179], v[212:213] op_sel:[1,1,0] op_sel_hi:[0,1,1] neg_hi:[1,0,0]
	v_pk_mul_f32 v[212:213], v[178:179], v[210:211] op_sel_hi:[1,0]
	s_nop 0
	v_pk_fma_f32 v[178:179], v[178:179], v[210:211], v[212:213] op_sel:[1,1,0] op_sel_hi:[0,1,1] neg_lo:[1,0,0]
	s_nop 0
	v_pk_mul_f32 v[210:211], v[162:163], v[178:179] op_sel_hi:[1,0]
	s_nop 0
	v_pk_fma_f32 v[162:163], v[162:163], v[178:179], v[210:211] op_sel:[1,1,0] op_sel_hi:[0,1,1] neg_hi:[1,0,0]
	v_add_u32_e32 v178, 0x1000, v38
	ds_write2st64_b64 v38, v[164:165], v[170:171] offset0:8 offset1:26
	ds_write2st64_b64 v38, v[186:187], v[182:183] offset0:44 offset1:62
	ds_write2st64_b64 v38, v[188:189], v[192:193] offset0:80 offset1:98
	ds_write_b64 v38, v[190:191] offset:59392
	ds_write_b64 v178, v[194:195] offset:64512
	v_add_u32_e32 v164, 0x13000, v38
	ds_write_b64 v164, v[168:169]
	v_add_u32_e32 v164, 0x15400, v38
	ds_write_b64 v164, v[184:185]
	v_add_u32_e32 v164, 0x17800, v38
	ds_write_b64 v164, v[180:181]
	v_add_u32_e32 v164, 0x19c00, v38
	ds_write_b64 v164, v[172:173]
	v_add_u32_e32 v164, 0x1c000, v38
	ds_write_b64 v164, v[174:175]
	v_add_u32_e32 v164, 0x1e400, v38
	ds_write_b64 v164, v[166:167]
	v_add_u32_e32 v164, 0x20800, v38
	v_add_u32_e32 v38, 0x22c00, v38
	ds_write_b64 v164, v[176:177]
	ds_write_b64 v38, v[162:163]
	v_mov_b32_e32 v164, v204
	s_waitcnt lgkmcnt(0)
	s_barrier
	s_cselect_b32 s99, 1, 0
	v_readfirstlane_b32 s98, v0
	s_cmp_lt_u32 s98, 0x100
	s_cbranch_scc1 .Lfft_stg_19667
	s_sleep 8
.Lfft_stg_19667:
	s_cmp_lg_u32 s99, 0
	s_nop 0
	v_and_b32_e32 v38, 63, v164
	v_cvt_f32_ubyte0_e32 v162, v38
	v_mul_f32_e32 v163, 0x3a800000, v162
	v_cos_f32_e32 v162, v163
	v_sin_f32_e32 v163, v163
	v_lshlrev_b32_e32 v210, 4, v164
.LBB0_764:
	v_add_u32_e32 v164, s86, v210
	v_and_b32_e32 v164, 0xfffffc00, v164
	v_or_b32_e32 v165, v164, v38
	v_bitop3_b32 v164, v164, s97, v38 bitop3:0xc8
	v_lshlrev_b32_e32 v165, 3, v165
	v_add3_u32 v211, 0, v164, v165
	v_add_u32_e32 v212, 0x800, v211
	v_add_u32_e32 v213, 0x1000, v211
	ds_read2_b64 v[164:167], v211 offset1:72
	ds_read2_b64 v[168:171], v211 offset0:144 offset1:216
	ds_read2_b64 v[172:175], v212 offset0:32 offset1:104
	ds_read2_b64 v[176:179], v212 offset0:176 offset1:248
	ds_read2_b64 v[180:183], v213 offset0:64 offset1:136
	v_add_u32_e32 v214, 0x1400, v211
	ds_read2_b64 v[184:187], v214 offset0:80 offset1:152
	v_add_u32_e32 v215, 0x1800, v211
	ds_read2_b64 v[188:191], v215 offset0:96 offset1:168
	v_add_u32_e32 v216, 0x1c00, v211
	ds_read2_b64 v[192:195], v216 offset0:112 offset1:184
	s_waitcnt lgkmcnt(3)
	v_pk_add_f32 v[218:219], v[164:165], v[180:181]
	v_pk_add_f32 v[164:165], v[164:165], v[180:181] neg_lo:[0,1] neg_hi:[0,1]
	v_pk_add_f32 v[180:181], v[166:167], v[182:183]
	v_pk_add_f32 v[166:167], v[166:167], v[182:183] neg_lo:[0,1] neg_hi:[0,1]
	v_mov_b64_e32 v[182:183], s[4:5]
	v_pk_mul_f32 v[220:221], v[166:167], v[182:183] op_sel_hi:[1,0]
	s_movk_i32 s86, 0x2000
	v_pk_fma_f32 v[166:167], v[166:167], v[182:183], v[220:221] op_sel:[1,1,0] op_sel_hi:[0,1,1] neg_hi:[1,0,0]
	s_waitcnt lgkmcnt(2)
	v_pk_add_f32 v[182:183], v[168:169], v[184:185]
	v_pk_add_f32 v[168:169], v[168:169], v[184:185] neg_lo:[0,1] neg_hi:[0,1]
	v_mov_b64_e32 v[184:185], s[6:7]
	v_pk_mul_f32 v[220:221], v[168:169], v[184:185] op_sel_hi:[1,0]
	s_and_b64 vcc, exec, s[84:85]
	v_pk_fma_f32 v[168:169], v[168:169], v[184:185], v[220:221] op_sel:[1,1,0] op_sel_hi:[0,1,1] neg_hi:[1,0,0]
	v_pk_add_f32 v[220:221], v[170:171], v[186:187]
	v_pk_add_f32 v[170:171], v[170:171], v[186:187] neg_lo:[0,1] neg_hi:[0,1]
	v_mov_b64_e32 v[186:187], s[10:11]
	v_pk_mul_f32 v[222:223], v[170:171], v[186:187] op_sel_hi:[1,0]
	s_mov_b64 s[84:85], 0
	v_pk_fma_f32 v[170:171], v[170:171], v[186:187], v[222:223] op_sel:[1,1,0] op_sel_hi:[0,1,1] neg_hi:[1,0,0]
	s_waitcnt lgkmcnt(1)
	v_pk_add_f32 v[186:187], v[172:173], v[188:189]
	v_pk_add_f32 v[172:173], v[172:173], v[188:189] op_sel:[1,1] op_sel_hi:[0,0] neg_lo:[0,1] neg_hi:[1,0]
	v_pk_add_f32 v[188:189], v[174:175], v[190:191]
	v_pk_add_f32 v[174:175], v[174:175], v[190:191] neg_lo:[0,1] neg_hi:[0,1]
	v_mov_b64_e32 v[190:191], s[12:13]
	v_pk_mul_f32 v[222:223], v[174:175], v[190:191] op_sel_hi:[1,0]
	s_nop 0
	v_pk_fma_f32 v[174:175], v[174:175], v[190:191], v[222:223] op_sel:[1,1,0] op_sel_hi:[0,1,1] neg_hi:[1,0,0]
	s_waitcnt lgkmcnt(0)
	v_pk_add_f32 v[190:191], v[176:177], v[192:193]
	v_pk_add_f32 v[176:177], v[176:177], v[192:193] neg_lo:[0,1] neg_hi:[0,1]
	v_mov_b64_e32 v[192:193], s[14:15]
	v_pk_mul_f32 v[222:223], v[176:177], v[192:193] op_sel_hi:[1,0]
	s_nop 0
	v_pk_fma_f32 v[176:177], v[176:177], v[192:193], v[222:223] op_sel:[1,1,0] op_sel_hi:[0,1,1] neg_hi:[1,0,0]
	v_pk_add_f32 v[222:223], v[178:179], v[194:195]
	v_pk_add_f32 v[178:179], v[178:179], v[194:195] neg_lo:[0,1] neg_hi:[0,1]
	v_mov_b64_e32 v[194:195], s[16:17]
	v_pk_mul_f32 v[224:225], v[178:179], v[194:195] op_sel_hi:[1,0]
	s_nop 0
	v_pk_fma_f32 v[178:179], v[178:179], v[194:195], v[224:225] op_sel:[1,1,0] op_sel_hi:[0,1,1] neg_hi:[1,0,0]
	v_pk_add_f32 v[194:195], v[218:219], v[186:187]
	v_pk_add_f32 v[186:187], v[218:219], v[186:187] neg_lo:[0,1] neg_hi:[0,1]
	v_pk_add_f32 v[218:219], v[180:181], v[188:189]
	v_pk_add_f32 v[180:181], v[180:181], v[188:189] neg_lo:[0,1] neg_hi:[0,1]
	s_nop 0
	v_pk_mul_f32 v[188:189], v[180:181], v[184:185] op_sel_hi:[1,0]
	s_nop 0
	v_pk_fma_f32 v[180:181], v[180:181], v[184:185], v[188:189] op_sel:[1,1,0] op_sel_hi:[0,1,1] neg_hi:[1,0,0]
	v_pk_add_f32 v[188:189], v[182:183], v[190:191]
	v_pk_add_f32 v[182:183], v[182:183], v[190:191] op_sel:[1,1] op_sel_hi:[0,0] neg_lo:[0,1] neg_hi:[1,0]
	v_pk_add_f32 v[190:191], v[220:221], v[222:223]
	v_pk_add_f32 v[220:221], v[220:221], v[222:223] neg_lo:[0,1] neg_hi:[0,1]
	s_nop 0
	v_pk_mul_f32 v[222:223], v[220:221], v[192:193] op_sel_hi:[1,0]
	s_nop 0
	v_pk_fma_f32 v[220:221], v[220:221], v[192:193], v[222:223] op_sel:[1,1,0] op_sel_hi:[0,1,1] neg_hi:[1,0,0]
	v_pk_add_f32 v[222:223], v[164:165], v[172:173]
	v_pk_add_f32 v[164:165], v[164:165], v[172:173] neg_lo:[0,1] neg_hi:[0,1]
	v_pk_add_f32 v[172:173], v[166:167], v[174:175]
	v_pk_add_f32 v[166:167], v[166:167], v[174:175] neg_lo:[0,1] neg_hi:[0,1]
	s_nop 0
	v_pk_mul_f32 v[174:175], v[166:167], v[184:185] op_sel_hi:[1,0]
	s_nop 0
	v_pk_fma_f32 v[166:167], v[166:167], v[184:185], v[174:175] op_sel:[1,1,0] op_sel_hi:[0,1,1] neg_hi:[1,0,0]
	v_pk_add_f32 v[174:175], v[168:169], v[176:177]
	v_pk_add_f32 v[168:169], v[168:169], v[176:177] op_sel:[1,1] op_sel_hi:[0,0] neg_lo:[0,1] neg_hi:[1,0]
	v_pk_add_f32 v[176:177], v[170:171], v[178:179]
	v_pk_add_f32 v[170:171], v[170:171], v[178:179] neg_lo:[0,1] neg_hi:[0,1]
	v_pk_add_f32 v[184:185], v[194:195], v[188:189] neg_lo:[0,1] neg_hi:[0,1]
	v_pk_mul_f32 v[178:179], v[170:171], v[192:193] op_sel_hi:[1,0]
	v_pk_add_f32 v[224:225], v[164:165], v[168:169]
	v_pk_fma_f32 v[170:171], v[170:171], v[192:193], v[178:179] op_sel:[1,1,0] op_sel_hi:[0,1,1] neg_hi:[1,0,0]
	v_pk_add_f32 v[178:179], v[194:195], v[188:189]
	v_pk_add_f32 v[188:189], v[218:219], v[190:191]
	v_pk_add_f32 v[190:191], v[218:219], v[190:191] op_sel:[1,1] op_sel_hi:[0,0] neg_lo:[0,1] neg_hi:[1,0]
	v_pk_add_f32 v[194:195], v[186:187], v[182:183]
	v_pk_add_f32 v[218:219], v[180:181], v[220:221]
	v_pk_add_f32 v[180:181], v[180:181], v[220:221] op_sel:[1,1] op_sel_hi:[0,0] neg_lo:[0,1] neg_hi:[1,0]
	v_pk_add_f32 v[220:221], v[222:223], v[174:175]
	v_pk_add_f32 v[174:175], v[222:223], v[174:175] neg_lo:[0,1] neg_hi:[0,1]
	v_pk_add_f32 v[222:223], v[172:173], v[176:177]
	v_pk_add_f32 v[172:173], v[172:173], v[176:177] op_sel:[1,1] op_sel_hi:[0,0] neg_lo:[0,1] neg_hi:[1,0]
	v_pk_add_f32 v[182:183], v[186:187], v[182:183] neg_lo:[0,1] neg_hi:[0,1]
	v_pk_add_f32 v[226:227], v[164:165], v[168:169] neg_lo:[0,1] neg_hi:[0,1]
	v_pk_add_f32 v[186:187], v[184:185], v[190:191]
	v_pk_add_f32 v[168:169], v[184:185], v[190:191] neg_lo:[0,1] neg_hi:[0,1]
	v_pk_add_f32 v[192:193], v[194:195], v[218:219]
	v_pk_add_f32 v[176:177], v[194:195], v[218:219] neg_lo:[0,1] neg_hi:[0,1]
	v_pk_add_f32 v[218:219], v[220:221], v[222:223]
	v_pk_add_f32 v[190:191], v[174:175], v[172:173]
	v_pk_add_f32 v[174:175], v[174:175], v[172:173] neg_lo:[0,1] neg_hi:[0,1]
	v_pk_mul_f32 v[172:173], v[218:219], v[162:163] op_sel_hi:[1,0]
	v_pk_add_f32 v[228:229], v[166:167], v[170:171]
	v_pk_fma_f32 v[172:173], v[218:219], v[162:163], v[172:173] op_sel:[1,1,0] op_sel_hi:[0,1,1] neg_hi:[1,0,0]
	v_pk_mul_f32 v[218:219], v[162:163], v[162:163] op_sel_hi:[1,0]
	v_pk_add_f32 v[170:171], v[166:167], v[170:171] op_sel:[1,1] op_sel_hi:[0,0] neg_lo:[0,1] neg_hi:[1,0]
	v_pk_add_f32 v[184:185], v[182:183], v[180:181]
	v_pk_add_f32 v[166:167], v[182:183], v[180:181] neg_lo:[0,1] neg_hi:[0,1]
	v_pk_add_f32 v[182:183], v[220:221], v[222:223] neg_lo:[0,1] neg_hi:[0,1]
	v_pk_fma_f32 v[218:219], v[162:163], v[162:163], v[218:219] op_sel:[1,1,0] op_sel_hi:[0,1,1] neg_lo:[1,0,0]
	v_pk_add_f32 v[194:195], v[224:225], v[228:229]
	v_pk_mul_f32 v[220:221], v[192:193], v[218:219] op_sel_hi:[1,0]
	v_pk_add_f32 v[164:165], v[178:179], v[188:189]
	v_pk_fma_f32 v[192:193], v[192:193], v[218:219], v[220:221] op_sel:[1,1,0] op_sel_hi:[0,1,1] neg_hi:[1,0,0]
	v_pk_mul_f32 v[220:221], v[218:219], v[162:163] op_sel_hi:[1,0]
	v_pk_add_f32 v[178:179], v[178:179], v[188:189] neg_lo:[0,1] neg_hi:[0,1]
	v_pk_fma_f32 v[218:219], v[218:219], v[162:163], v[220:221] op_sel:[1,1,0] op_sel_hi:[0,1,1] neg_lo:[1,0,0]
	v_pk_add_f32 v[188:189], v[226:227], v[170:171]
	v_pk_mul_f32 v[220:221], v[194:195], v[218:219] op_sel_hi:[1,0]
	v_pk_add_f32 v[180:181], v[224:225], v[228:229] neg_lo:[0,1] neg_hi:[0,1]
	v_pk_fma_f32 v[194:195], v[194:195], v[218:219], v[220:221] op_sel:[1,1,0] op_sel_hi:[0,1,1] neg_hi:[1,0,0]
	v_pk_mul_f32 v[220:221], v[218:219], v[162:163] op_sel_hi:[1,0]
	v_pk_add_f32 v[170:171], v[226:227], v[170:171] neg_lo:[0,1] neg_hi:[0,1]
	v_pk_fma_f32 v[218:219], v[218:219], v[162:163], v[220:221] op_sel:[1,1,0] op_sel_hi:[0,1,1] neg_lo:[1,0,0]
	s_nop 0
	v_pk_mul_f32 v[220:221], v[186:187], v[218:219] op_sel_hi:[1,0]
	s_nop 0
	v_pk_fma_f32 v[186:187], v[186:187], v[218:219], v[220:221] op_sel:[1,1,0] op_sel_hi:[0,1,1] neg_hi:[1,0,0]
	v_pk_mul_f32 v[220:221], v[218:219], v[162:163] op_sel_hi:[1,0]
	s_nop 0
	v_pk_fma_f32 v[218:219], v[218:219], v[162:163], v[220:221] op_sel:[1,1,0] op_sel_hi:[0,1,1] neg_lo:[1,0,0]
	s_nop 0
	v_pk_mul_f32 v[220:221], v[190:191], v[218:219] op_sel_hi:[1,0]
	s_nop 0
	v_pk_fma_f32 v[190:191], v[190:191], v[218:219], v[220:221] op_sel:[1,1,0] op_sel_hi:[0,1,1] neg_hi:[1,0,0]
	v_pk_mul_f32 v[220:221], v[218:219], v[162:163] op_sel_hi:[1,0]
	s_nop 0
	v_pk_fma_f32 v[218:219], v[218:219], v[162:163], v[220:221] op_sel:[1,1,0] op_sel_hi:[0,1,1] neg_lo:[1,0,0]
	s_nop 0
	v_pk_mul_f32 v[220:221], v[184:185], v[218:219] op_sel_hi:[1,0]
	s_nop 0
	v_pk_fma_f32 v[184:185], v[184:185], v[218:219], v[220:221] op_sel:[1,1,0] op_sel_hi:[0,1,1] neg_hi:[1,0,0]
	v_pk_mul_f32 v[220:221], v[218:219], v[162:163] op_sel_hi:[1,0]
	s_nop 0
	v_pk_fma_f32 v[218:219], v[218:219], v[162:163], v[220:221] op_sel:[1,1,0] op_sel_hi:[0,1,1] neg_lo:[1,0,0]
	s_nop 0
	v_pk_mul_f32 v[220:221], v[188:189], v[218:219] op_sel_hi:[1,0]
	s_nop 0
	v_pk_fma_f32 v[188:189], v[188:189], v[218:219], v[220:221] op_sel:[1,1,0] op_sel_hi:[0,1,1] neg_hi:[1,0,0]
	v_pk_mul_f32 v[220:221], v[218:219], v[162:163] op_sel_hi:[1,0]
	s_nop 0
	v_pk_fma_f32 v[218:219], v[218:219], v[162:163], v[220:221] op_sel:[1,1,0] op_sel_hi:[0,1,1] neg_lo:[1,0,0]
	s_nop 0
	v_pk_mul_f32 v[220:221], v[178:179], v[218:219] op_sel_hi:[1,0]
	s_nop 0
	v_pk_fma_f32 v[178:179], v[178:179], v[218:219], v[220:221] op_sel:[1,1,0] op_sel_hi:[0,1,1] neg_hi:[1,0,0]
	v_pk_mul_f32 v[220:221], v[218:219], v[162:163] op_sel_hi:[1,0]
	s_nop 0
	v_pk_fma_f32 v[218:219], v[218:219], v[162:163], v[220:221] op_sel:[1,1,0] op_sel_hi:[0,1,1] neg_lo:[1,0,0]
	s_nop 0
	v_pk_mul_f32 v[220:221], v[182:183], v[218:219] op_sel_hi:[1,0]
	s_nop 0
	v_pk_fma_f32 v[182:183], v[182:183], v[218:219], v[220:221] op_sel:[1,1,0] op_sel_hi:[0,1,1] neg_hi:[1,0,0]
	v_pk_mul_f32 v[220:221], v[218:219], v[162:163] op_sel_hi:[1,0]
	s_nop 0
	v_pk_fma_f32 v[218:219], v[218:219], v[162:163], v[220:221] op_sel:[1,1,0] op_sel_hi:[0,1,1] neg_lo:[1,0,0]
	s_nop 0
	v_pk_mul_f32 v[220:221], v[176:177], v[218:219] op_sel_hi:[1,0]
	s_nop 0
	v_pk_fma_f32 v[176:177], v[176:177], v[218:219], v[220:221] op_sel:[1,1,0] op_sel_hi:[0,1,1] neg_hi:[1,0,0]
	v_pk_mul_f32 v[220:221], v[218:219], v[162:163] op_sel_hi:[1,0]
	s_nop 0
	v_pk_fma_f32 v[218:219], v[218:219], v[162:163], v[220:221] op_sel:[1,1,0] op_sel_hi:[0,1,1] neg_lo:[1,0,0]
	s_nop 0
	v_pk_mul_f32 v[220:221], v[180:181], v[218:219] op_sel_hi:[1,0]
	s_nop 0
	v_pk_fma_f32 v[180:181], v[180:181], v[218:219], v[220:221] op_sel:[1,1,0] op_sel_hi:[0,1,1] neg_hi:[1,0,0]
	v_pk_mul_f32 v[220:221], v[218:219], v[162:163] op_sel_hi:[1,0]
	s_nop 0
	v_pk_fma_f32 v[218:219], v[218:219], v[162:163], v[220:221] op_sel:[1,1,0] op_sel_hi:[0,1,1] neg_lo:[1,0,0]
	s_nop 0
	v_pk_mul_f32 v[220:221], v[168:169], v[218:219] op_sel_hi:[1,0]
	s_nop 0
	v_pk_fma_f32 v[168:169], v[168:169], v[218:219], v[220:221] op_sel:[1,1,0] op_sel_hi:[0,1,1] neg_hi:[1,0,0]
	v_pk_mul_f32 v[220:221], v[218:219], v[162:163] op_sel_hi:[1,0]
	s_nop 0
	v_pk_fma_f32 v[218:219], v[218:219], v[162:163], v[220:221] op_sel:[1,1,0] op_sel_hi:[0,1,1] neg_lo:[1,0,0]
	s_nop 0
	v_pk_mul_f32 v[220:221], v[174:175], v[218:219] op_sel_hi:[1,0]
	s_nop 0
	v_pk_fma_f32 v[174:175], v[174:175], v[218:219], v[220:221] op_sel:[1,1,0] op_sel_hi:[0,1,1] neg_hi:[1,0,0]
	v_pk_mul_f32 v[220:221], v[218:219], v[162:163] op_sel_hi:[1,0]
	s_nop 0
	v_pk_fma_f32 v[218:219], v[218:219], v[162:163], v[220:221] op_sel:[1,1,0] op_sel_hi:[0,1,1] neg_lo:[1,0,0]
	s_nop 0
	v_pk_mul_f32 v[220:221], v[166:167], v[218:219] op_sel_hi:[1,0]
	s_nop 0
	v_pk_fma_f32 v[166:167], v[166:167], v[218:219], v[220:221] op_sel:[1,1,0] op_sel_hi:[0,1,1] neg_hi:[1,0,0]
	v_pk_mul_f32 v[220:221], v[218:219], v[162:163] op_sel_hi:[1,0]
	s_nop 0
	v_pk_fma_f32 v[218:219], v[218:219], v[162:163], v[220:221] op_sel:[1,1,0] op_sel_hi:[0,1,1] neg_lo:[1,0,0]
	s_nop 0
	v_pk_mul_f32 v[220:221], v[170:171], v[218:219] op_sel_hi:[1,0]
	s_nop 0
	v_pk_fma_f32 v[170:171], v[170:171], v[218:219], v[220:221] op_sel:[1,1,0] op_sel_hi:[0,1,1] neg_hi:[1,0,0]
	ds_write2_b64 v211, v[164:165], v[172:173] offset1:72
	ds_write2_b64 v211, v[192:193], v[194:195] offset0:144 offset1:216
	ds_write2_b64 v212, v[186:187], v[190:191] offset0:32 offset1:104
	ds_write2_b64 v212, v[184:185], v[188:189] offset0:176 offset1:248
	ds_write2_b64 v213, v[178:179], v[182:183] offset0:64 offset1:136
	ds_write2_b64 v214, v[176:177], v[180:181] offset0:80 offset1:152
	ds_write2_b64 v215, v[168:169], v[174:175] offset0:96 offset1:168
	ds_write2_b64 v216, v[166:167], v[170:171] offset0:112 offset1:184
	s_cbranch_vccnz .LBB0_764
	v_mov_b32_e32 v38, v204
	s_waitcnt lgkmcnt(0)
	s_barrier
	s_cselect_b32 s99, 1, 0
	v_readfirstlane_b32 s98, v0
	s_cmp_lt_u32 s98, 0x100
	s_cbranch_scc1 .Lfft_stg_20082
	s_sleep 8
.Lfft_stg_20082:
	s_cmp_lg_u32 s99, 0
	s_mov_b32 s84, 0
	v_and_b32_e32 v164, 7, v38
	v_cvt_f32_ubyte0_e32 v162, v164
	v_mul_f32_e32 v163, 0x3c800000, v162
	v_cos_f32_e32 v162, v163
	v_sin_f32_e32 v163, v163
	v_lshlrev_b32_e32 v38, 3, v38
	v_lshl_add_u32 v164, v164, 3, 0
.LBB0_766:
	v_add_u32_e32 v165, s84, v38
	v_and_b32_e32 v165, 0xffffffc0, v165
	v_lshlrev_b32_e32 v166, 3, v165
	v_add3_u32 v165, v164, v165, v166
	ds_read2_b64 v[166:169], v165 offset1:9
	ds_read2_b64 v[170:173], v165 offset0:18 offset1:27
	ds_read2_b64 v[174:177], v165 offset0:36 offset1:45
	ds_read2_b64 v[178:181], v165 offset0:54 offset1:63
	s_addk_i32 s84, 0x1000
	s_cmpk_lg_i32 s84, 0x4000
	s_waitcnt lgkmcnt(1)
	v_pk_add_f32 v[182:183], v[166:167], v[174:175]
	v_pk_add_f32 v[166:167], v[166:167], v[174:175] neg_lo:[0,1] neg_hi:[0,1]
	v_pk_add_f32 v[174:175], v[168:169], v[176:177]
	v_pk_add_f32 v[168:169], v[168:169], v[176:177] neg_lo:[0,1] neg_hi:[0,1]
	v_mov_b64_e32 v[176:177], s[6:7]
	v_pk_mul_f32 v[184:185], v[168:169], v[176:177] op_sel_hi:[1,0]
	s_nop 0
	v_pk_fma_f32 v[168:169], v[168:169], v[176:177], v[184:185] op_sel:[1,1,0] op_sel_hi:[0,1,1] neg_hi:[1,0,0]
	s_waitcnt lgkmcnt(0)
	v_pk_add_f32 v[176:177], v[170:171], v[178:179]
	v_pk_add_f32 v[170:171], v[170:171], v[178:179] op_sel:[1,1] op_sel_hi:[0,0] neg_lo:[0,1] neg_hi:[1,0]
	v_pk_add_f32 v[178:179], v[172:173], v[180:181]
	v_pk_add_f32 v[172:173], v[172:173], v[180:181] neg_lo:[0,1] neg_hi:[0,1]
	v_mov_b64_e32 v[180:181], s[14:15]
	v_pk_mul_f32 v[184:185], v[172:173], v[180:181] op_sel_hi:[1,0]
	s_nop 0
	v_pk_fma_f32 v[172:173], v[172:173], v[180:181], v[184:185] op_sel:[1,1,0] op_sel_hi:[0,1,1] neg_hi:[1,0,0]
	v_pk_add_f32 v[180:181], v[182:183], v[176:177]
	v_pk_add_f32 v[176:177], v[182:183], v[176:177] neg_lo:[0,1] neg_hi:[0,1]
	v_pk_add_f32 v[182:183], v[174:175], v[178:179]
	v_pk_add_f32 v[174:175], v[174:175], v[178:179] op_sel:[1,1] op_sel_hi:[0,0] neg_lo:[0,1] neg_hi:[1,0]
	v_pk_add_f32 v[178:179], v[166:167], v[170:171]
	v_pk_add_f32 v[166:167], v[166:167], v[170:171] neg_lo:[0,1] neg_hi:[0,1]
	v_pk_add_f32 v[170:171], v[168:169], v[172:173]
	v_pk_add_f32 v[168:169], v[168:169], v[172:173] op_sel:[1,1] op_sel_hi:[0,0] neg_lo:[0,1] neg_hi:[1,0]
	v_pk_add_f32 v[172:173], v[180:181], v[182:183]
	v_pk_add_f32 v[180:181], v[180:181], v[182:183] neg_lo:[0,1] neg_hi:[0,1]
	v_pk_add_f32 v[182:183], v[176:177], v[174:175]
	v_pk_add_f32 v[174:175], v[176:177], v[174:175] neg_lo:[0,1] neg_hi:[0,1]
	v_pk_add_f32 v[176:177], v[178:179], v[170:171]
	v_pk_add_f32 v[170:171], v[178:179], v[170:171] neg_lo:[0,1] neg_hi:[0,1]
	v_pk_add_f32 v[178:179], v[166:167], v[168:169]
	v_pk_add_f32 v[166:167], v[166:167], v[168:169] neg_lo:[0,1] neg_hi:[0,1]
	v_pk_mul_f32 v[168:169], v[176:177], v[162:163] op_sel_hi:[1,0]
	s_nop 0
	v_pk_fma_f32 v[168:169], v[176:177], v[162:163], v[168:169] op_sel:[1,1,0] op_sel_hi:[0,1,1] neg_hi:[1,0,0]
	v_pk_mul_f32 v[176:177], v[162:163], v[162:163] op_sel_hi:[1,0]
	s_nop 0
	v_pk_fma_f32 v[176:177], v[162:163], v[162:163], v[176:177] op_sel:[1,1,0] op_sel_hi:[0,1,1] neg_lo:[1,0,0]
	s_nop 0
	v_pk_mul_f32 v[184:185], v[182:183], v[176:177] op_sel_hi:[1,0]
	s_nop 0
	v_pk_fma_f32 v[182:183], v[182:183], v[176:177], v[184:185] op_sel:[1,1,0] op_sel_hi:[0,1,1] neg_hi:[1,0,0]
	v_pk_mul_f32 v[184:185], v[176:177], v[162:163] op_sel_hi:[1,0]
	s_nop 0
	v_pk_fma_f32 v[176:177], v[176:177], v[162:163], v[184:185] op_sel:[1,1,0] op_sel_hi:[0,1,1] neg_lo:[1,0,0]
	s_nop 0
	v_pk_mul_f32 v[184:185], v[178:179], v[176:177] op_sel_hi:[1,0]
	s_nop 0
	v_pk_fma_f32 v[178:179], v[178:179], v[176:177], v[184:185] op_sel:[1,1,0] op_sel_hi:[0,1,1] neg_hi:[1,0,0]
	v_pk_mul_f32 v[184:185], v[176:177], v[162:163] op_sel_hi:[1,0]
	s_nop 0
	v_pk_fma_f32 v[176:177], v[176:177], v[162:163], v[184:185] op_sel:[1,1,0] op_sel_hi:[0,1,1] neg_lo:[1,0,0]
	s_nop 0
	v_pk_mul_f32 v[184:185], v[180:181], v[176:177] op_sel_hi:[1,0]
	s_nop 0
	v_pk_fma_f32 v[180:181], v[180:181], v[176:177], v[184:185] op_sel:[1,1,0] op_sel_hi:[0,1,1] neg_hi:[1,0,0]
	v_pk_mul_f32 v[184:185], v[176:177], v[162:163] op_sel_hi:[1,0]
	s_nop 0
	v_pk_fma_f32 v[176:177], v[176:177], v[162:163], v[184:185] op_sel:[1,1,0] op_sel_hi:[0,1,1] neg_lo:[1,0,0]
	s_nop 0
	v_pk_mul_f32 v[184:185], v[170:171], v[176:177] op_sel_hi:[1,0]
	s_nop 0
	v_pk_fma_f32 v[170:171], v[170:171], v[176:177], v[184:185] op_sel:[1,1,0] op_sel_hi:[0,1,1] neg_hi:[1,0,0]
	v_pk_mul_f32 v[184:185], v[176:177], v[162:163] op_sel_hi:[1,0]
	s_nop 0
	v_pk_fma_f32 v[176:177], v[176:177], v[162:163], v[184:185] op_sel:[1,1,0] op_sel_hi:[0,1,1] neg_lo:[1,0,0]
	s_nop 0
	v_pk_mul_f32 v[184:185], v[174:175], v[176:177] op_sel_hi:[1,0]
	s_nop 0
	v_pk_fma_f32 v[174:175], v[174:175], v[176:177], v[184:185] op_sel:[1,1,0] op_sel_hi:[0,1,1] neg_hi:[1,0,0]
	v_pk_mul_f32 v[184:185], v[176:177], v[162:163] op_sel_hi:[1,0]
	s_nop 0
	v_pk_fma_f32 v[176:177], v[176:177], v[162:163], v[184:185] op_sel:[1,1,0] op_sel_hi:[0,1,1] neg_lo:[1,0,0]
	s_nop 0
	v_pk_mul_f32 v[184:185], v[166:167], v[176:177] op_sel_hi:[1,0]
	s_nop 0
	v_pk_fma_f32 v[166:167], v[166:167], v[176:177], v[184:185] op_sel:[1,1,0] op_sel_hi:[0,1,1] neg_hi:[1,0,0]
	ds_write2_b64 v165, v[172:173], v[168:169] offset1:9
	ds_write2_b64 v165, v[182:183], v[178:179] offset0:18 offset1:27
	ds_write2_b64 v165, v[180:181], v[170:171] offset0:36 offset1:45
	ds_write2_b64 v165, v[174:175], v[166:167] offset0:54 offset1:63
	s_cbranch_scc1 .LBB0_766
	v_mov_b32_e32 v38, v204
	s_waitcnt lgkmcnt(0)
	s_barrier
	s_cselect_b32 s99, 1, 0
	v_readfirstlane_b32 s98, v0
	s_cmp_lt_u32 s98, 0x100
	s_cbranch_scc1 .Lfft_stg_20261
	s_sleep 8
.Lfft_stg_20261:
	s_cmp_lg_u32 s99, 0
	s_mov_b32 s84, 0
	v_mul_lo_u32 v38, v38, s33
	v_add_u32_e32 v38, 0, v38
.LBB0_768:
	v_add_u32_e32 v182, s84, v38
	ds_read2_b64 v[162:165], v182 offset1:1
	ds_read2_b64 v[166:169], v182 offset0:2 offset1:3
	ds_read2_b64 v[170:173], v182 offset0:4 offset1:5
	ds_read2_b64 v[174:177], v182 offset0:6 offset1:7
	s_add_i32 s84, s84, 0x9000
	s_cmp_lg_u32 s84, 0x24000
	s_waitcnt lgkmcnt(1)
	v_pk_add_f32 v[178:179], v[162:163], v[170:171]
	v_pk_add_f32 v[162:163], v[162:163], v[170:171] neg_lo:[0,1] neg_hi:[0,1]
	v_pk_add_f32 v[170:171], v[164:165], v[172:173]
	v_pk_add_f32 v[164:165], v[164:165], v[172:173] neg_lo:[0,1] neg_hi:[0,1]
	v_mov_b64_e32 v[172:173], s[6:7]
	v_pk_mul_f32 v[180:181], v[164:165], v[172:173] op_sel_hi:[1,0]
	s_nop 0
	v_pk_fma_f32 v[164:165], v[164:165], v[172:173], v[180:181] op_sel:[1,1,0] op_sel_hi:[0,1,1] neg_hi:[1,0,0]
	s_waitcnt lgkmcnt(0)
	v_pk_add_f32 v[172:173], v[166:167], v[174:175]
	v_pk_add_f32 v[166:167], v[166:167], v[174:175] op_sel:[1,1] op_sel_hi:[0,0] neg_lo:[0,1] neg_hi:[1,0]
	v_pk_add_f32 v[174:175], v[168:169], v[176:177]
	v_pk_add_f32 v[168:169], v[168:169], v[176:177] neg_lo:[0,1] neg_hi:[0,1]
	v_mov_b64_e32 v[176:177], s[14:15]
	v_pk_mul_f32 v[180:181], v[168:169], v[176:177] op_sel_hi:[1,0]
	s_nop 0
	v_pk_fma_f32 v[168:169], v[168:169], v[176:177], v[180:181] op_sel:[1,1,0] op_sel_hi:[0,1,1] neg_hi:[1,0,0]
	v_pk_add_f32 v[176:177], v[178:179], v[172:173]
	v_pk_add_f32 v[172:173], v[178:179], v[172:173] neg_lo:[0,1] neg_hi:[0,1]
	v_pk_add_f32 v[178:179], v[170:171], v[174:175]
	v_pk_add_f32 v[170:171], v[170:171], v[174:175] op_sel:[1,1] op_sel_hi:[0,0] neg_lo:[0,1] neg_hi:[1,0]
	v_pk_add_f32 v[174:175], v[162:163], v[166:167]
	v_pk_add_f32 v[162:163], v[162:163], v[166:167] neg_lo:[0,1] neg_hi:[0,1]
	v_pk_add_f32 v[166:167], v[164:165], v[168:169]
	v_pk_add_f32 v[164:165], v[164:165], v[168:169] op_sel:[1,1] op_sel_hi:[0,0] neg_lo:[0,1] neg_hi:[1,0]
	v_pk_add_f32 v[168:169], v[176:177], v[178:179]
	v_pk_add_f32 v[176:177], v[176:177], v[178:179] neg_lo:[0,1] neg_hi:[0,1]
	v_pk_add_f32 v[178:179], v[172:173], v[170:171]
	v_pk_add_f32 v[170:171], v[172:173], v[170:171] neg_lo:[0,1] neg_hi:[0,1]
	v_pk_add_f32 v[172:173], v[174:175], v[166:167]
	v_pk_add_f32 v[166:167], v[174:175], v[166:167] neg_lo:[0,1] neg_hi:[0,1]
	v_pk_add_f32 v[174:175], v[162:163], v[164:165]
	v_pk_add_f32 v[162:163], v[162:163], v[164:165] neg_lo:[0,1] neg_hi:[0,1]
	ds_write2_b64 v182, v[168:169], v[172:173] offset1:1
	ds_write2_b64 v182, v[178:179], v[174:175] offset0:2 offset1:3
	ds_write2_b64 v182, v[176:177], v[166:167] offset0:4 offset1:5
	ds_write2_b64 v182, v[170:171], v[162:163] offset0:6 offset1:7
	s_cbranch_scc1 .LBB0_768
	s_waitcnt lgkmcnt(0)
	s_barrier
	s_cselect_b32 s99, 1, 0
	v_readfirstlane_b32 s98, v0
	s_cmp_lt_u32 s98, 0x100
	s_cbranch_scc1 .Lfft_stg_20334
	s_sleep 8
.Lfft_stg_20334:
	s_cmp_lg_u32 s99, 0
	s_nop 0
	v_cvt_f32_i32_e32 v38, v209
	v_lshlrev_b32_e32 v165, 2, v209
	v_lshrrev_b32_e32 v166, 5, v209
	v_ashrrev_i32_e32 v167, 11, v209
	v_mul_f32_e32 v38, 0x38800000, v38
	v_cos_f32_e32 v163, v38
	v_sin_f32_e32 v162, v38
	v_lshlrev_b32_e32 v38, 10, v209
	v_sub_u32_e32 v164, 0, v209
	v_and_b32_e32 v38, 0x3c00, v38
	v_and_b32_e32 v166, 56, v166
	v_and_or_b32 v165, v165, s9, v167
	v_or3_b32 v38, v165, v38, v166
	v_lshlrev_b32_e32 v165, 10, v164
	v_lshlrev_b32_e32 v166, 2, v164
	v_lshrrev_b32_e32 v167, 5, v164
	v_bfe_u32 v164, v164, 11, 3
	v_and_b32_e32 v165, 0x3c00, v165
	v_and_b32_e32 v166, 0x3c0, v166
	v_and_or_b32 v164, v167, 56, v164
	v_mul_i32_i24_e32 v38, 9, v38
	v_or3_b32 v164, v164, v166, v165
	v_and_b32_e32 v38, -8, v38
	v_mul_u32_u24_e32 v164, 9, v164
	v_add_u32_e32 v38, 0, v38
	v_and_b32_e32 v164, 0x3fff8, v164
	v_add_u32_e32 v176, 0, v164
	ds_read_b64 v[164:165], v38
	ds_read_b64 v[166:167], v176
	v_pk_fma_f32 v[168:169], v[162:163], 0, v[162:163] op_sel:[0,0,1] op_sel_hi:[1,0,0] neg_lo:[1,0,0] neg_hi:[1,0,0]
	v_pk_fma_f32 v[170:171], v[162:163], 0, v[162:163] op_sel:[0,0,1] op_sel_hi:[1,0,0]
	s_nop 0
	v_mov_b32_e32 v169, v171
	s_waitcnt lgkmcnt(0)
	v_pk_add_f32 v[170:171], v[164:165], v[166:167] neg_hi:[0,1]
	v_pk_add_f32 v[164:165], v[164:165], v[166:167] op_sel:[1,1] op_sel_hi:[0,0] neg_hi:[1,0]
	v_pk_add_f32 v[166:167], v[158:159], v[160:161] neg_hi:[0,1]
	v_pk_add_f32 v[158:159], v[158:159], v[160:161] op_sel:[1,1] op_sel_hi:[0,0] neg_hi:[1,0]
	s_nop 0
	v_pk_mul_f32 v[160:161], v[170:171], v[166:167] op_sel_hi:[1,0]
	v_pk_mul_f32 v[172:173], v[164:165], v[158:159] op_sel_hi:[1,0]
	s_nop 0
	v_pk_fma_f32 v[160:161], v[170:171], v[166:167], v[160:161] op_sel:[1,1,0] op_sel_hi:[0,1,1] neg_lo:[1,0,0]
	v_pk_fma_f32 v[172:173], v[164:165], v[158:159], v[172:173] op_sel:[1,1,0] op_sel_hi:[0,1,1] neg_lo:[1,0,0]
	s_nop 0
	v_pk_mul_f32 v[174:175], v[172:173], v[168:169] op_sel_hi:[1,0]
	s_nop 0
	v_pk_fma_f32 v[168:169], v[172:173], v[168:169], v[174:175] op_sel:[1,1,0] op_sel_hi:[0,1,1] neg_hi:[1,0,0]
	s_nop 0
	v_pk_add_f32 v[160:161], v[160:161], v[168:169]
	v_pk_mul_f32 v[168:169], v[170:171], v[158:159] op_sel_hi:[1,0]
	s_nop 0
	v_pk_fma_f32 v[158:159], v[170:171], v[158:159], v[168:169] op_sel:[1,1,0] op_sel_hi:[0,1,1] neg_lo:[1,0,0]
	v_pk_mul_f32 v[168:169], v[164:165], v[166:167] op_sel_hi:[1,0]
	s_nop 0
	v_pk_fma_f32 v[164:165], v[164:165], v[166:167], v[168:169] op_sel:[1,1,0] op_sel_hi:[0,1,1] neg_lo:[1,0,0]
	s_nop 0
	v_pk_add_f32 v[158:159], v[158:159], v[164:165]
	s_nop 0
	v_pk_add_f32 v[164:165], v[160:161], v[158:159] op_sel:[0,1] op_sel_hi:[1,0] neg_lo:[0,1]
	v_pk_add_f32 v[158:159], v[160:161], v[158:159] op_sel:[0,1] op_sel_hi:[1,0] neg_hi:[1,0]
	ds_write_b64 v38, v[164:165]
	ds_write_b64 v176, v[158:159]
	v_add_u32_e32 v158, 1, v209
	v_lshlrev_b32_e32 v164, 10, v158
	v_lshlrev_b32_e32 v165, 2, v158
	v_lshrrev_b32_e32 v166, 5, v158
	v_ashrrev_i32_e32 v158, 11, v158
	v_and_b32_e32 v164, 0x3c00, v164
	v_and_b32_e32 v166, 56, v166
	v_and_or_b32 v158, v165, s9, v158
	v_or3_b32 v158, v158, v164, v166
	v_mul_i32_i24_e32 v158, 9, v158
	v_not_b32_e32 v159, v209
	v_and_b32_e32 v158, -8, v158
	v_add_u32_e32 v174, 0, v158
	v_lshlrev_b32_e32 v158, 10, v159
	v_lshlrev_b32_e32 v164, 2, v159
	v_lshrrev_b32_e32 v165, 5, v159
	v_bfe_u32 v159, v159, 11, 3
	v_and_b32_e32 v158, 0x3c00, v158
	v_and_b32_e32 v164, 0x3c0, v164
	v_and_or_b32 v159, v165, 56, v159
	v_or3_b32 v158, v159, v164, v158
	v_mul_u32_u24_e32 v158, 9, v158
	v_and_b32_e32 v158, 0x3fff8, v158
	v_add_u32_e32 v159, 0, v158
	ds_read_b64 v[164:165], v159
	ds_read_b64 v[166:167], v174
	v_pk_mul_f32 v[160:161], v[162:163], s[20:21] op_sel_hi:[0,1]
	v_mov_b32_e32 v38, v163
	v_mov_b32_e32 v158, v163
	v_pk_fma_f32 v[168:169], v[38:39], s[22:23], v[160:161] neg_lo:[0,0,1] neg_hi:[0,0,1]
	v_pk_fma_f32 v[160:161], v[158:159], s[22:23], v[160:161] op_sel_hi:[0,1,1]
	v_mov_b32_e32 v169, v161
	s_waitcnt lgkmcnt(0)
	v_pk_add_f32 v[160:161], v[166:167], v[164:165] neg_hi:[0,1]
	v_pk_add_f32 v[164:165], v[166:167], v[164:165] op_sel:[1,1] op_sel_hi:[0,0] neg_hi:[1,0]
	v_pk_add_f32 v[166:167], v[154:155], v[156:157] neg_hi:[0,1]
	v_pk_add_f32 v[154:155], v[154:155], v[156:157] op_sel:[1,1] op_sel_hi:[0,0] neg_hi:[1,0]
	s_nop 0
	v_pk_mul_f32 v[156:157], v[160:161], v[166:167] op_sel_hi:[1,0]
	v_pk_mul_f32 v[170:171], v[164:165], v[154:155] op_sel_hi:[1,0]
	s_nop 0
	v_pk_fma_f32 v[156:157], v[160:161], v[166:167], v[156:157] op_sel:[1,1,0] op_sel_hi:[0,1,1] neg_lo:[1,0,0]
	v_pk_fma_f32 v[170:171], v[164:165], v[154:155], v[170:171] op_sel:[1,1,0] op_sel_hi:[0,1,1] neg_lo:[1,0,0]
	s_nop 0
	v_pk_mul_f32 v[172:173], v[170:171], v[168:169] op_sel_hi:[1,0]
	s_nop 0
	v_pk_fma_f32 v[168:169], v[170:171], v[168:169], v[172:173] op_sel:[1,1,0] op_sel_hi:[0,1,1] neg_hi:[1,0,0]
	s_nop 0
	v_pk_add_f32 v[156:157], v[156:157], v[168:169]
	v_pk_mul_f32 v[168:169], v[160:161], v[154:155] op_sel_hi:[1,0]
	s_nop 0
	v_pk_fma_f32 v[154:155], v[160:161], v[154:155], v[168:169] op_sel:[1,1,0] op_sel_hi:[0,1,1] neg_lo:[1,0,0]
	v_pk_mul_f32 v[160:161], v[164:165], v[166:167] op_sel_hi:[1,0]
	s_nop 0
	v_pk_fma_f32 v[160:161], v[164:165], v[166:167], v[160:161] op_sel:[1,1,0] op_sel_hi:[0,1,1] neg_lo:[1,0,0]
	s_nop 0
	v_pk_add_f32 v[154:155], v[154:155], v[160:161]
	s_nop 0
	v_pk_add_f32 v[160:161], v[156:157], v[154:155] op_sel:[0,1] op_sel_hi:[1,0] neg_lo:[0,1]
	v_pk_add_f32 v[154:155], v[156:157], v[154:155] op_sel:[0,1] op_sel_hi:[1,0] neg_hi:[1,0]
	ds_write_b64 v174, v[160:161]
	ds_write_b64 v159, v[154:155]
	v_add_u32_e32 v154, 2, v209
	v_lshlrev_b32_e32 v156, 10, v154
	v_lshlrev_b32_e32 v157, 2, v154
	v_lshrrev_b32_e32 v159, 5, v154
	v_ashrrev_i32_e32 v154, 11, v154
	v_and_b32_e32 v156, 0x3c00, v156
	v_and_b32_e32 v159, 56, v159
	v_and_or_b32 v154, v157, s9, v154
	v_or3_b32 v154, v154, v156, v159
	v_mul_i32_i24_e32 v154, 9, v154
	v_sub_u32_e32 v155, -2, v209
	v_and_b32_e32 v154, -8, v154
	v_add_u32_e32 v159, 0, v154
	v_lshlrev_b32_e32 v154, 10, v155
	v_lshlrev_b32_e32 v156, 2, v155
	v_lshrrev_b32_e32 v157, 5, v155
	v_bfe_u32 v155, v155, 11, 3
	v_and_b32_e32 v154, 0x3c00, v154
	v_and_b32_e32 v156, 0x3c0, v156
	v_and_or_b32 v155, v157, 56, v155
	v_or3_b32 v154, v155, v156, v154
	v_mul_u32_u24_e32 v154, 9, v154
	v_and_b32_e32 v154, 0x3fff8, v154
	v_add_u32_e32 v163, 0, v154
	ds_read_b64 v[154:155], v159
	ds_read_b64 v[156:157], v163
	v_pk_mul_f32 v[160:161], v[162:163], s[24:25] op_sel_hi:[0,1]
	v_pk_fma_f32 v[164:165], v[38:39], s[26:27], v[160:161] neg_lo:[0,0,1] neg_hi:[0,0,1]
	v_pk_fma_f32 v[160:161], v[158:159], s[26:27], v[160:161] op_sel_hi:[0,1,1]
	v_mov_b32_e32 v165, v161
	s_waitcnt lgkmcnt(0)
	v_pk_add_f32 v[160:161], v[154:155], v[156:157] neg_hi:[0,1]
	v_pk_add_f32 v[154:155], v[154:155], v[156:157] op_sel:[1,1] op_sel_hi:[0,0] neg_hi:[1,0]
	v_pk_add_f32 v[156:157], v[150:151], v[152:153] neg_hi:[0,1]
	v_pk_add_f32 v[150:151], v[150:151], v[152:153] op_sel:[1,1] op_sel_hi:[0,0] neg_hi:[1,0]
	s_nop 0
	v_pk_mul_f32 v[152:153], v[160:161], v[156:157] op_sel_hi:[1,0]
	v_pk_mul_f32 v[166:167], v[154:155], v[150:151] op_sel_hi:[1,0]
	s_nop 0
	v_pk_fma_f32 v[152:153], v[160:161], v[156:157], v[152:153] op_sel:[1,1,0] op_sel_hi:[0,1,1] neg_lo:[1,0,0]
	v_pk_fma_f32 v[166:167], v[154:155], v[150:151], v[166:167] op_sel:[1,1,0] op_sel_hi:[0,1,1] neg_lo:[1,0,0]
	s_nop 0
	v_pk_mul_f32 v[168:169], v[166:167], v[164:165] op_sel_hi:[1,0]
	s_nop 0
	v_pk_fma_f32 v[164:165], v[166:167], v[164:165], v[168:169] op_sel:[1,1,0] op_sel_hi:[0,1,1] neg_hi:[1,0,0]
	s_nop 0
	v_pk_add_f32 v[152:153], v[152:153], v[164:165]
	v_pk_mul_f32 v[164:165], v[160:161], v[150:151] op_sel_hi:[1,0]
	s_nop 0
	v_pk_fma_f32 v[150:151], v[160:161], v[150:151], v[164:165] op_sel:[1,1,0] op_sel_hi:[0,1,1] neg_lo:[1,0,0]
	v_pk_mul_f32 v[160:161], v[154:155], v[156:157] op_sel_hi:[1,0]
	s_nop 0
	v_pk_fma_f32 v[154:155], v[154:155], v[156:157], v[160:161] op_sel:[1,1,0] op_sel_hi:[0,1,1] neg_lo:[1,0,0]
	s_nop 0
	v_pk_add_f32 v[150:151], v[150:151], v[154:155]
	s_nop 0
	v_pk_add_f32 v[154:155], v[152:153], v[150:151] op_sel:[0,1] op_sel_hi:[1,0] neg_lo:[0,1]
	v_pk_add_f32 v[150:151], v[152:153], v[150:151] op_sel:[0,1] op_sel_hi:[1,0] neg_hi:[1,0]
	ds_write_b64 v159, v[154:155]
	ds_write_b64 v163, v[150:151]
	v_add_u32_e32 v150, 3, v209
	v_lshlrev_b32_e32 v152, 10, v150
	v_lshlrev_b32_e32 v153, 2, v150
	v_lshrrev_b32_e32 v154, 5, v150
	v_ashrrev_i32_e32 v150, 11, v150
	v_and_b32_e32 v152, 0x3c00, v152
	v_and_b32_e32 v154, 56, v154
	v_and_or_b32 v150, v153, s9, v150
	v_or3_b32 v150, v150, v152, v154
	v_mul_i32_i24_e32 v150, 9, v150
	v_sub_u32_e32 v151, -3, v209
	v_and_b32_e32 v150, -8, v150
	v_add_u32_e32 v159, 0, v150
	v_lshlrev_b32_e32 v150, 10, v151
	v_lshlrev_b32_e32 v152, 2, v151
	v_lshrrev_b32_e32 v153, 5, v151
	v_bfe_u32 v151, v151, 11, 3
	v_and_b32_e32 v150, 0x3c00, v150
	v_and_b32_e32 v152, 0x3c0, v152
	v_and_or_b32 v151, v153, 56, v151
	v_or3_b32 v150, v151, v152, v150
	v_mul_u32_u24_e32 v150, 9, v150
	v_and_b32_e32 v150, 0x3fff8, v150
	v_add_u32_e32 v163, 0, v150
	ds_read_b64 v[150:151], v159
	ds_read_b64 v[152:153], v163
	v_pk_mul_f32 v[154:155], v[162:163], s[28:29] op_sel_hi:[0,1]
	v_pk_fma_f32 v[156:157], v[38:39], s[30:31], v[154:155] neg_lo:[0,0,1] neg_hi:[0,0,1]
	v_pk_fma_f32 v[154:155], v[158:159], s[30:31], v[154:155] op_sel_hi:[0,1,1]
	v_mov_b32_e32 v157, v155
	s_waitcnt lgkmcnt(0)
	v_pk_add_f32 v[154:155], v[150:151], v[152:153] neg_hi:[0,1]
	v_pk_add_f32 v[150:151], v[150:151], v[152:153] op_sel:[1,1] op_sel_hi:[0,0] neg_hi:[1,0]
	v_pk_add_f32 v[152:153], v[146:147], v[148:149] neg_hi:[0,1]
	v_pk_add_f32 v[146:147], v[146:147], v[148:149] op_sel:[1,1] op_sel_hi:[0,0] neg_hi:[1,0]
	s_nop 0
	v_pk_mul_f32 v[148:149], v[154:155], v[152:153] op_sel_hi:[1,0]
	v_pk_mul_f32 v[160:161], v[150:151], v[146:147] op_sel_hi:[1,0]
	s_nop 0
	v_pk_fma_f32 v[148:149], v[154:155], v[152:153], v[148:149] op_sel:[1,1,0] op_sel_hi:[0,1,1] neg_lo:[1,0,0]
	v_pk_fma_f32 v[160:161], v[150:151], v[146:147], v[160:161] op_sel:[1,1,0] op_sel_hi:[0,1,1] neg_lo:[1,0,0]
	s_nop 0
	v_pk_mul_f32 v[164:165], v[160:161], v[156:157] op_sel_hi:[1,0]
	s_nop 0
	v_pk_fma_f32 v[156:157], v[160:161], v[156:157], v[164:165] op_sel:[1,1,0] op_sel_hi:[0,1,1] neg_hi:[1,0,0]
	s_nop 0
	v_pk_add_f32 v[148:149], v[148:149], v[156:157]
	v_pk_mul_f32 v[156:157], v[154:155], v[146:147] op_sel_hi:[1,0]
	s_nop 0
	v_pk_fma_f32 v[146:147], v[154:155], v[146:147], v[156:157] op_sel:[1,1,0] op_sel_hi:[0,1,1] neg_lo:[1,0,0]
	v_pk_mul_f32 v[154:155], v[150:151], v[152:153] op_sel_hi:[1,0]
	s_nop 0
	v_pk_fma_f32 v[150:151], v[150:151], v[152:153], v[154:155] op_sel:[1,1,0] op_sel_hi:[0,1,1] neg_lo:[1,0,0]
	s_nop 0
	v_pk_add_f32 v[146:147], v[146:147], v[150:151]
	s_nop 0
	v_pk_add_f32 v[150:151], v[148:149], v[146:147] op_sel:[0,1] op_sel_hi:[1,0] neg_lo:[0,1]
	v_pk_add_f32 v[146:147], v[148:149], v[146:147] op_sel:[0,1] op_sel_hi:[1,0] neg_hi:[1,0]
	ds_write_b64 v159, v[150:151]
	ds_write_b64 v163, v[146:147]
	v_add_u32_e32 v146, 4, v209
	v_lshlrev_b32_e32 v148, 10, v146
	v_lshlrev_b32_e32 v149, 2, v146
	v_lshrrev_b32_e32 v150, 5, v146
	v_ashrrev_i32_e32 v146, 11, v146
	v_and_b32_e32 v148, 0x3c00, v148
	v_and_b32_e32 v150, 56, v150
	v_and_or_b32 v146, v149, s9, v146
	v_or3_b32 v146, v146, v148, v150
	v_mul_i32_i24_e32 v146, 9, v146
	v_sub_u32_e32 v147, -4, v209
	v_and_b32_e32 v146, -8, v146
	v_add_u32_e32 v159, 0, v146
	v_lshlrev_b32_e32 v146, 10, v147
	v_lshlrev_b32_e32 v148, 2, v147
	v_lshrrev_b32_e32 v149, 5, v147
	v_bfe_u32 v147, v147, 11, 3
	v_and_b32_e32 v146, 0x3c00, v146
	v_and_b32_e32 v148, 0x3c0, v148
	v_and_or_b32 v147, v149, 56, v147
	v_or3_b32 v146, v147, v148, v146
	v_mul_u32_u24_e32 v146, 9, v146
	v_and_b32_e32 v146, 0x3fff8, v146
	v_add_u32_e32 v160, 0, v146
	ds_read_b64 v[146:147], v159
	ds_read_b64 v[148:149], v160
	v_pk_mul_f32 v[150:151], v[162:163], s[34:35] op_sel_hi:[0,1]
	v_pk_fma_f32 v[152:153], v[38:39], s[36:37], v[150:151] neg_lo:[0,0,1] neg_hi:[0,0,1]
	v_pk_fma_f32 v[150:151], v[158:159], s[36:37], v[150:151] op_sel_hi:[0,1,1]
	v_mov_b32_e32 v153, v151
	s_waitcnt lgkmcnt(0)
	v_pk_add_f32 v[150:151], v[146:147], v[148:149] neg_hi:[0,1]
	v_pk_add_f32 v[146:147], v[146:147], v[148:149] op_sel:[1,1] op_sel_hi:[0,0] neg_hi:[1,0]
	v_pk_add_f32 v[148:149], v[142:143], v[144:145] neg_hi:[0,1]
	v_pk_add_f32 v[142:143], v[142:143], v[144:145] op_sel:[1,1] op_sel_hi:[0,0] neg_hi:[1,0]
	s_nop 0
	v_pk_mul_f32 v[144:145], v[150:151], v[148:149] op_sel_hi:[1,0]
	v_pk_mul_f32 v[154:155], v[146:147], v[142:143] op_sel_hi:[1,0]
	s_nop 0
	v_pk_fma_f32 v[144:145], v[150:151], v[148:149], v[144:145] op_sel:[1,1,0] op_sel_hi:[0,1,1] neg_lo:[1,0,0]
	v_pk_fma_f32 v[154:155], v[146:147], v[142:143], v[154:155] op_sel:[1,1,0] op_sel_hi:[0,1,1] neg_lo:[1,0,0]
	s_nop 0
	v_pk_mul_f32 v[156:157], v[154:155], v[152:153] op_sel_hi:[1,0]
	s_nop 0
	v_pk_fma_f32 v[152:153], v[154:155], v[152:153], v[156:157] op_sel:[1,1,0] op_sel_hi:[0,1,1] neg_hi:[1,0,0]
	s_nop 0
	v_pk_add_f32 v[144:145], v[144:145], v[152:153]
	v_pk_mul_f32 v[152:153], v[150:151], v[142:143] op_sel_hi:[1,0]
	s_nop 0
	v_pk_fma_f32 v[142:143], v[150:151], v[142:143], v[152:153] op_sel:[1,1,0] op_sel_hi:[0,1,1] neg_lo:[1,0,0]
	v_pk_mul_f32 v[150:151], v[146:147], v[148:149] op_sel_hi:[1,0]
	s_nop 0
	v_pk_fma_f32 v[146:147], v[146:147], v[148:149], v[150:151] op_sel:[1,1,0] op_sel_hi:[0,1,1] neg_lo:[1,0,0]
	s_nop 0
	v_pk_add_f32 v[142:143], v[142:143], v[146:147]
	s_nop 0
	v_pk_add_f32 v[146:147], v[144:145], v[142:143] op_sel:[0,1] op_sel_hi:[1,0] neg_lo:[0,1]
	v_pk_add_f32 v[142:143], v[144:145], v[142:143] op_sel:[0,1] op_sel_hi:[1,0] neg_hi:[1,0]
	ds_write_b64 v159, v[146:147]
	ds_write_b64 v160, v[142:143]
	v_add_u32_e32 v142, 5, v209
	v_lshlrev_b32_e32 v144, 10, v142
	v_lshlrev_b32_e32 v145, 2, v142
	v_lshrrev_b32_e32 v146, 5, v142
	v_ashrrev_i32_e32 v142, 11, v142
	v_and_b32_e32 v144, 0x3c00, v144
	v_and_b32_e32 v146, 56, v146
	v_and_or_b32 v142, v145, s9, v142
	v_or3_b32 v142, v142, v144, v146
	v_mul_i32_i24_e32 v142, 9, v142
	v_sub_u32_e32 v143, -5, v209
	v_and_b32_e32 v142, -8, v142
	v_add_u32_e32 v154, 0, v142
	v_lshlrev_b32_e32 v142, 10, v143
	v_lshlrev_b32_e32 v144, 2, v143
	v_lshrrev_b32_e32 v145, 5, v143
	v_bfe_u32 v143, v143, 11, 3
	v_and_b32_e32 v142, 0x3c00, v142
	v_and_b32_e32 v144, 0x3c0, v144
	v_and_or_b32 v143, v145, 56, v143
	v_or3_b32 v142, v143, v144, v142
	v_mul_u32_u24_e32 v142, 9, v142
	v_and_b32_e32 v142, 0x3fff8, v142
	v_add_u32_e32 v155, 0, v142
	ds_read_b64 v[142:143], v154
	ds_read_b64 v[144:145], v155
	v_pk_mul_f32 v[146:147], v[162:163], s[38:39] op_sel_hi:[0,1]
	v_pk_fma_f32 v[148:149], v[38:39], s[40:41], v[146:147] neg_lo:[0,0,1] neg_hi:[0,0,1]
	v_pk_fma_f32 v[146:147], v[158:159], s[40:41], v[146:147] op_sel_hi:[0,1,1]
	v_mov_b32_e32 v149, v147
	s_waitcnt lgkmcnt(0)
	v_pk_add_f32 v[146:147], v[142:143], v[144:145] neg_hi:[0,1]
	v_pk_add_f32 v[142:143], v[142:143], v[144:145] op_sel:[1,1] op_sel_hi:[0,0] neg_hi:[1,0]
	v_pk_add_f32 v[144:145], v[138:139], v[140:141] neg_hi:[0,1]
	v_pk_add_f32 v[138:139], v[138:139], v[140:141] op_sel:[1,1] op_sel_hi:[0,0] neg_hi:[1,0]
	s_nop 0
	v_pk_mul_f32 v[140:141], v[146:147], v[144:145] op_sel_hi:[1,0]
	v_pk_mul_f32 v[150:151], v[142:143], v[138:139] op_sel_hi:[1,0]
	s_nop 0
	v_pk_fma_f32 v[140:141], v[146:147], v[144:145], v[140:141] op_sel:[1,1,0] op_sel_hi:[0,1,1] neg_lo:[1,0,0]
	v_pk_fma_f32 v[150:151], v[142:143], v[138:139], v[150:151] op_sel:[1,1,0] op_sel_hi:[0,1,1] neg_lo:[1,0,0]
	s_nop 0
	v_pk_mul_f32 v[152:153], v[150:151], v[148:149] op_sel_hi:[1,0]
	s_nop 0
	v_pk_fma_f32 v[148:149], v[150:151], v[148:149], v[152:153] op_sel:[1,1,0] op_sel_hi:[0,1,1] neg_hi:[1,0,0]
	s_nop 0
	v_pk_add_f32 v[140:141], v[140:141], v[148:149]
	v_pk_mul_f32 v[148:149], v[146:147], v[138:139] op_sel_hi:[1,0]
	s_nop 0
	v_pk_fma_f32 v[138:139], v[146:147], v[138:139], v[148:149] op_sel:[1,1,0] op_sel_hi:[0,1,1] neg_lo:[1,0,0]
	v_pk_mul_f32 v[146:147], v[142:143], v[144:145] op_sel_hi:[1,0]
	s_nop 0
	v_pk_fma_f32 v[142:143], v[142:143], v[144:145], v[146:147] op_sel:[1,1,0] op_sel_hi:[0,1,1] neg_lo:[1,0,0]
	s_nop 0
	v_pk_add_f32 v[138:139], v[138:139], v[142:143]
	s_nop 0
	v_pk_add_f32 v[142:143], v[140:141], v[138:139] op_sel:[0,1] op_sel_hi:[1,0] neg_lo:[0,1]
	v_pk_add_f32 v[138:139], v[140:141], v[138:139] op_sel:[0,1] op_sel_hi:[1,0] neg_hi:[1,0]
	ds_write_b64 v154, v[142:143]
	ds_write_b64 v155, v[138:139]
	v_add_u32_e32 v138, 6, v209
	v_lshlrev_b32_e32 v140, 10, v138
	v_lshlrev_b32_e32 v141, 2, v138
	v_lshrrev_b32_e32 v142, 5, v138
	v_ashrrev_i32_e32 v138, 11, v138
	v_and_b32_e32 v140, 0x3c00, v140
	v_and_b32_e32 v142, 56, v142
	v_and_or_b32 v138, v141, s9, v138
	v_or3_b32 v138, v138, v140, v142
	v_mul_i32_i24_e32 v138, 9, v138
	v_sub_u32_e32 v139, -6, v209
	v_and_b32_e32 v138, -8, v138
	v_add_u32_e32 v150, 0, v138
	v_lshlrev_b32_e32 v138, 10, v139
	v_lshlrev_b32_e32 v140, 2, v139
	v_lshrrev_b32_e32 v141, 5, v139
	v_bfe_u32 v139, v139, 11, 3
	v_and_b32_e32 v138, 0x3c00, v138
	v_and_b32_e32 v140, 0x3c0, v140
	v_and_or_b32 v139, v141, 56, v139
	v_or3_b32 v138, v139, v140, v138
	v_mul_u32_u24_e32 v138, 9, v138
	v_and_b32_e32 v138, 0x3fff8, v138
	v_add_u32_e32 v151, 0, v138
	ds_read_b64 v[138:139], v150
	ds_read_b64 v[140:141], v151
	v_pk_mul_f32 v[142:143], v[162:163], s[42:43] op_sel_hi:[0,1]
	v_pk_fma_f32 v[144:145], v[38:39], s[44:45], v[142:143] neg_lo:[0,0,1] neg_hi:[0,0,1]
	v_pk_fma_f32 v[142:143], v[158:159], s[44:45], v[142:143] op_sel_hi:[0,1,1]
	v_mov_b32_e32 v145, v143
	s_waitcnt lgkmcnt(0)
	v_pk_add_f32 v[142:143], v[138:139], v[140:141] neg_hi:[0,1]
	v_pk_add_f32 v[138:139], v[138:139], v[140:141] op_sel:[1,1] op_sel_hi:[0,0] neg_hi:[1,0]
	v_pk_add_f32 v[140:141], v[134:135], v[136:137] neg_hi:[0,1]
	v_pk_add_f32 v[134:135], v[134:135], v[136:137] op_sel:[1,1] op_sel_hi:[0,0] neg_hi:[1,0]
	s_nop 0
	v_pk_mul_f32 v[136:137], v[142:143], v[140:141] op_sel_hi:[1,0]
	v_pk_mul_f32 v[146:147], v[138:139], v[134:135] op_sel_hi:[1,0]
	s_nop 0
	v_pk_fma_f32 v[136:137], v[142:143], v[140:141], v[136:137] op_sel:[1,1,0] op_sel_hi:[0,1,1] neg_lo:[1,0,0]
	v_pk_fma_f32 v[146:147], v[138:139], v[134:135], v[146:147] op_sel:[1,1,0] op_sel_hi:[0,1,1] neg_lo:[1,0,0]
	s_nop 0
	v_pk_mul_f32 v[148:149], v[146:147], v[144:145] op_sel_hi:[1,0]
	s_nop 0
	v_pk_fma_f32 v[144:145], v[146:147], v[144:145], v[148:149] op_sel:[1,1,0] op_sel_hi:[0,1,1] neg_hi:[1,0,0]
	s_nop 0
	v_pk_add_f32 v[136:137], v[136:137], v[144:145]
	v_pk_mul_f32 v[144:145], v[142:143], v[134:135] op_sel_hi:[1,0]
	s_nop 0
	v_pk_fma_f32 v[134:135], v[142:143], v[134:135], v[144:145] op_sel:[1,1,0] op_sel_hi:[0,1,1] neg_lo:[1,0,0]
	v_pk_mul_f32 v[142:143], v[138:139], v[140:141] op_sel_hi:[1,0]
	s_nop 0
	v_pk_fma_f32 v[138:139], v[138:139], v[140:141], v[142:143] op_sel:[1,1,0] op_sel_hi:[0,1,1] neg_lo:[1,0,0]
	s_nop 0
	v_pk_add_f32 v[134:135], v[134:135], v[138:139]
	s_nop 0
	v_pk_add_f32 v[138:139], v[136:137], v[134:135] op_sel:[0,1] op_sel_hi:[1,0] neg_lo:[0,1]
	v_pk_add_f32 v[134:135], v[136:137], v[134:135] op_sel:[0,1] op_sel_hi:[1,0] neg_hi:[1,0]
	ds_write_b64 v150, v[138:139]
	ds_write_b64 v151, v[134:135]
	v_add_u32_e32 v134, 7, v209
	v_lshlrev_b32_e32 v136, 10, v134
	v_lshlrev_b32_e32 v137, 2, v134
	v_lshrrev_b32_e32 v138, 5, v134
	v_ashrrev_i32_e32 v134, 11, v134
	v_and_b32_e32 v136, 0x3c00, v136
	v_and_b32_e32 v138, 56, v138
	v_and_or_b32 v134, v137, s9, v134
	v_or3_b32 v134, v134, v136, v138
	v_mul_i32_i24_e32 v134, 9, v134
	v_sub_u32_e32 v135, -7, v209
	v_and_b32_e32 v134, -8, v134
	v_add_u32_e32 v146, 0, v134
	v_lshlrev_b32_e32 v134, 10, v135
	v_lshlrev_b32_e32 v136, 2, v135
	v_lshrrev_b32_e32 v137, 5, v135
	v_bfe_u32 v135, v135, 11, 3
	v_and_b32_e32 v134, 0x3c00, v134
	v_and_b32_e32 v136, 0x3c0, v136
	v_and_or_b32 v135, v137, 56, v135
	v_or3_b32 v134, v135, v136, v134
	v_mul_u32_u24_e32 v134, 9, v134
	v_and_b32_e32 v134, 0x3fff8, v134
	v_add_u32_e32 v147, 0, v134
	ds_read_b64 v[134:135], v146
	ds_read_b64 v[136:137], v147
	v_pk_mul_f32 v[138:139], v[162:163], s[46:47] op_sel_hi:[0,1]
	v_pk_fma_f32 v[140:141], v[38:39], s[48:49], v[138:139] neg_lo:[0,0,1] neg_hi:[0,0,1]
	v_pk_fma_f32 v[138:139], v[158:159], s[48:49], v[138:139] op_sel_hi:[0,1,1]
	v_mov_b32_e32 v141, v139
	s_waitcnt lgkmcnt(0)
	v_pk_add_f32 v[138:139], v[134:135], v[136:137] neg_hi:[0,1]
	v_pk_add_f32 v[134:135], v[134:135], v[136:137] op_sel:[1,1] op_sel_hi:[0,0] neg_hi:[1,0]
	v_pk_add_f32 v[136:137], v[130:131], v[132:133] neg_hi:[0,1]
	v_pk_add_f32 v[130:131], v[130:131], v[132:133] op_sel:[1,1] op_sel_hi:[0,0] neg_hi:[1,0]
	s_nop 0
	v_pk_mul_f32 v[132:133], v[138:139], v[136:137] op_sel_hi:[1,0]
	v_pk_mul_f32 v[142:143], v[134:135], v[130:131] op_sel_hi:[1,0]
	s_nop 0
	v_pk_fma_f32 v[132:133], v[138:139], v[136:137], v[132:133] op_sel:[1,1,0] op_sel_hi:[0,1,1] neg_lo:[1,0,0]
	v_pk_fma_f32 v[142:143], v[134:135], v[130:131], v[142:143] op_sel:[1,1,0] op_sel_hi:[0,1,1] neg_lo:[1,0,0]
	s_nop 0
	v_pk_mul_f32 v[144:145], v[142:143], v[140:141] op_sel_hi:[1,0]
	s_nop 0
	v_pk_fma_f32 v[140:141], v[142:143], v[140:141], v[144:145] op_sel:[1,1,0] op_sel_hi:[0,1,1] neg_hi:[1,0,0]
	s_nop 0
	v_pk_add_f32 v[132:133], v[132:133], v[140:141]
	v_pk_mul_f32 v[140:141], v[138:139], v[130:131] op_sel_hi:[1,0]
	s_nop 0
	v_pk_fma_f32 v[130:131], v[138:139], v[130:131], v[140:141] op_sel:[1,1,0] op_sel_hi:[0,1,1] neg_lo:[1,0,0]
	v_pk_mul_f32 v[138:139], v[134:135], v[136:137] op_sel_hi:[1,0]
	s_nop 0
	v_pk_fma_f32 v[134:135], v[134:135], v[136:137], v[138:139] op_sel:[1,1,0] op_sel_hi:[0,1,1] neg_lo:[1,0,0]
	s_nop 0
	v_pk_add_f32 v[130:131], v[130:131], v[134:135]
	s_nop 0
	v_pk_add_f32 v[134:135], v[132:133], v[130:131] op_sel:[0,1] op_sel_hi:[1,0] neg_lo:[0,1]
	v_pk_add_f32 v[130:131], v[132:133], v[130:131] op_sel:[0,1] op_sel_hi:[1,0] neg_hi:[1,0]
	ds_write_b64 v146, v[134:135]
	ds_write_b64 v147, v[130:131]
	v_add_u32_e32 v130, 8, v209
	v_lshlrev_b32_e32 v132, 10, v130
	v_lshlrev_b32_e32 v133, 2, v130
	v_lshrrev_b32_e32 v134, 5, v130
	v_ashrrev_i32_e32 v130, 11, v130
	v_and_b32_e32 v132, 0x3c00, v132
	v_and_b32_e32 v134, 56, v134
	v_and_or_b32 v130, v133, s9, v130
	v_or3_b32 v130, v130, v132, v134
	v_mul_i32_i24_e32 v130, 9, v130
	v_sub_u32_e32 v131, -8, v209
	v_and_b32_e32 v130, -8, v130
	v_add_u32_e32 v142, 0, v130
	v_lshlrev_b32_e32 v130, 10, v131
	v_lshlrev_b32_e32 v132, 2, v131
	v_lshrrev_b32_e32 v133, 5, v131
	v_bfe_u32 v131, v131, 11, 3
	v_and_b32_e32 v130, 0x3c00, v130
	v_and_b32_e32 v132, 0x3c0, v132
	v_and_or_b32 v131, v133, 56, v131
	v_or3_b32 v130, v131, v132, v130
	v_mul_u32_u24_e32 v130, 9, v130
	v_and_b32_e32 v130, 0x3fff8, v130
	v_add_u32_e32 v143, 0, v130
	ds_read_b64 v[130:131], v142
	ds_read_b64 v[132:133], v143
	v_pk_mul_f32 v[134:135], v[162:163], s[50:51] op_sel_hi:[0,1]
	v_pk_fma_f32 v[136:137], v[38:39], s[52:53], v[134:135] neg_lo:[0,0,1] neg_hi:[0,0,1]
	v_pk_fma_f32 v[134:135], v[158:159], s[52:53], v[134:135] op_sel_hi:[0,1,1]
	v_mov_b32_e32 v137, v135
	s_waitcnt lgkmcnt(0)
	v_pk_add_f32 v[134:135], v[130:131], v[132:133] neg_hi:[0,1]
	v_pk_add_f32 v[130:131], v[130:131], v[132:133] op_sel:[1,1] op_sel_hi:[0,0] neg_hi:[1,0]
	v_pk_add_f32 v[132:133], v[126:127], v[128:129] neg_hi:[0,1]
	v_pk_add_f32 v[126:127], v[126:127], v[128:129] op_sel:[1,1] op_sel_hi:[0,0] neg_hi:[1,0]
	s_nop 0
	v_pk_mul_f32 v[128:129], v[134:135], v[132:133] op_sel_hi:[1,0]
	v_pk_mul_f32 v[138:139], v[130:131], v[126:127] op_sel_hi:[1,0]
	s_nop 0
	v_pk_fma_f32 v[128:129], v[134:135], v[132:133], v[128:129] op_sel:[1,1,0] op_sel_hi:[0,1,1] neg_lo:[1,0,0]
	v_pk_fma_f32 v[138:139], v[130:131], v[126:127], v[138:139] op_sel:[1,1,0] op_sel_hi:[0,1,1] neg_lo:[1,0,0]
	s_nop 0
	v_pk_mul_f32 v[140:141], v[138:139], v[136:137] op_sel_hi:[1,0]
	s_nop 0
	v_pk_fma_f32 v[136:137], v[138:139], v[136:137], v[140:141] op_sel:[1,1,0] op_sel_hi:[0,1,1] neg_hi:[1,0,0]
	s_nop 0
	v_pk_add_f32 v[128:129], v[128:129], v[136:137]
	v_pk_mul_f32 v[136:137], v[134:135], v[126:127] op_sel_hi:[1,0]
	s_nop 0
	v_pk_fma_f32 v[126:127], v[134:135], v[126:127], v[136:137] op_sel:[1,1,0] op_sel_hi:[0,1,1] neg_lo:[1,0,0]
	v_pk_mul_f32 v[134:135], v[130:131], v[132:133] op_sel_hi:[1,0]
	s_nop 0
	v_pk_fma_f32 v[130:131], v[130:131], v[132:133], v[134:135] op_sel:[1,1,0] op_sel_hi:[0,1,1] neg_lo:[1,0,0]
	s_nop 0
	v_pk_add_f32 v[126:127], v[126:127], v[130:131]
	s_nop 0
	v_pk_add_f32 v[130:131], v[128:129], v[126:127] op_sel:[0,1] op_sel_hi:[1,0] neg_lo:[0,1]
	v_pk_add_f32 v[126:127], v[128:129], v[126:127] op_sel:[0,1] op_sel_hi:[1,0] neg_hi:[1,0]
	ds_write_b64 v142, v[130:131]
	ds_write_b64 v143, v[126:127]
	v_add_u32_e32 v126, 9, v209
	v_lshlrev_b32_e32 v128, 10, v126
	v_lshlrev_b32_e32 v129, 2, v126
	v_lshrrev_b32_e32 v130, 5, v126
	v_ashrrev_i32_e32 v126, 11, v126
	v_and_b32_e32 v128, 0x3c00, v128
	v_and_b32_e32 v130, 56, v130
	v_and_or_b32 v126, v129, s9, v126
	v_or3_b32 v126, v126, v128, v130
	v_mul_i32_i24_e32 v126, 9, v126
	v_sub_u32_e32 v127, -9, v209
	v_and_b32_e32 v126, -8, v126
	v_add_u32_e32 v138, 0, v126
	v_lshlrev_b32_e32 v126, 10, v127
	v_lshlrev_b32_e32 v128, 2, v127
	v_lshrrev_b32_e32 v129, 5, v127
	v_bfe_u32 v127, v127, 11, 3
	v_and_b32_e32 v126, 0x3c00, v126
	v_and_b32_e32 v128, 0x3c0, v128
	v_and_or_b32 v127, v129, 56, v127
	v_or3_b32 v126, v127, v128, v126
	v_mul_u32_u24_e32 v126, 9, v126
	v_and_b32_e32 v126, 0x3fff8, v126
	v_add_u32_e32 v139, 0, v126
	ds_read_b64 v[126:127], v138
	ds_read_b64 v[128:129], v139
	v_pk_mul_f32 v[130:131], v[162:163], s[54:55] op_sel_hi:[0,1]
	v_pk_fma_f32 v[132:133], v[38:39], s[56:57], v[130:131] neg_lo:[0,0,1] neg_hi:[0,0,1]
	v_pk_fma_f32 v[130:131], v[158:159], s[56:57], v[130:131] op_sel_hi:[0,1,1]
	v_mov_b32_e32 v133, v131
	s_waitcnt lgkmcnt(0)
	v_pk_add_f32 v[130:131], v[126:127], v[128:129] neg_hi:[0,1]
	v_pk_add_f32 v[126:127], v[126:127], v[128:129] op_sel:[1,1] op_sel_hi:[0,0] neg_hi:[1,0]
	v_pk_add_f32 v[128:129], v[122:123], v[124:125] neg_hi:[0,1]
	v_pk_add_f32 v[122:123], v[122:123], v[124:125] op_sel:[1,1] op_sel_hi:[0,0] neg_hi:[1,0]
	s_nop 0
	v_pk_mul_f32 v[124:125], v[130:131], v[128:129] op_sel_hi:[1,0]
	v_pk_mul_f32 v[134:135], v[126:127], v[122:123] op_sel_hi:[1,0]
	s_nop 0
	v_pk_fma_f32 v[124:125], v[130:131], v[128:129], v[124:125] op_sel:[1,1,0] op_sel_hi:[0,1,1] neg_lo:[1,0,0]
	v_pk_fma_f32 v[134:135], v[126:127], v[122:123], v[134:135] op_sel:[1,1,0] op_sel_hi:[0,1,1] neg_lo:[1,0,0]
	s_nop 0
	v_pk_mul_f32 v[136:137], v[134:135], v[132:133] op_sel_hi:[1,0]
	s_nop 0
	v_pk_fma_f32 v[132:133], v[134:135], v[132:133], v[136:137] op_sel:[1,1,0] op_sel_hi:[0,1,1] neg_hi:[1,0,0]
	s_nop 0
	v_pk_add_f32 v[124:125], v[124:125], v[132:133]
	v_pk_mul_f32 v[132:133], v[130:131], v[122:123] op_sel_hi:[1,0]
	s_nop 0
	v_pk_fma_f32 v[122:123], v[130:131], v[122:123], v[132:133] op_sel:[1,1,0] op_sel_hi:[0,1,1] neg_lo:[1,0,0]
	v_pk_mul_f32 v[130:131], v[126:127], v[128:129] op_sel_hi:[1,0]
	s_nop 0
	v_pk_fma_f32 v[126:127], v[126:127], v[128:129], v[130:131] op_sel:[1,1,0] op_sel_hi:[0,1,1] neg_lo:[1,0,0]
	s_nop 0
	v_pk_add_f32 v[122:123], v[122:123], v[126:127]
	s_nop 0
	v_pk_add_f32 v[126:127], v[124:125], v[122:123] op_sel:[0,1] op_sel_hi:[1,0] neg_lo:[0,1]
	v_pk_add_f32 v[122:123], v[124:125], v[122:123] op_sel:[0,1] op_sel_hi:[1,0] neg_hi:[1,0]
	ds_write_b64 v138, v[126:127]
	ds_write_b64 v139, v[122:123]
	v_add_u32_e32 v122, 10, v209
	v_lshlrev_b32_e32 v124, 10, v122
	v_lshlrev_b32_e32 v125, 2, v122
	v_lshrrev_b32_e32 v126, 5, v122
	v_ashrrev_i32_e32 v122, 11, v122
	v_and_b32_e32 v124, 0x3c00, v124
	v_and_b32_e32 v126, 56, v126
	v_and_or_b32 v122, v125, s9, v122
	v_or3_b32 v122, v122, v124, v126
	v_mul_i32_i24_e32 v122, 9, v122
	v_sub_u32_e32 v123, -10, v209
	v_and_b32_e32 v122, -8, v122
	v_add_u32_e32 v134, 0, v122
	v_lshlrev_b32_e32 v122, 10, v123
	v_lshlrev_b32_e32 v124, 2, v123
	v_lshrrev_b32_e32 v125, 5, v123
	v_bfe_u32 v123, v123, 11, 3
	v_and_b32_e32 v122, 0x3c00, v122
	v_and_b32_e32 v124, 0x3c0, v124
	v_and_or_b32 v123, v125, 56, v123
	v_or3_b32 v122, v123, v124, v122
	v_mul_u32_u24_e32 v122, 9, v122
	v_and_b32_e32 v122, 0x3fff8, v122
	v_add_u32_e32 v135, 0, v122
	ds_read_b64 v[122:123], v134
	ds_read_b64 v[124:125], v135
	v_pk_mul_f32 v[126:127], v[162:163], s[58:59] op_sel_hi:[0,1]
	v_pk_fma_f32 v[128:129], v[38:39], s[60:61], v[126:127] neg_lo:[0,0,1] neg_hi:[0,0,1]
	v_pk_fma_f32 v[126:127], v[158:159], s[60:61], v[126:127] op_sel_hi:[0,1,1]
	v_mov_b32_e32 v129, v127
	s_waitcnt lgkmcnt(0)
	v_pk_add_f32 v[126:127], v[122:123], v[124:125] neg_hi:[0,1]
	v_pk_add_f32 v[122:123], v[122:123], v[124:125] op_sel:[1,1] op_sel_hi:[0,0] neg_hi:[1,0]
	v_pk_add_f32 v[124:125], v[118:119], v[120:121] neg_hi:[0,1]
	v_pk_add_f32 v[118:119], v[118:119], v[120:121] op_sel:[1,1] op_sel_hi:[0,0] neg_hi:[1,0]
	s_nop 0
	v_pk_mul_f32 v[120:121], v[126:127], v[124:125] op_sel_hi:[1,0]
	v_pk_mul_f32 v[130:131], v[122:123], v[118:119] op_sel_hi:[1,0]
	s_nop 0
	v_pk_fma_f32 v[120:121], v[126:127], v[124:125], v[120:121] op_sel:[1,1,0] op_sel_hi:[0,1,1] neg_lo:[1,0,0]
	v_pk_fma_f32 v[130:131], v[122:123], v[118:119], v[130:131] op_sel:[1,1,0] op_sel_hi:[0,1,1] neg_lo:[1,0,0]
	s_nop 0
	v_pk_mul_f32 v[132:133], v[130:131], v[128:129] op_sel_hi:[1,0]
	s_nop 0
	v_pk_fma_f32 v[128:129], v[130:131], v[128:129], v[132:133] op_sel:[1,1,0] op_sel_hi:[0,1,1] neg_hi:[1,0,0]
	s_nop 0
	v_pk_add_f32 v[120:121], v[120:121], v[128:129]
	v_pk_mul_f32 v[128:129], v[126:127], v[118:119] op_sel_hi:[1,0]
	s_nop 0
	v_pk_fma_f32 v[118:119], v[126:127], v[118:119], v[128:129] op_sel:[1,1,0] op_sel_hi:[0,1,1] neg_lo:[1,0,0]
	v_pk_mul_f32 v[126:127], v[122:123], v[124:125] op_sel_hi:[1,0]
	s_nop 0
	v_pk_fma_f32 v[122:123], v[122:123], v[124:125], v[126:127] op_sel:[1,1,0] op_sel_hi:[0,1,1] neg_lo:[1,0,0]
	s_nop 0
	v_pk_add_f32 v[118:119], v[118:119], v[122:123]
	s_nop 0
	v_pk_add_f32 v[122:123], v[120:121], v[118:119] op_sel:[0,1] op_sel_hi:[1,0] neg_lo:[0,1]
	v_pk_add_f32 v[118:119], v[120:121], v[118:119] op_sel:[0,1] op_sel_hi:[1,0] neg_hi:[1,0]
	ds_write_b64 v134, v[122:123]
	ds_write_b64 v135, v[118:119]
	v_add_u32_e32 v118, 11, v209
	v_lshlrev_b32_e32 v120, 10, v118
	v_lshlrev_b32_e32 v121, 2, v118
	v_lshrrev_b32_e32 v122, 5, v118
	v_ashrrev_i32_e32 v118, 11, v118
	v_and_b32_e32 v120, 0x3c00, v120
	v_and_b32_e32 v122, 56, v122
	v_and_or_b32 v118, v121, s9, v118
	v_or3_b32 v118, v118, v120, v122
	v_mul_i32_i24_e32 v118, 9, v118
	v_sub_u32_e32 v119, -11, v209
	v_and_b32_e32 v118, -8, v118
	v_add_u32_e32 v130, 0, v118
	v_lshlrev_b32_e32 v118, 10, v119
	v_lshlrev_b32_e32 v120, 2, v119
	v_lshrrev_b32_e32 v121, 5, v119
	v_bfe_u32 v119, v119, 11, 3
	v_and_b32_e32 v118, 0x3c00, v118
	v_and_b32_e32 v120, 0x3c0, v120
	v_and_or_b32 v119, v121, 56, v119
	v_or3_b32 v118, v119, v120, v118
	v_mul_u32_u24_e32 v118, 9, v118
	v_and_b32_e32 v118, 0x3fff8, v118
	v_add_u32_e32 v131, 0, v118
	ds_read_b64 v[118:119], v130
	ds_read_b64 v[120:121], v131
	v_pk_mul_f32 v[122:123], v[162:163], s[62:63] op_sel_hi:[0,1]
	v_pk_fma_f32 v[124:125], v[38:39], s[64:65], v[122:123] neg_lo:[0,0,1] neg_hi:[0,0,1]
	v_pk_fma_f32 v[122:123], v[158:159], s[64:65], v[122:123] op_sel_hi:[0,1,1]
	v_mov_b32_e32 v125, v123
	s_waitcnt lgkmcnt(0)
	v_pk_add_f32 v[122:123], v[118:119], v[120:121] neg_hi:[0,1]
	v_pk_add_f32 v[118:119], v[118:119], v[120:121] op_sel:[1,1] op_sel_hi:[0,0] neg_hi:[1,0]
	v_pk_add_f32 v[120:121], v[114:115], v[116:117] neg_hi:[0,1]
	v_pk_add_f32 v[114:115], v[114:115], v[116:117] op_sel:[1,1] op_sel_hi:[0,0] neg_hi:[1,0]
	s_nop 0
	v_pk_mul_f32 v[116:117], v[122:123], v[120:121] op_sel_hi:[1,0]
	v_pk_mul_f32 v[126:127], v[118:119], v[114:115] op_sel_hi:[1,0]
	s_nop 0
	v_pk_fma_f32 v[116:117], v[122:123], v[120:121], v[116:117] op_sel:[1,1,0] op_sel_hi:[0,1,1] neg_lo:[1,0,0]
	v_pk_fma_f32 v[126:127], v[118:119], v[114:115], v[126:127] op_sel:[1,1,0] op_sel_hi:[0,1,1] neg_lo:[1,0,0]
	s_nop 0
	v_pk_mul_f32 v[128:129], v[126:127], v[124:125] op_sel_hi:[1,0]
	s_nop 0
	v_pk_fma_f32 v[124:125], v[126:127], v[124:125], v[128:129] op_sel:[1,1,0] op_sel_hi:[0,1,1] neg_hi:[1,0,0]
	s_nop 0
	v_pk_add_f32 v[116:117], v[116:117], v[124:125]
	v_pk_mul_f32 v[124:125], v[122:123], v[114:115] op_sel_hi:[1,0]
	s_nop 0
	v_pk_fma_f32 v[114:115], v[122:123], v[114:115], v[124:125] op_sel:[1,1,0] op_sel_hi:[0,1,1] neg_lo:[1,0,0]
	v_pk_mul_f32 v[122:123], v[118:119], v[120:121] op_sel_hi:[1,0]
	s_nop 0
	v_pk_fma_f32 v[118:119], v[118:119], v[120:121], v[122:123] op_sel:[1,1,0] op_sel_hi:[0,1,1] neg_lo:[1,0,0]
	s_nop 0
	v_pk_add_f32 v[114:115], v[114:115], v[118:119]
	s_nop 0
	v_pk_add_f32 v[118:119], v[116:117], v[114:115] op_sel:[0,1] op_sel_hi:[1,0] neg_lo:[0,1]
	v_pk_add_f32 v[114:115], v[116:117], v[114:115] op_sel:[0,1] op_sel_hi:[1,0] neg_hi:[1,0]
	ds_write_b64 v130, v[118:119]
	ds_write_b64 v131, v[114:115]
	v_add_u32_e32 v114, 12, v209
	v_lshlrev_b32_e32 v116, 10, v114
	v_lshlrev_b32_e32 v117, 2, v114
	v_lshrrev_b32_e32 v118, 5, v114
	v_ashrrev_i32_e32 v114, 11, v114
	v_and_b32_e32 v116, 0x3c00, v116
	v_and_b32_e32 v118, 56, v118
	v_and_or_b32 v114, v117, s9, v114
	v_or3_b32 v114, v114, v116, v118
	v_mul_i32_i24_e32 v114, 9, v114
	v_sub_u32_e32 v115, -12, v209
	v_and_b32_e32 v114, -8, v114
	v_add_u32_e32 v126, 0, v114
	v_lshlrev_b32_e32 v114, 10, v115
	v_lshlrev_b32_e32 v116, 2, v115
	v_lshrrev_b32_e32 v117, 5, v115
	v_bfe_u32 v115, v115, 11, 3
	v_and_b32_e32 v114, 0x3c00, v114
	v_and_b32_e32 v116, 0x3c0, v116
	v_and_or_b32 v115, v117, 56, v115
	v_or3_b32 v114, v115, v116, v114
	v_mul_u32_u24_e32 v114, 9, v114
	v_and_b32_e32 v114, 0x3fff8, v114
	v_add_u32_e32 v127, 0, v114
	ds_read_b64 v[114:115], v126
	ds_read_b64 v[116:117], v127
	v_pk_mul_f32 v[118:119], v[162:163], s[66:67] op_sel_hi:[0,1]
	v_pk_fma_f32 v[120:121], v[38:39], s[68:69], v[118:119] neg_lo:[0,0,1] neg_hi:[0,0,1]
	v_pk_fma_f32 v[118:119], v[158:159], s[68:69], v[118:119] op_sel_hi:[0,1,1]
	v_mov_b32_e32 v121, v119
	s_waitcnt lgkmcnt(0)
	v_pk_add_f32 v[118:119], v[114:115], v[116:117] neg_hi:[0,1]
	v_pk_add_f32 v[114:115], v[114:115], v[116:117] op_sel:[1,1] op_sel_hi:[0,0] neg_hi:[1,0]
	v_pk_add_f32 v[116:117], v[110:111], v[112:113] neg_hi:[0,1]
	v_pk_add_f32 v[110:111], v[110:111], v[112:113] op_sel:[1,1] op_sel_hi:[0,0] neg_hi:[1,0]
	s_nop 0
	v_pk_mul_f32 v[112:113], v[118:119], v[116:117] op_sel_hi:[1,0]
	v_pk_mul_f32 v[122:123], v[114:115], v[110:111] op_sel_hi:[1,0]
	s_nop 0
	v_pk_fma_f32 v[112:113], v[118:119], v[116:117], v[112:113] op_sel:[1,1,0] op_sel_hi:[0,1,1] neg_lo:[1,0,0]
	v_pk_fma_f32 v[122:123], v[114:115], v[110:111], v[122:123] op_sel:[1,1,0] op_sel_hi:[0,1,1] neg_lo:[1,0,0]
	s_nop 0
	v_pk_mul_f32 v[124:125], v[122:123], v[120:121] op_sel_hi:[1,0]
	s_nop 0
	v_pk_fma_f32 v[120:121], v[122:123], v[120:121], v[124:125] op_sel:[1,1,0] op_sel_hi:[0,1,1] neg_hi:[1,0,0]
	s_nop 0
	v_pk_add_f32 v[112:113], v[112:113], v[120:121]
	v_pk_mul_f32 v[120:121], v[118:119], v[110:111] op_sel_hi:[1,0]
	s_nop 0
	v_pk_fma_f32 v[110:111], v[118:119], v[110:111], v[120:121] op_sel:[1,1,0] op_sel_hi:[0,1,1] neg_lo:[1,0,0]
	v_pk_mul_f32 v[118:119], v[114:115], v[116:117] op_sel_hi:[1,0]
	s_nop 0
	v_pk_fma_f32 v[114:115], v[114:115], v[116:117], v[118:119] op_sel:[1,1,0] op_sel_hi:[0,1,1] neg_lo:[1,0,0]
	s_nop 0
	v_pk_add_f32 v[110:111], v[110:111], v[114:115]
	s_nop 0
	v_pk_add_f32 v[114:115], v[112:113], v[110:111] op_sel:[0,1] op_sel_hi:[1,0] neg_lo:[0,1]
	v_pk_add_f32 v[110:111], v[112:113], v[110:111] op_sel:[0,1] op_sel_hi:[1,0] neg_hi:[1,0]
	ds_write_b64 v126, v[114:115]
	ds_write_b64 v127, v[110:111]
	v_add_u32_e32 v110, 13, v209
	v_lshlrev_b32_e32 v112, 10, v110
	v_lshlrev_b32_e32 v113, 2, v110
	v_lshrrev_b32_e32 v114, 5, v110
	v_ashrrev_i32_e32 v110, 11, v110
	v_and_b32_e32 v112, 0x3c00, v112
	v_and_b32_e32 v114, 56, v114
	v_and_or_b32 v110, v113, s9, v110
	v_or3_b32 v110, v110, v112, v114
	v_mul_i32_i24_e32 v110, 9, v110
	v_sub_u32_e32 v111, -13, v209
	v_and_b32_e32 v110, -8, v110
	v_add_u32_e32 v122, 0, v110
	v_lshlrev_b32_e32 v110, 10, v111
	v_lshlrev_b32_e32 v112, 2, v111
	v_lshrrev_b32_e32 v113, 5, v111
	v_bfe_u32 v111, v111, 11, 3
	v_and_b32_e32 v110, 0x3c00, v110
	v_and_b32_e32 v112, 0x3c0, v112
	v_and_or_b32 v111, v113, 56, v111
	v_or3_b32 v110, v111, v112, v110
	v_mul_u32_u24_e32 v110, 9, v110
	v_and_b32_e32 v110, 0x3fff8, v110
	v_add_u32_e32 v123, 0, v110
	ds_read_b64 v[110:111], v122
	ds_read_b64 v[112:113], v123
	v_pk_mul_f32 v[114:115], v[162:163], s[70:71] op_sel_hi:[0,1]
	v_pk_fma_f32 v[116:117], v[38:39], s[72:73], v[114:115] neg_lo:[0,0,1] neg_hi:[0,0,1]
	v_pk_fma_f32 v[114:115], v[158:159], s[72:73], v[114:115] op_sel_hi:[0,1,1]
	v_mov_b32_e32 v117, v115
	s_waitcnt lgkmcnt(0)
	v_pk_add_f32 v[114:115], v[110:111], v[112:113] neg_hi:[0,1]
	v_pk_add_f32 v[110:111], v[110:111], v[112:113] op_sel:[1,1] op_sel_hi:[0,0] neg_hi:[1,0]
	v_pk_add_f32 v[112:113], v[106:107], v[108:109] neg_hi:[0,1]
	v_pk_add_f32 v[106:107], v[106:107], v[108:109] op_sel:[1,1] op_sel_hi:[0,0] neg_hi:[1,0]
	s_nop 0
	v_pk_mul_f32 v[108:109], v[114:115], v[112:113] op_sel_hi:[1,0]
	v_pk_mul_f32 v[118:119], v[110:111], v[106:107] op_sel_hi:[1,0]
	s_nop 0
	v_pk_fma_f32 v[108:109], v[114:115], v[112:113], v[108:109] op_sel:[1,1,0] op_sel_hi:[0,1,1] neg_lo:[1,0,0]
	v_pk_fma_f32 v[118:119], v[110:111], v[106:107], v[118:119] op_sel:[1,1,0] op_sel_hi:[0,1,1] neg_lo:[1,0,0]
	s_nop 0
	v_pk_mul_f32 v[120:121], v[118:119], v[116:117] op_sel_hi:[1,0]
	s_nop 0
	v_pk_fma_f32 v[116:117], v[118:119], v[116:117], v[120:121] op_sel:[1,1,0] op_sel_hi:[0,1,1] neg_hi:[1,0,0]
	s_nop 0
	v_pk_add_f32 v[108:109], v[108:109], v[116:117]
	v_pk_mul_f32 v[116:117], v[114:115], v[106:107] op_sel_hi:[1,0]
	s_nop 0
	v_pk_fma_f32 v[106:107], v[114:115], v[106:107], v[116:117] op_sel:[1,1,0] op_sel_hi:[0,1,1] neg_lo:[1,0,0]
	v_pk_mul_f32 v[114:115], v[110:111], v[112:113] op_sel_hi:[1,0]
	s_nop 0
	v_pk_fma_f32 v[110:111], v[110:111], v[112:113], v[114:115] op_sel:[1,1,0] op_sel_hi:[0,1,1] neg_lo:[1,0,0]
	s_nop 0
	v_pk_add_f32 v[106:107], v[106:107], v[110:111]
	s_nop 0
	v_pk_add_f32 v[110:111], v[108:109], v[106:107] op_sel:[0,1] op_sel_hi:[1,0] neg_lo:[0,1]
	v_pk_add_f32 v[106:107], v[108:109], v[106:107] op_sel:[0,1] op_sel_hi:[1,0] neg_hi:[1,0]
	ds_write_b64 v122, v[110:111]
	ds_write_b64 v123, v[106:107]
	v_add_u32_e32 v106, 14, v209
	v_lshlrev_b32_e32 v108, 10, v106
	v_lshlrev_b32_e32 v109, 2, v106
	v_lshrrev_b32_e32 v110, 5, v106
	v_ashrrev_i32_e32 v106, 11, v106
	v_and_b32_e32 v108, 0x3c00, v108
	v_and_b32_e32 v110, 56, v110
	v_and_or_b32 v106, v109, s9, v106
	v_or3_b32 v106, v106, v108, v110
	v_mul_i32_i24_e32 v106, 9, v106
	v_sub_u32_e32 v107, -14, v209
	v_and_b32_e32 v106, -8, v106
	v_add_u32_e32 v118, 0, v106
	v_lshlrev_b32_e32 v106, 10, v107
	v_lshlrev_b32_e32 v108, 2, v107
	v_lshrrev_b32_e32 v109, 5, v107
	v_bfe_u32 v107, v107, 11, 3
	v_and_b32_e32 v106, 0x3c00, v106
	v_and_b32_e32 v108, 0x3c0, v108
	v_and_or_b32 v107, v109, 56, v107
	v_or3_b32 v106, v107, v108, v106
	v_mul_u32_u24_e32 v106, 9, v106
	v_and_b32_e32 v106, 0x3fff8, v106
	v_add_u32_e32 v119, 0, v106
	ds_read_b64 v[106:107], v118
	ds_read_b64 v[108:109], v119
	v_pk_mul_f32 v[110:111], v[162:163], s[74:75] op_sel_hi:[0,1]
	v_pk_fma_f32 v[112:113], v[38:39], s[76:77], v[110:111] neg_lo:[0,0,1] neg_hi:[0,0,1]
	v_pk_fma_f32 v[110:111], v[158:159], s[76:77], v[110:111] op_sel_hi:[0,1,1]
	v_mov_b32_e32 v113, v111
	s_waitcnt lgkmcnt(0)
	v_pk_add_f32 v[110:111], v[106:107], v[108:109] neg_hi:[0,1]
	v_pk_add_f32 v[106:107], v[106:107], v[108:109] op_sel:[1,1] op_sel_hi:[0,0] neg_hi:[1,0]
	v_pk_add_f32 v[108:109], v[102:103], v[104:105] neg_hi:[0,1]
	v_pk_add_f32 v[102:103], v[102:103], v[104:105] op_sel:[1,1] op_sel_hi:[0,0] neg_hi:[1,0]
	s_nop 0
	v_pk_mul_f32 v[104:105], v[110:111], v[108:109] op_sel_hi:[1,0]
	v_pk_mul_f32 v[114:115], v[106:107], v[102:103] op_sel_hi:[1,0]
	s_nop 0
	v_pk_fma_f32 v[104:105], v[110:111], v[108:109], v[104:105] op_sel:[1,1,0] op_sel_hi:[0,1,1] neg_lo:[1,0,0]
	v_pk_fma_f32 v[114:115], v[106:107], v[102:103], v[114:115] op_sel:[1,1,0] op_sel_hi:[0,1,1] neg_lo:[1,0,0]
	s_nop 0
	v_pk_mul_f32 v[116:117], v[114:115], v[112:113] op_sel_hi:[1,0]
	s_nop 0
	v_pk_fma_f32 v[112:113], v[114:115], v[112:113], v[116:117] op_sel:[1,1,0] op_sel_hi:[0,1,1] neg_hi:[1,0,0]
	s_nop 0
	v_pk_add_f32 v[104:105], v[104:105], v[112:113]
	v_pk_mul_f32 v[112:113], v[110:111], v[102:103] op_sel_hi:[1,0]
	s_nop 0
	v_pk_fma_f32 v[102:103], v[110:111], v[102:103], v[112:113] op_sel:[1,1,0] op_sel_hi:[0,1,1] neg_lo:[1,0,0]
	v_pk_mul_f32 v[110:111], v[106:107], v[108:109] op_sel_hi:[1,0]
	s_nop 0
	v_pk_fma_f32 v[106:107], v[106:107], v[108:109], v[110:111] op_sel:[1,1,0] op_sel_hi:[0,1,1] neg_lo:[1,0,0]
	s_nop 0
	v_pk_add_f32 v[102:103], v[102:103], v[106:107]
	s_nop 0
	v_pk_add_f32 v[106:107], v[104:105], v[102:103] op_sel:[0,1] op_sel_hi:[1,0] neg_lo:[0,1]
	v_pk_add_f32 v[102:103], v[104:105], v[102:103] op_sel:[0,1] op_sel_hi:[1,0] neg_hi:[1,0]
	ds_write_b64 v118, v[106:107]
	ds_write_b64 v119, v[102:103]
	v_add_u32_e32 v102, 15, v209
	v_lshlrev_b32_e32 v104, 10, v102
	v_lshlrev_b32_e32 v105, 2, v102
	v_lshrrev_b32_e32 v106, 5, v102
	v_ashrrev_i32_e32 v102, 11, v102
	v_and_b32_e32 v104, 0x3c00, v104
	v_and_b32_e32 v106, 56, v106
	v_and_or_b32 v102, v105, s9, v102
	v_or3_b32 v102, v102, v104, v106
	v_mul_i32_i24_e32 v102, 9, v102
	v_sub_u32_e32 v103, -15, v209
	v_and_b32_e32 v102, -8, v102
	v_add_u32_e32 v114, 0, v102
	v_lshlrev_b32_e32 v102, 10, v103
	v_lshlrev_b32_e32 v104, 2, v103
	v_lshrrev_b32_e32 v105, 5, v103
	v_bfe_u32 v103, v103, 11, 3
	v_and_b32_e32 v102, 0x3c00, v102
	v_and_b32_e32 v104, 0x3c0, v104
	v_and_or_b32 v103, v105, 56, v103
	v_or3_b32 v102, v103, v104, v102
	v_mul_u32_u24_e32 v102, 9, v102
	v_and_b32_e32 v102, 0x3fff8, v102
	v_add_u32_e32 v115, 0, v102
	ds_read_b64 v[102:103], v114
	ds_read_b64 v[104:105], v115
	v_pk_mul_f32 v[106:107], v[162:163], s[78:79] op_sel_hi:[0,1]
	v_pk_fma_f32 v[108:109], v[38:39], s[80:81], v[106:107] neg_lo:[0,0,1] neg_hi:[0,0,1]
	v_pk_fma_f32 v[106:107], v[158:159], s[80:81], v[106:107] op_sel_hi:[0,1,1]
	v_mov_b32_e32 v109, v107
	s_waitcnt lgkmcnt(0)
	v_pk_add_f32 v[106:107], v[102:103], v[104:105] neg_hi:[0,1]
	v_pk_add_f32 v[102:103], v[102:103], v[104:105] op_sel:[1,1] op_sel_hi:[0,0] neg_hi:[1,0]
	v_pk_add_f32 v[104:105], v[2:3], v[4:5] neg_hi:[0,1]
	v_pk_add_f32 v[2:3], v[2:3], v[4:5] op_sel:[1,1] op_sel_hi:[0,0] neg_hi:[1,0]
	s_nop 0
	v_pk_mul_f32 v[4:5], v[106:107], v[104:105] op_sel_hi:[1,0]
	v_pk_mul_f32 v[110:111], v[102:103], v[2:3] op_sel_hi:[1,0]
	s_nop 0
	v_pk_fma_f32 v[4:5], v[106:107], v[104:105], v[4:5] op_sel:[1,1,0] op_sel_hi:[0,1,1] neg_lo:[1,0,0]
	v_pk_fma_f32 v[110:111], v[102:103], v[2:3], v[110:111] op_sel:[1,1,0] op_sel_hi:[0,1,1] neg_lo:[1,0,0]
	s_nop 0
	v_pk_mul_f32 v[112:113], v[110:111], v[108:109] op_sel_hi:[1,0]
	s_nop 0
	v_pk_fma_f32 v[108:109], v[110:111], v[108:109], v[112:113] op_sel:[1,1,0] op_sel_hi:[0,1,1] neg_hi:[1,0,0]
	s_nop 0
	v_pk_add_f32 v[4:5], v[4:5], v[108:109]
	v_pk_mul_f32 v[108:109], v[106:107], v[2:3] op_sel_hi:[1,0]
	s_nop 0
	v_pk_fma_f32 v[2:3], v[106:107], v[2:3], v[108:109] op_sel:[1,1,0] op_sel_hi:[0,1,1] neg_lo:[1,0,0]
	v_pk_mul_f32 v[106:107], v[102:103], v[104:105] op_sel_hi:[1,0]
	s_nop 0
	v_pk_fma_f32 v[102:103], v[102:103], v[104:105], v[106:107] op_sel:[1,1,0] op_sel_hi:[0,1,1] neg_lo:[1,0,0]
	s_nop 0
	v_pk_add_f32 v[2:3], v[2:3], v[102:103]
	s_nop 0
	v_pk_add_f32 v[102:103], v[4:5], v[2:3] op_sel:[0,1] op_sel_hi:[1,0] neg_lo:[0,1]
	ds_write_b64 v114, v[102:103]
	v_pk_add_f32 v[2:3], v[4:5], v[2:3] op_sel:[0,1] op_sel_hi:[1,0] neg_hi:[1,0]
	ds_write_b64 v115, v[2:3]
	s_and_saveexec_b64 s[84:85], s[0:1]
	s_cbranch_execz .LBB0_771
	v_mov_b32_e32 v4, s94
	ds_read_b64 v[2:3], v203 offset:32
	ds_read_b64 v[4:5], v4
	s_waitcnt lgkmcnt(1)
	v_pk_add_f32 v[102:103], v[2:3], v[2:3] neg_hi:[0,1]
	v_pk_add_f32 v[2:3], v[2:3], v[2:3] op_sel:[1,1] op_sel_hi:[0,0] neg_hi:[1,0]
	s_waitcnt lgkmcnt(0)
	v_pk_add_f32 v[104:105], v[4:5], v[4:5] neg_hi:[0,1]
	v_pk_add_f32 v[4:5], v[4:5], v[4:5] op_sel:[1,1] op_sel_hi:[0,0] neg_hi:[1,0]
	v_mov_b64_e32 v[110:111], s[2:3]
	v_pk_mul_f32 v[108:109], v[2:3], v[4:5] op_sel_hi:[1,0]
	v_pk_mul_f32 v[106:107], v[102:103], v[104:105] op_sel_hi:[1,0]
	s_nop 0
	v_pk_fma_f32 v[108:109], v[2:3], v[4:5], v[108:109] op_sel:[1,1,0] op_sel_hi:[0,1,1] neg_lo:[1,0,0]
	v_pk_fma_f32 v[106:107], v[102:103], v[104:105], v[106:107] op_sel:[1,1,0] op_sel_hi:[0,1,1] neg_lo:[1,0,0]
	s_nop 0
	v_pk_mul_f32 v[112:113], v[108:109], v[110:111] op_sel_hi:[1,0]
	s_nop 0
	v_pk_fma_f32 v[108:109], v[108:109], v[110:111], v[112:113] op_sel:[1,1,0] op_sel_hi:[0,1,1] neg_hi:[1,0,0]
	s_nop 0
	v_pk_add_f32 v[106:107], v[106:107], v[108:109]
	v_pk_mul_f32 v[108:109], v[102:103], v[4:5] op_sel_hi:[1,0]
	s_nop 0
	v_pk_fma_f32 v[4:5], v[102:103], v[4:5], v[108:109] op_sel:[1,1,0] op_sel_hi:[0,1,1] neg_lo:[1,0,0]
	v_pk_mul_f32 v[102:103], v[2:3], v[104:105] op_sel_hi:[1,0]
	s_nop 0
	v_pk_fma_f32 v[2:3], v[2:3], v[104:105], v[102:103] op_sel:[1,1,0] op_sel_hi:[0,1,1] neg_lo:[1,0,0]
	s_nop 0
	v_pk_add_f32 v[2:3], v[4:5], v[2:3]
	s_nop 0
	v_pk_add_f32 v[2:3], v[106:107], v[2:3] op_sel:[0,1] op_sel_hi:[1,0] neg_hi:[1,0]
	ds_write_b64 v203, v[2:3] offset:32
.LBB0_771:
	s_or_b64 exec, exec, s[84:85]
	s_waitcnt lgkmcnt(0)
	s_barrier
	s_cselect_b32 s99, 1, 0
	v_readfirstlane_b32 s98, v0
	s_cmp_lt_u32 s98, 0x100
	s_cbranch_scc1 .Lfft_stg_21885
	s_sleep 8
.Lfft_stg_21885:
	s_cmp_lg_u32 s99, 0
	s_or_b32 s84, s83, s82
	s_cmp_eq_u32 s83, 3
	s_cbranch_scc1 .LBB0_773
	s_ashr_i32 s85, s84, 31
	v_mov_b32_e32 v2, v204
	s_lshl_b64 s[86:87], s[84:85], 16
	s_add_u32 s85, s86, 0x10000
	s_addc_u32 vcc_lo, s87, 0
	v_lshlrev_b32_e32 v2, 1, v2
	s_add_u32 s86, s88, s85
	v_add_u32_e32 v6, 0x400, v2
	s_addc_u32 s87, s89, vcc_lo
	v_ashrrev_i32_e32 v7, 31, v6
	v_lshl_add_u64 v[8:9], v[6:7], 2, s[86:87]
	v_add_u32_e32 v6, 0x800, v2
	v_ashrrev_i32_e32 v7, 31, v6
	v_add_u32_e32 v14, 0x1400, v2
	v_lshl_add_u64 v[10:11], v[6:7], 2, s[86:87]
	v_add_u32_e32 v6, 0xc00, v2
	v_ashrrev_i32_e32 v15, 31, v14
	v_ashrrev_i32_e32 v3, 31, v2
	v_ashrrev_i32_e32 v7, 31, v6
	v_lshl_add_u64 v[16:17], v[14:15], 2, s[86:87]
	v_add_u32_e32 v14, 0x1800, v2
	v_lshl_add_u64 v[4:5], v[2:3], 2, s[86:87]
	v_lshl_add_u64 v[12:13], v[6:7], 2, s[86:87]
	v_ashrrev_i32_e32 v15, 31, v14
	v_add_u32_e32 v22, 0x2400, v2
	global_load_dwordx2 v[6:7], v[4:5], off
	s_nop 0
	global_load_dwordx2 v[8:9], v[8:9], off
	s_nop 0
	global_load_dwordx2 v[10:11], v[10:11], off
	s_nop 0
	global_load_dwordx2 v[12:13], v[12:13], off
	v_add_u32_e32 v4, 0x1000, v2
	v_lshl_add_u64 v[18:19], v[14:15], 2, s[86:87]
	v_add_u32_e32 v14, 0x1c00, v2
	v_ashrrev_i32_e32 v23, 31, v22
	v_ashrrev_i32_e32 v5, 31, v4
	v_ashrrev_i32_e32 v15, 31, v14
	v_lshl_add_u64 v[24:25], v[22:23], 2, s[86:87]
	v_add_u32_e32 v22, 0x2800, v2
	v_lshl_add_u64 v[4:5], v[4:5], 2, s[86:87]
	v_lshl_add_u64 v[20:21], v[14:15], 2, s[86:87]
	v_ashrrev_i32_e32 v23, 31, v22
	v_add_u32_e32 v30, 0x3400, v2
	global_load_dwordx2 v[14:15], v[4:5], off
	s_nop 0
	global_load_dwordx2 v[16:17], v[16:17], off
	s_nop 0
	global_load_dwordx2 v[18:19], v[18:19], off
	s_nop 0
	global_load_dwordx2 v[20:21], v[20:21], off
	v_add_u32_e32 v4, 0x2000, v2
	v_lshl_add_u64 v[26:27], v[22:23], 2, s[86:87]
	v_add_u32_e32 v22, 0x2c00, v2
	v_ashrrev_i32_e32 v31, 31, v30
	v_ashrrev_i32_e32 v5, 31, v4
	v_ashrrev_i32_e32 v23, 31, v22
	v_lshl_add_u64 v[32:33], v[30:31], 2, s[86:87]
	v_add_u32_e32 v30, 0x3800, v2
	v_lshl_add_u64 v[4:5], v[4:5], 2, s[86:87]
	v_lshl_add_u64 v[28:29], v[22:23], 2, s[86:87]
	v_ashrrev_i32_e32 v31, 31, v30
	global_load_dwordx2 v[22:23], v[4:5], off
	s_nop 0
	global_load_dwordx2 v[24:25], v[24:25], off
	s_nop 0
	global_load_dwordx2 v[26:27], v[26:27], off
	s_nop 0
	global_load_dwordx2 v[28:29], v[28:29], off
	v_add_u32_e32 v4, 0x3000, v2
	v_lshl_add_u64 v[34:35], v[30:31], 2, s[86:87]
	v_add_u32_e32 v30, 0x3c00, v2
	v_ashrrev_i32_e32 v5, 31, v4
	v_ashrrev_i32_e32 v31, 31, v30
	v_lshl_add_u64 v[4:5], v[4:5], 2, s[86:87]
	v_lshl_add_u64 v[36:37], v[30:31], 2, s[86:87]
	s_add_u32 s86, s90, s85
	v_sub_u32_e32 v40, 0x3c00, v2
	s_addc_u32 s87, s91, vcc_lo
	v_ashrrev_i32_e32 v41, 31, v40
	v_lshl_add_u64 v[44:45], v[40:41], 2, s[86:87]
	v_sub_u32_e32 v40, 0x3800, v2
	v_sub_u32_e32 v38, 0x3fff, v2
	v_sub_u32_e32 v42, 0x3bff, v2
	v_ashrrev_i32_e32 v41, 31, v40
	global_load_dwordx2 v[30:31], v[4:5], off
	s_nop 0
	global_load_dwordx2 v[32:33], v[32:33], off
	s_nop 0
	global_load_dwordx2 v[34:35], v[34:35], off
	s_nop 0
	global_load_dwordx2 v[36:37], v[36:37], off
	v_sub_u32_e32 v4, 0x4000, v2
	v_ashrrev_i32_e32 v39, 31, v38
	v_ashrrev_i32_e32 v43, 31, v42
	v_sub_u32_e32 v46, 0x37ff, v2
	v_lshl_add_u64 v[48:49], v[40:41], 2, s[86:87]
	v_sub_u32_e32 v40, 0x3400, v2
	v_sub_u32_e32 v50, 0x33ff, v2
	v_lshl_add_u64 v[38:39], v[38:39], 2, s[86:87]
	v_ashrrev_i32_e32 v5, 31, v4
	v_lshl_add_u64 v[42:43], v[42:43], 2, s[86:87]
	v_ashrrev_i32_e32 v47, 31, v46
	v_ashrrev_i32_e32 v51, 31, v50
	v_ashrrev_i32_e32 v41, 31, v40
	v_lshl_add_u64 v[4:5], v[4:5], 2, s[86:87]
	v_lshl_add_u64 v[46:47], v[46:47], 2, s[86:87]
	v_lshl_add_u64 v[50:51], v[50:51], 2, s[86:87]
	v_lshl_add_u64 v[52:53], v[40:41], 2, s[86:87]
	global_load_dword v39, v[38:39], off
	s_nop 0
	global_load_dword v205, v[4:5], off
	global_load_dword v41, v[42:43], off
	global_load_dword v40, v[44:45], off
	s_nop 0
	global_load_dword v43, v[46:47], off
	global_load_dword v42, v[48:49], off
	global_load_dword v45, v[50:51], off
	global_load_dword v44, v[52:53], off
	v_sub_u32_e32 v48, 0x2c00, v2
	v_ashrrev_i32_e32 v49, 31, v48
	v_lshl_add_u64 v[52:53], v[48:49], 2, s[86:87]
	v_sub_u32_e32 v48, 0x2800, v2
	v_sub_u32_e32 v46, 0x2fff, v2
	v_sub_u32_e32 v50, 0x2bff, v2
	v_ashrrev_i32_e32 v49, 31, v48
	v_sub_u32_e32 v4, 0x3000, v2
	v_ashrrev_i32_e32 v47, 31, v46
	v_ashrrev_i32_e32 v51, 31, v50
	v_sub_u32_e32 v54, 0x27ff, v2
	v_lshl_add_u64 v[56:57], v[48:49], 2, s[86:87]
	v_sub_u32_e32 v48, 0x2400, v2
	v_sub_u32_e32 v58, 0x23ff, v2
	v_lshl_add_u64 v[46:47], v[46:47], 2, s[86:87]
	v_ashrrev_i32_e32 v5, 31, v4
	v_lshl_add_u64 v[50:51], v[50:51], 2, s[86:87]
	v_ashrrev_i32_e32 v55, 31, v54
	v_ashrrev_i32_e32 v59, 31, v58
	v_ashrrev_i32_e32 v49, 31, v48
	v_lshl_add_u64 v[4:5], v[4:5], 2, s[86:87]
	v_lshl_add_u64 v[54:55], v[54:55], 2, s[86:87]
	v_lshl_add_u64 v[58:59], v[58:59], 2, s[86:87]
	v_lshl_add_u64 v[60:61], v[48:49], 2, s[86:87]
	global_load_dword v47, v[46:47], off
	s_nop 0
	global_load_dword v46, v[4:5], off
	global_load_dword v49, v[50:51], off
	global_load_dword v48, v[52:53], off
	s_nop 0
	global_load_dword v51, v[54:55], off
	global_load_dword v50, v[56:57], off
	global_load_dword v53, v[58:59], off
	global_load_dword v52, v[60:61], off
	v_sub_u32_e32 v56, 0x1c00, v2
	v_ashrrev_i32_e32 v57, 31, v56
	v_lshl_add_u64 v[60:61], v[56:57], 2, s[86:87]
	v_sub_u32_e32 v56, 0x1800, v2
	v_sub_u32_e32 v54, 0x1fff, v2
	v_sub_u32_e32 v58, 0x1bff, v2
	v_ashrrev_i32_e32 v57, 31, v56
	v_sub_u32_e32 v4, 0x2000, v2
	v_ashrrev_i32_e32 v55, 31, v54
	v_ashrrev_i32_e32 v59, 31, v58
	v_sub_u32_e32 v62, 0x17ff, v2
	v_lshl_add_u64 v[64:65], v[56:57], 2, s[86:87]
	v_sub_u32_e32 v56, 0x1400, v2
	v_sub_u32_e32 v66, 0x13ff, v2
	v_lshl_add_u64 v[54:55], v[54:55], 2, s[86:87]
	v_ashrrev_i32_e32 v5, 31, v4
	v_lshl_add_u64 v[58:59], v[58:59], 2, s[86:87]
	v_ashrrev_i32_e32 v63, 31, v62
	v_ashrrev_i32_e32 v67, 31, v66
	v_ashrrev_i32_e32 v57, 31, v56
	v_lshl_add_u64 v[4:5], v[4:5], 2, s[86:87]
	v_lshl_add_u64 v[62:63], v[62:63], 2, s[86:87]
	v_lshl_add_u64 v[66:67], v[66:67], 2, s[86:87]
	v_lshl_add_u64 v[68:69], v[56:57], 2, s[86:87]
	global_load_dword v55, v[54:55], off
	s_nop 0
	global_load_dword v54, v[4:5], off
	global_load_dword v57, v[58:59], off
	global_load_dword v56, v[60:61], off
	s_nop 0
	global_load_dword v59, v[62:63], off
	global_load_dword v58, v[64:65], off
	global_load_dword v61, v[66:67], off
	global_load_dword v60, v[68:69], off
	v_sub_u32_e32 v64, 0xc00, v2
	v_ashrrev_i32_e32 v65, 31, v64
	v_lshl_add_u64 v[68:69], v[64:65], 2, s[86:87]
	v_sub_u32_e32 v64, 0x800, v2
	v_ashrrev_i32_e32 v65, 31, v64
	v_sub_u32_e32 v4, 0x1000, v2
	v_sub_u32_e32 v62, 0xfff, v2
	v_sub_u32_e32 v66, 0xbff, v2
	v_sub_u32_e32 v70, 0x7ff, v2
	v_lshl_add_u64 v[72:73], v[64:65], 2, s[86:87]
	v_sub_u32_e32 v64, 0x400, v2
	v_sub_u32_e32 v2, 0x3ff, v2
	v_ashrrev_i32_e32 v63, 31, v62
	v_ashrrev_i32_e32 v67, 31, v66
	v_ashrrev_i32_e32 v3, 31, v2
	v_lshl_add_u64 v[62:63], v[62:63], 2, s[86:87]
	v_ashrrev_i32_e32 v5, 31, v4
	v_lshl_add_u64 v[66:67], v[66:67], 2, s[86:87]
	v_ashrrev_i32_e32 v71, 31, v70
	v_lshl_add_u64 v[2:3], v[2:3], 2, s[86:87]
	v_ashrrev_i32_e32 v65, 31, v64
	v_lshl_add_u64 v[4:5], v[4:5], 2, s[86:87]
	v_lshl_add_u64 v[70:71], v[70:71], 2, s[86:87]
	v_lshl_add_u64 v[74:75], v[64:65], 2, s[86:87]
	global_load_dword v63, v[62:63], off
	s_nop 0
	global_load_dword v62, v[4:5], off
	global_load_dword v65, v[66:67], off
	global_load_dword v64, v[68:69], off
	s_nop 0
	global_load_dword v67, v[70:71], off
	global_load_dword v66, v[72:73], off
	global_load_dword v69, v[2:3], off
	global_load_dword v68, v[74:75], off
	v_mov_b32_e32 v2, v204
	s_add_u32 s86, s92, s85
	v_lshlrev_b32_e32 v2, 1, v2
	v_add_u32_e32 v70, 0x400, v2
	s_addc_u32 s87, s93, vcc_lo
	v_ashrrev_i32_e32 v71, 31, v70
	v_lshl_add_u64 v[72:73], v[70:71], 2, s[86:87]
	v_add_u32_e32 v70, 0x800, v2
	v_ashrrev_i32_e32 v71, 31, v70
	v_add_u32_e32 v78, 0x1400, v2
	v_lshl_add_u64 v[74:75], v[70:71], 2, s[86:87]
	v_add_u32_e32 v70, 0xc00, v2
	v_ashrrev_i32_e32 v79, 31, v78
	v_ashrrev_i32_e32 v3, 31, v2
	v_ashrrev_i32_e32 v71, 31, v70
	v_lshl_add_u64 v[80:81], v[78:79], 2, s[86:87]
	v_add_u32_e32 v78, 0x1800, v2
	v_lshl_add_u64 v[4:5], v[2:3], 2, s[86:87]
	v_lshl_add_u64 v[76:77], v[70:71], 2, s[86:87]
	v_ashrrev_i32_e32 v79, 31, v78
	v_add_u32_e32 v86, 0x2400, v2
	global_load_dwordx2 v[70:71], v[4:5], off
	s_nop 0
	global_load_dwordx2 v[72:73], v[72:73], off
	s_nop 0
	global_load_dwordx2 v[74:75], v[74:75], off
	s_nop 0
	global_load_dwordx2 v[76:77], v[76:77], off
	v_add_u32_e32 v4, 0x1000, v2
	v_lshl_add_u64 v[82:83], v[78:79], 2, s[86:87]
	v_add_u32_e32 v78, 0x1c00, v2
	v_ashrrev_i32_e32 v87, 31, v86
	v_ashrrev_i32_e32 v5, 31, v4
	v_ashrrev_i32_e32 v79, 31, v78
	v_lshl_add_u64 v[88:89], v[86:87], 2, s[86:87]
	v_add_u32_e32 v86, 0x2800, v2
	v_lshl_add_u64 v[4:5], v[4:5], 2, s[86:87]
	v_lshl_add_u64 v[84:85], v[78:79], 2, s[86:87]
	v_ashrrev_i32_e32 v87, 31, v86
	global_load_dwordx2 v[78:79], v[4:5], off
	s_nop 0
	global_load_dwordx2 v[80:81], v[80:81], off
	s_nop 0
	global_load_dwordx2 v[82:83], v[82:83], off
	s_nop 0
	global_load_dwordx2 v[84:85], v[84:85], off
	v_add_u32_e32 v4, 0x2000, v2
	v_lshl_add_u64 v[90:91], v[86:87], 2, s[86:87]
	v_add_u32_e32 v86, 0x2c00, v2
	v_ashrrev_i32_e32 v5, 31, v4
	v_ashrrev_i32_e32 v87, 31, v86
	v_add_u32_e32 v94, 0x3400, v2
	v_lshl_add_u64 v[4:5], v[4:5], 2, s[86:87]
	v_lshl_add_u64 v[92:93], v[86:87], 2, s[86:87]
	v_ashrrev_i32_e32 v95, 31, v94
	global_load_dwordx2 v[86:87], v[4:5], off
	s_nop 0
	global_load_dwordx2 v[88:89], v[88:89], off
	s_nop 0
	global_load_dwordx2 v[90:91], v[90:91], off
	s_nop 0
	global_load_dwordx2 v[92:93], v[92:93], off
	v_add_u32_e32 v4, 0x3000, v2
	v_lshl_add_u64 v[96:97], v[94:95], 2, s[86:87]
	v_add_u32_e32 v94, 0x3800, v2
	v_ashrrev_i32_e32 v5, 31, v4
	v_ashrrev_i32_e32 v95, 31, v94
	v_add_u32_e32 v2, 0x3c00, v2
	v_lshl_add_u64 v[4:5], v[4:5], 2, s[86:87]
	v_lshl_add_u64 v[98:99], v[94:95], 2, s[86:87]
	v_ashrrev_i32_e32 v3, 31, v2
	v_lshl_add_u64 v[2:3], v[2:3], 2, s[86:87]
	global_load_dwordx2 v[94:95], v[4:5], off
	s_nop 0
	global_load_dwordx2 v[96:97], v[96:97], off
	s_nop 0
	global_load_dwordx2 v[98:99], v[98:99], off
	s_nop 0
	global_load_dwordx2 v[100:101], v[2:3], off

.LBB0_774:
	v_add_u32_e32 v3, s85, v2
	ds_read2_b64 v[102:105], v3 offset1:1
	ds_read2_b64 v[106:109], v3 offset0:2 offset1:3
	ds_read2_b64 v[110:113], v3 offset0:4 offset1:5
	ds_read2_b64 v[114:117], v3 offset0:6 offset1:7
	s_add_i32 s85, s85, 0x9000
	s_cmp_lg_u32 s85, 0x24000
	s_waitcnt lgkmcnt(1)
	v_pk_add_f32 v[4:5], v[102:103], v[110:111]
	v_pk_add_f32 v[102:103], v[102:103], v[110:111] neg_lo:[0,1] neg_hi:[0,1]
	v_pk_add_f32 v[110:111], v[104:105], v[112:113]
	v_pk_add_f32 v[104:105], v[104:105], v[112:113] neg_lo:[0,1] neg_hi:[0,1]
	v_mov_b64_e32 v[112:113], s[6:7]
	v_pk_mul_f32 v[118:119], v[104:105], v[112:113] op_sel_hi:[1,0]
	s_nop 0
	v_pk_fma_f32 v[104:105], v[104:105], v[112:113], v[118:119] op_sel:[1,1,0] op_sel_hi:[0,1,1] neg_lo:[1,0,0]
	s_waitcnt lgkmcnt(0)
	v_pk_add_f32 v[112:113], v[106:107], v[114:115]
	v_pk_add_f32 v[106:107], v[106:107], v[114:115] op_sel:[1,1] op_sel_hi:[0,0] neg_lo:[1,0] neg_hi:[0,1]
	v_pk_add_f32 v[114:115], v[108:109], v[116:117]
	v_pk_add_f32 v[108:109], v[108:109], v[116:117] neg_lo:[0,1] neg_hi:[0,1]
	v_mov_b64_e32 v[116:117], s[14:15]
	v_pk_mul_f32 v[118:119], v[108:109], v[116:117] op_sel_hi:[1,0]
	s_nop 0
	v_pk_fma_f32 v[108:109], v[108:109], v[116:117], v[118:119] op_sel:[1,1,0] op_sel_hi:[0,1,1] neg_lo:[1,0,0]
	v_pk_add_f32 v[116:117], v[4:5], v[112:113]
	v_pk_add_f32 v[4:5], v[4:5], v[112:113] neg_lo:[0,1] neg_hi:[0,1]
	v_pk_add_f32 v[112:113], v[110:111], v[114:115]
	v_pk_add_f32 v[110:111], v[110:111], v[114:115] op_sel:[1,1] op_sel_hi:[0,0] neg_lo:[1,0] neg_hi:[0,1]
	v_pk_add_f32 v[114:115], v[102:103], v[106:107]
	v_pk_add_f32 v[102:103], v[102:103], v[106:107] neg_lo:[0,1] neg_hi:[0,1]
	v_pk_add_f32 v[106:107], v[104:105], v[108:109]
	v_pk_add_f32 v[104:105], v[104:105], v[108:109] op_sel:[1,1] op_sel_hi:[0,0] neg_lo:[1,0] neg_hi:[0,1]
	v_pk_add_f32 v[108:109], v[116:117], v[112:113]
	v_pk_add_f32 v[112:113], v[116:117], v[112:113] neg_lo:[0,1] neg_hi:[0,1]
	v_pk_add_f32 v[116:117], v[4:5], v[110:111]
	v_pk_add_f32 v[4:5], v[4:5], v[110:111] neg_lo:[0,1] neg_hi:[0,1]
	v_pk_add_f32 v[110:111], v[114:115], v[106:107]
	v_pk_add_f32 v[106:107], v[114:115], v[106:107] neg_lo:[0,1] neg_hi:[0,1]
	v_pk_add_f32 v[114:115], v[102:103], v[104:105]
	v_pk_add_f32 v[102:103], v[102:103], v[104:105] neg_lo:[0,1] neg_hi:[0,1]
	ds_write2_b64 v3, v[108:109], v[110:111] offset1:1
	ds_write2_b64 v3, v[116:117], v[114:115] offset0:2 offset1:3
	ds_write2_b64 v3, v[112:113], v[106:107] offset0:4 offset1:5
	ds_write2_b64 v3, v[4:5], v[102:103] offset0:6 offset1:7
	s_cbranch_scc1 .LBB0_774
	v_mov_b32_e32 v4, v204
	s_waitcnt lgkmcnt(0)
	s_barrier
	s_cselect_b32 s99, 1, 0
	v_readfirstlane_b32 s98, v0
	s_cmp_lt_u32 s98, 0x100
	s_cbranch_scc1 .Lfft_stg_22269
	s_sleep 8
.Lfft_stg_22269:
	s_cmp_lg_u32 s99, 0
	s_mov_b32 s85, 0
	v_and_b32_e32 v5, 7, v4
	v_cvt_f32_ubyte0_e32 v2, v5
	v_mul_f32_e32 v3, 0x3c800000, v2
	v_cos_f32_e32 v2, v3
	v_sin_f32_e32 v3, v3
	v_lshlrev_b32_e32 v4, 3, v4
	v_lshl_add_u32 v5, v5, 3, 0
.LBB0_776:
	v_add_u32_e32 v38, s85, v4
	v_and_b32_e32 v38, 0xffffffc0, v38
	v_lshlrev_b32_e32 v102, 3, v38
	v_add3_u32 v38, v5, v38, v102
	ds_read2_b64 v[102:105], v38 offset1:9
	s_waitcnt lgkmcnt(0)
	v_pk_mul_f32 v[106:107], v[104:105], v[2:3] op_sel_hi:[1,0]
	s_addk_i32 s85, 0x1000
	v_pk_fma_f32 v[108:109], v[104:105], v[2:3], v[106:107] op_sel:[1,1,0] op_sel_hi:[0,1,1] neg_lo:[1,0,0]
	v_pk_mul_f32 v[104:105], v[2:3], v[2:3] op_sel_hi:[1,0]
	s_cmpk_lg_i32 s85, 0x4000
	v_pk_fma_f32 v[110:111], v[2:3], v[2:3], v[104:105] op_sel:[1,1,0] op_sel_hi:[0,1,1] neg_lo:[1,0,0]
	ds_read2_b64 v[104:107], v38 offset0:18 offset1:27
	s_waitcnt lgkmcnt(0)
	v_pk_mul_f32 v[112:113], v[104:105], v[110:111] op_sel_hi:[1,0]
	s_nop 0
	v_pk_fma_f32 v[112:113], v[104:105], v[110:111], v[112:113] op_sel:[1,1,0] op_sel_hi:[0,1,1] neg_lo:[1,0,0]
	v_pk_mul_f32 v[104:105], v[110:111], v[2:3] op_sel_hi:[1,0]
	s_nop 0
	v_pk_fma_f32 v[104:105], v[110:111], v[2:3], v[104:105] op_sel:[1,1,0] op_sel_hi:[0,1,1] neg_lo:[1,0,0]
	s_nop 0
	v_pk_mul_f32 v[110:111], v[106:107], v[104:105] op_sel_hi:[1,0]
	s_nop 0
	v_pk_fma_f32 v[110:111], v[106:107], v[104:105], v[110:111] op_sel:[1,1,0] op_sel_hi:[0,1,1] neg_lo:[1,0,0]
	v_pk_mul_f32 v[106:107], v[104:105], v[2:3] op_sel_hi:[1,0]
	s_nop 0
	v_pk_fma_f32 v[114:115], v[104:105], v[2:3], v[106:107] op_sel:[1,1,0] op_sel_hi:[0,1,1] neg_lo:[1,0,0]
	ds_read2_b64 v[104:107], v38 offset0:36 offset1:45
	s_waitcnt lgkmcnt(0)
	v_pk_mul_f32 v[116:117], v[104:105], v[114:115] op_sel_hi:[1,0]
	s_nop 0
	v_pk_fma_f32 v[116:117], v[104:105], v[114:115], v[116:117] op_sel:[1,1,0] op_sel_hi:[0,1,1] neg_lo:[1,0,0]
	v_pk_mul_f32 v[104:105], v[114:115], v[2:3] op_sel_hi:[1,0]
	s_nop 0
	v_pk_fma_f32 v[104:105], v[114:115], v[2:3], v[104:105] op_sel:[1,1,0] op_sel_hi:[0,1,1] neg_lo:[1,0,0]
	s_nop 0
	v_pk_mul_f32 v[114:115], v[106:107], v[104:105] op_sel_hi:[1,0]
	s_nop 0
	v_pk_fma_f32 v[114:115], v[106:107], v[104:105], v[114:115] op_sel:[1,1,0] op_sel_hi:[0,1,1] neg_lo:[1,0,0]
	v_pk_mul_f32 v[106:107], v[104:105], v[2:3] op_sel_hi:[1,0]
	s_nop 0
	v_pk_fma_f32 v[118:119], v[104:105], v[2:3], v[106:107] op_sel:[1,1,0] op_sel_hi:[0,1,1] neg_lo:[1,0,0]
	ds_read2_b64 v[104:107], v38 offset0:54 offset1:63
	s_waitcnt lgkmcnt(0)
	v_pk_mul_f32 v[120:121], v[104:105], v[118:119] op_sel_hi:[1,0]
	s_nop 0
	v_pk_fma_f32 v[104:105], v[104:105], v[118:119], v[120:121] op_sel:[1,1,0] op_sel_hi:[0,1,1] neg_lo:[1,0,0]
	v_pk_mul_f32 v[120:121], v[118:119], v[2:3] op_sel_hi:[1,0]
	s_nop 0
	v_pk_fma_f32 v[118:119], v[118:119], v[2:3], v[120:121] op_sel:[1,1,0] op_sel_hi:[0,1,1] neg_lo:[1,0,0]
	s_nop 0
	v_pk_mul_f32 v[120:121], v[106:107], v[118:119] op_sel_hi:[1,0]
	s_nop 0
	v_pk_fma_f32 v[106:107], v[106:107], v[118:119], v[120:121] op_sel:[1,1,0] op_sel_hi:[0,1,1] neg_lo:[1,0,0]
	v_pk_add_f32 v[118:119], v[102:103], v[116:117]
	v_pk_add_f32 v[102:103], v[102:103], v[116:117] neg_lo:[0,1] neg_hi:[0,1]
	v_pk_add_f32 v[116:117], v[108:109], v[114:115]
	v_pk_add_f32 v[108:109], v[108:109], v[114:115] neg_lo:[0,1] neg_hi:[0,1]
	v_mov_b64_e32 v[114:115], s[6:7]
	v_pk_mul_f32 v[120:121], v[108:109], v[114:115] op_sel_hi:[1,0]
	s_nop 0
	v_pk_fma_f32 v[108:109], v[108:109], v[114:115], v[120:121] op_sel:[1,1,0] op_sel_hi:[0,1,1] neg_lo:[1,0,0]
	v_pk_add_f32 v[114:115], v[112:113], v[104:105]
	v_pk_add_f32 v[104:105], v[112:113], v[104:105] op_sel:[1,1] op_sel_hi:[0,0] neg_lo:[1,0] neg_hi:[0,1]
	v_pk_add_f32 v[112:113], v[110:111], v[106:107]
	v_pk_add_f32 v[106:107], v[110:111], v[106:107] neg_lo:[0,1] neg_hi:[0,1]
	v_mov_b64_e32 v[110:111], s[14:15]
	v_pk_mul_f32 v[120:121], v[106:107], v[110:111] op_sel_hi:[1,0]
	s_nop 0
	v_pk_fma_f32 v[106:107], v[106:107], v[110:111], v[120:121] op_sel:[1,1,0] op_sel_hi:[0,1,1] neg_lo:[1,0,0]
	v_pk_add_f32 v[110:111], v[118:119], v[114:115]
	v_pk_add_f32 v[114:115], v[118:119], v[114:115] neg_lo:[0,1] neg_hi:[0,1]
	v_pk_add_f32 v[118:119], v[116:117], v[112:113]
	v_pk_add_f32 v[112:113], v[116:117], v[112:113] op_sel:[1,1] op_sel_hi:[0,0] neg_lo:[1,0] neg_hi:[0,1]
	v_pk_add_f32 v[116:117], v[102:103], v[104:105]
	v_pk_add_f32 v[102:103], v[102:103], v[104:105] neg_lo:[0,1] neg_hi:[0,1]
	v_pk_add_f32 v[104:105], v[108:109], v[106:107]
	v_pk_add_f32 v[106:107], v[108:109], v[106:107] op_sel:[1,1] op_sel_hi:[0,0] neg_lo:[1,0] neg_hi:[0,1]
	v_pk_add_f32 v[108:109], v[110:111], v[118:119]
	v_pk_add_f32 v[110:111], v[110:111], v[118:119] neg_lo:[0,1] neg_hi:[0,1]
	v_pk_add_f32 v[118:119], v[114:115], v[112:113]
	v_pk_add_f32 v[112:113], v[114:115], v[112:113] neg_lo:[0,1] neg_hi:[0,1]
	v_pk_add_f32 v[114:115], v[116:117], v[104:105]
	v_pk_add_f32 v[104:105], v[116:117], v[104:105] neg_lo:[0,1] neg_hi:[0,1]
	v_pk_add_f32 v[116:117], v[102:103], v[106:107]
	v_pk_add_f32 v[102:103], v[102:103], v[106:107] neg_lo:[0,1] neg_hi:[0,1]
	ds_write2_b64 v38, v[108:109], v[114:115] offset1:9
	ds_write2_b64 v38, v[118:119], v[116:117] offset0:18 offset1:27
	ds_write2_b64 v38, v[110:111], v[104:105] offset0:36 offset1:45
	ds_write2_b64 v38, v[112:113], v[102:103] offset0:54 offset1:63
	s_cbranch_scc1 .LBB0_776
	v_mov_b32_e32 v4, v204
	s_waitcnt lgkmcnt(0)
	s_barrier
	s_cselect_b32 s99, 1, 0
	v_readfirstlane_b32 s98, v0
	s_cmp_lt_u32 s98, 0x100
	s_cbranch_scc1 .Lfft_stg_22445
	s_sleep 8
.Lfft_stg_22445:
	s_cmp_lg_u32 s99, 0
	s_mov_b32 s85, 0
	v_and_b32_e32 v38, 63, v4
	v_cvt_f32_ubyte0_e32 v2, v38
	v_mul_f32_e32 v3, 0x3a800000, v2
	v_cos_f32_e32 v2, v3
	v_sin_f32_e32 v3, v3
	v_lshlrev_b32_e32 v132, 4, v4
	s_mov_b64 s[86:87], -1
.LBB0_778:
	v_add_u32_e32 v4, s85, v132
	v_and_b32_e32 v4, 0xfffffc00, v4
	v_or_b32_e32 v5, v4, v38
	v_bitop3_b32 v4, v4, s97, v38 bitop3:0xc8
	v_lshlrev_b32_e32 v5, 3, v5
	v_add3_u32 v133, 0, v4, v5
	ds_read2_b64 v[102:105], v133 offset1:72
	s_waitcnt lgkmcnt(0)
	v_pk_mul_f32 v[4:5], v[104:105], v[2:3] op_sel_hi:[1,0]
	v_add_u32_e32 v134, 0x800, v133
	v_pk_fma_f32 v[130:131], v[104:105], v[2:3], v[4:5] op_sel:[1,1,0] op_sel_hi:[0,1,1] neg_lo:[1,0,0]
	v_pk_mul_f32 v[4:5], v[2:3], v[2:3] op_sel_hi:[1,0]
	ds_read2_b64 v[104:107], v133 offset0:144 offset1:216
	v_pk_fma_f32 v[4:5], v[2:3], v[2:3], v[4:5] op_sel:[1,1,0] op_sel_hi:[0,1,1] neg_lo:[1,0,0]
	v_add_u32_e32 v135, 0x1000, v133
	s_waitcnt lgkmcnt(0)
	v_pk_mul_f32 v[108:109], v[104:105], v[4:5] op_sel_hi:[1,0]
	v_add_u32_e32 v136, 0x1400, v133
	v_pk_fma_f32 v[120:121], v[104:105], v[4:5], v[108:109] op_sel:[1,1,0] op_sel_hi:[0,1,1] neg_lo:[1,0,0]
	v_pk_mul_f32 v[104:105], v[4:5], v[2:3] op_sel_hi:[1,0]
	v_add_u32_e32 v137, 0x1800, v133
	v_pk_fma_f32 v[4:5], v[4:5], v[2:3], v[104:105] op_sel:[1,1,0] op_sel_hi:[0,1,1] neg_lo:[1,0,0]
	v_add_u32_e32 v138, 0x1c00, v133
	v_pk_mul_f32 v[104:105], v[106:107], v[4:5] op_sel_hi:[1,0]
	s_movk_i32 s85, 0x2000
	v_pk_fma_f32 v[118:119], v[106:107], v[4:5], v[104:105] op_sel:[1,1,0] op_sel_hi:[0,1,1] neg_lo:[1,0,0]
	v_pk_mul_f32 v[104:105], v[4:5], v[2:3] op_sel_hi:[1,0]
	s_and_b64 vcc, exec, s[86:87]
	v_pk_fma_f32 v[4:5], v[4:5], v[2:3], v[104:105] op_sel:[1,1,0] op_sel_hi:[0,1,1] neg_lo:[1,0,0]
	ds_read2_b64 v[104:107], v134 offset0:32 offset1:104
	s_waitcnt lgkmcnt(0)
	v_pk_mul_f32 v[108:109], v[104:105], v[4:5] op_sel_hi:[1,0]
	s_mov_b64 s[86:87], 0
	v_pk_fma_f32 v[112:113], v[104:105], v[4:5], v[108:109] op_sel:[1,1,0] op_sel_hi:[0,1,1] neg_lo:[1,0,0]
	v_pk_mul_f32 v[104:105], v[4:5], v[2:3] op_sel_hi:[1,0]
	s_nop 0
	v_pk_fma_f32 v[4:5], v[4:5], v[2:3], v[104:105] op_sel:[1,1,0] op_sel_hi:[0,1,1] neg_lo:[1,0,0]
	s_nop 0
	v_pk_mul_f32 v[104:105], v[106:107], v[4:5] op_sel_hi:[1,0]
	s_nop 0
	v_pk_fma_f32 v[114:115], v[106:107], v[4:5], v[104:105] op_sel:[1,1,0] op_sel_hi:[0,1,1] neg_lo:[1,0,0]
	v_pk_mul_f32 v[104:105], v[4:5], v[2:3] op_sel_hi:[1,0]
	s_nop 0
	v_pk_fma_f32 v[4:5], v[4:5], v[2:3], v[104:105] op_sel:[1,1,0] op_sel_hi:[0,1,1] neg_lo:[1,0,0]
	ds_read2_b64 v[104:107], v134 offset0:176 offset1:248
	s_waitcnt lgkmcnt(0)
	v_pk_mul_f32 v[108:109], v[104:105], v[4:5] op_sel_hi:[1,0]
	s_nop 0
	v_pk_fma_f32 v[104:105], v[104:105], v[4:5], v[108:109] op_sel:[1,1,0] op_sel_hi:[0,1,1] neg_lo:[1,0,0]
	v_pk_mul_f32 v[108:109], v[4:5], v[2:3] op_sel_hi:[1,0]
	s_nop 0
	v_pk_fma_f32 v[108:109], v[4:5], v[2:3], v[108:109] op_sel:[1,1,0] op_sel_hi:[0,1,1] neg_lo:[1,0,0]
	s_nop 0
	v_pk_mul_f32 v[4:5], v[106:107], v[108:109] op_sel_hi:[1,0]
	s_nop 0
	v_pk_fma_f32 v[4:5], v[106:107], v[108:109], v[4:5] op_sel:[1,1,0] op_sel_hi:[0,1,1] neg_lo:[1,0,0]
	v_pk_mul_f32 v[106:107], v[108:109], v[2:3] op_sel_hi:[1,0]
	s_nop 0
	v_pk_fma_f32 v[110:111], v[108:109], v[2:3], v[106:107] op_sel:[1,1,0] op_sel_hi:[0,1,1] neg_lo:[1,0,0]
	ds_read2_b64 v[106:109], v135 offset0:64 offset1:136
	s_waitcnt lgkmcnt(0)
	v_pk_mul_f32 v[116:117], v[106:107], v[110:111] op_sel_hi:[1,0]
	s_nop 0
	v_pk_fma_f32 v[140:141], v[106:107], v[110:111], v[116:117] op_sel:[1,1,0] op_sel_hi:[0,1,1] neg_lo:[1,0,0]
	v_pk_mul_f32 v[106:107], v[110:111], v[2:3] op_sel_hi:[1,0]
	s_nop 0
	v_pk_fma_f32 v[106:107], v[110:111], v[2:3], v[106:107] op_sel:[1,1,0] op_sel_hi:[0,1,1] neg_lo:[1,0,0]
	s_nop 0
	v_pk_mul_f32 v[110:111], v[108:109], v[106:107] op_sel_hi:[1,0]
	s_nop 0
	v_pk_fma_f32 v[142:143], v[108:109], v[106:107], v[110:111] op_sel:[1,1,0] op_sel_hi:[0,1,1] neg_lo:[1,0,0]
	v_pk_mul_f32 v[108:109], v[106:107], v[2:3] op_sel_hi:[1,0]
	s_nop 0
	v_pk_fma_f32 v[110:111], v[106:107], v[2:3], v[108:109] op_sel:[1,1,0] op_sel_hi:[0,1,1] neg_lo:[1,0,0]
	ds_read2_b64 v[106:109], v136 offset0:80 offset1:152
	s_waitcnt lgkmcnt(0)
	v_pk_mul_f32 v[116:117], v[106:107], v[110:111] op_sel_hi:[1,0]
	s_nop 0
	v_pk_fma_f32 v[128:129], v[106:107], v[110:111], v[116:117] op_sel:[1,1,0] op_sel_hi:[0,1,1] neg_lo:[1,0,0]
	v_pk_mul_f32 v[106:107], v[110:111], v[2:3] op_sel_hi:[1,0]
	s_nop 0
	v_pk_fma_f32 v[106:107], v[110:111], v[2:3], v[106:107] op_sel:[1,1,0] op_sel_hi:[0,1,1] neg_lo:[1,0,0]
	s_nop 0
	v_pk_mul_f32 v[110:111], v[108:109], v[106:107] op_sel_hi:[1,0]
	s_nop 0
	v_pk_fma_f32 v[126:127], v[108:109], v[106:107], v[110:111] op_sel:[1,1,0] op_sel_hi:[0,1,1] neg_lo:[1,0,0]
	v_pk_mul_f32 v[108:109], v[106:107], v[2:3] op_sel_hi:[1,0]
	s_nop 0
	v_pk_fma_f32 v[110:111], v[106:107], v[2:3], v[108:109] op_sel:[1,1,0] op_sel_hi:[0,1,1] neg_lo:[1,0,0]
	ds_read2_b64 v[106:109], v137 offset0:96 offset1:168
	s_waitcnt lgkmcnt(0)
	v_pk_mul_f32 v[116:117], v[106:107], v[110:111] op_sel_hi:[1,0]
	s_nop 0
	v_pk_fma_f32 v[122:123], v[106:107], v[110:111], v[116:117] op_sel:[1,1,0] op_sel_hi:[0,1,1] neg_lo:[1,0,0]
	v_pk_mul_f32 v[106:107], v[110:111], v[2:3] op_sel_hi:[1,0]
	s_nop 0
	v_pk_fma_f32 v[106:107], v[110:111], v[2:3], v[106:107] op_sel:[1,1,0] op_sel_hi:[0,1,1] neg_lo:[1,0,0]
	s_nop 0
	v_pk_mul_f32 v[110:111], v[108:109], v[106:107] op_sel_hi:[1,0]
	s_nop 0
	v_pk_fma_f32 v[124:125], v[108:109], v[106:107], v[110:111] op_sel:[1,1,0] op_sel_hi:[0,1,1] neg_lo:[1,0,0]
	v_pk_mul_f32 v[108:109], v[106:107], v[2:3] op_sel_hi:[1,0]
	s_nop 0
	v_pk_fma_f32 v[110:111], v[106:107], v[2:3], v[108:109] op_sel:[1,1,0] op_sel_hi:[0,1,1] neg_lo:[1,0,0]
	ds_read2_b64 v[106:109], v138 offset0:112 offset1:184
	s_waitcnt lgkmcnt(0)
	v_pk_mul_f32 v[116:117], v[106:107], v[110:111] op_sel_hi:[1,0]
	s_nop 0
	v_pk_fma_f32 v[116:117], v[106:107], v[110:111], v[116:117] op_sel:[1,1,0] op_sel_hi:[0,1,1] neg_lo:[1,0,0]
	v_pk_mul_f32 v[106:107], v[110:111], v[2:3] op_sel_hi:[1,0]
	s_nop 0
	v_pk_fma_f32 v[106:107], v[110:111], v[2:3], v[106:107] op_sel:[1,1,0] op_sel_hi:[0,1,1] neg_lo:[1,0,0]
	s_nop 0
	v_pk_mul_f32 v[110:111], v[108:109], v[106:107] op_sel_hi:[1,0]
	s_nop 0
	v_pk_fma_f32 v[110:111], v[108:109], v[106:107], v[110:111] op_sel:[1,1,0] op_sel_hi:[0,1,1] neg_lo:[1,0,0]
	v_pk_add_f32 v[106:107], v[102:103], v[140:141]
	v_pk_add_f32 v[102:103], v[102:103], v[140:141] neg_lo:[0,1] neg_hi:[0,1]
	v_pk_add_f32 v[108:109], v[130:131], v[142:143]
	v_pk_add_f32 v[130:131], v[130:131], v[142:143] neg_lo:[0,1] neg_hi:[0,1]
	v_mov_b64_e32 v[140:141], s[4:5]
	v_pk_mul_f32 v[142:143], v[130:131], v[140:141] op_sel_hi:[1,0]
	s_nop 0
	v_pk_fma_f32 v[130:131], v[130:131], v[140:141], v[142:143] op_sel:[1,1,0] op_sel_hi:[0,1,1] neg_lo:[1,0,0]
	v_pk_add_f32 v[140:141], v[120:121], v[128:129]
	v_pk_add_f32 v[120:121], v[120:121], v[128:129] neg_lo:[0,1] neg_hi:[0,1]
	v_mov_b64_e32 v[128:129], s[6:7]
	v_pk_mul_f32 v[142:143], v[120:121], v[128:129] op_sel_hi:[1,0]
	s_nop 0
	v_pk_fma_f32 v[120:121], v[120:121], v[128:129], v[142:143] op_sel:[1,1,0] op_sel_hi:[0,1,1] neg_lo:[1,0,0]
	v_pk_add_f32 v[142:143], v[118:119], v[126:127]
	v_pk_add_f32 v[118:119], v[118:119], v[126:127] neg_lo:[0,1] neg_hi:[0,1]
	v_mov_b64_e32 v[126:127], s[10:11]
	v_pk_mul_f32 v[144:145], v[118:119], v[126:127] op_sel_hi:[1,0]
	s_nop 0
	v_pk_fma_f32 v[118:119], v[118:119], v[126:127], v[144:145] op_sel:[1,1,0] op_sel_hi:[0,1,1] neg_lo:[1,0,0]
	v_pk_add_f32 v[126:127], v[112:113], v[122:123]
	v_pk_add_f32 v[112:113], v[112:113], v[122:123] op_sel:[1,1] op_sel_hi:[0,0] neg_lo:[1,0] neg_hi:[0,1]
	v_pk_add_f32 v[122:123], v[114:115], v[124:125]
	v_pk_add_f32 v[114:115], v[114:115], v[124:125] neg_lo:[0,1] neg_hi:[0,1]
	v_mov_b64_e32 v[124:125], s[12:13]
	v_pk_mul_f32 v[144:145], v[114:115], v[124:125] op_sel_hi:[1,0]
	s_nop 0
	v_pk_fma_f32 v[114:115], v[114:115], v[124:125], v[144:145] op_sel:[1,1,0] op_sel_hi:[0,1,1] neg_lo:[1,0,0]
	v_pk_add_f32 v[124:125], v[104:105], v[116:117]
	v_pk_add_f32 v[104:105], v[104:105], v[116:117] neg_lo:[0,1] neg_hi:[0,1]
	v_mov_b64_e32 v[116:117], s[14:15]
	v_pk_mul_f32 v[144:145], v[104:105], v[116:117] op_sel_hi:[1,0]
	s_nop 0
	v_pk_fma_f32 v[104:105], v[104:105], v[116:117], v[144:145] op_sel:[1,1,0] op_sel_hi:[0,1,1] neg_lo:[1,0,0]
	v_pk_add_f32 v[144:145], v[4:5], v[110:111]
	v_pk_add_f32 v[4:5], v[4:5], v[110:111] neg_lo:[0,1] neg_hi:[0,1]
	v_mov_b64_e32 v[110:111], s[16:17]
	v_pk_mul_f32 v[146:147], v[4:5], v[110:111] op_sel_hi:[1,0]
	s_nop 0
	v_pk_fma_f32 v[4:5], v[4:5], v[110:111], v[146:147] op_sel:[1,1,0] op_sel_hi:[0,1,1] neg_lo:[1,0,0]
	v_pk_add_f32 v[110:111], v[106:107], v[126:127]
	v_pk_add_f32 v[106:107], v[106:107], v[126:127] neg_lo:[0,1] neg_hi:[0,1]
	v_pk_add_f32 v[126:127], v[108:109], v[122:123]
	v_pk_add_f32 v[108:109], v[108:109], v[122:123] neg_lo:[0,1] neg_hi:[0,1]
	s_nop 0
	v_pk_mul_f32 v[122:123], v[108:109], v[128:129] op_sel_hi:[1,0]
	s_nop 0
	v_pk_fma_f32 v[108:109], v[108:109], v[128:129], v[122:123] op_sel:[1,1,0] op_sel_hi:[0,1,1] neg_lo:[1,0,0]
	v_pk_add_f32 v[122:123], v[140:141], v[124:125]
	v_pk_add_f32 v[124:125], v[140:141], v[124:125] op_sel:[1,1] op_sel_hi:[0,0] neg_lo:[1,0] neg_hi:[0,1]
	v_pk_add_f32 v[140:141], v[142:143], v[144:145]
	v_pk_add_f32 v[142:143], v[142:143], v[144:145] neg_lo:[0,1] neg_hi:[0,1]
	s_nop 0
	v_pk_mul_f32 v[144:145], v[142:143], v[116:117] op_sel_hi:[1,0]
	s_nop 0
	v_pk_fma_f32 v[142:143], v[142:143], v[116:117], v[144:145] op_sel:[1,1,0] op_sel_hi:[0,1,1] neg_lo:[1,0,0]
	v_pk_add_f32 v[144:145], v[102:103], v[112:113]
	v_pk_add_f32 v[102:103], v[102:103], v[112:113] neg_lo:[0,1] neg_hi:[0,1]
	v_pk_add_f32 v[112:113], v[130:131], v[114:115]
	v_pk_add_f32 v[114:115], v[130:131], v[114:115] neg_lo:[0,1] neg_hi:[0,1]
	s_nop 0
	v_pk_mul_f32 v[130:131], v[114:115], v[128:129] op_sel_hi:[1,0]
	s_nop 0
	v_pk_fma_f32 v[114:115], v[114:115], v[128:129], v[130:131] op_sel:[1,1,0] op_sel_hi:[0,1,1] neg_lo:[1,0,0]
	v_pk_add_f32 v[128:129], v[120:121], v[104:105]
	v_pk_add_f32 v[104:105], v[120:121], v[104:105] op_sel:[1,1] op_sel_hi:[0,0] neg_lo:[1,0] neg_hi:[0,1]
	v_pk_add_f32 v[120:121], v[118:119], v[4:5]
	v_pk_add_f32 v[4:5], v[118:119], v[4:5] neg_lo:[0,1] neg_hi:[0,1]
	v_pk_add_f32 v[130:131], v[144:145], v[128:129]
	v_pk_mul_f32 v[118:119], v[4:5], v[116:117] op_sel_hi:[1,0]
	v_pk_add_f32 v[128:129], v[144:145], v[128:129] neg_lo:[0,1] neg_hi:[0,1]
	v_pk_fma_f32 v[4:5], v[4:5], v[116:117], v[118:119] op_sel:[1,1,0] op_sel_hi:[0,1,1] neg_lo:[1,0,0]
	v_pk_add_f32 v[116:117], v[110:111], v[122:123]
	v_pk_add_f32 v[110:111], v[110:111], v[122:123] neg_lo:[0,1] neg_hi:[0,1]
	v_pk_add_f32 v[118:119], v[126:127], v[140:141]
	v_pk_add_f32 v[122:123], v[126:127], v[140:141] op_sel:[1,1] op_sel_hi:[0,0] neg_lo:[1,0] neg_hi:[0,1]
	v_pk_add_f32 v[126:127], v[106:107], v[124:125]
	v_pk_add_f32 v[106:107], v[106:107], v[124:125] neg_lo:[0,1] neg_hi:[0,1]
	v_pk_add_f32 v[124:125], v[108:109], v[142:143]
	v_pk_add_f32 v[108:109], v[108:109], v[142:143] op_sel:[1,1] op_sel_hi:[0,0] neg_lo:[1,0] neg_hi:[0,1]
	v_pk_add_f32 v[140:141], v[112:113], v[120:121]
	v_pk_add_f32 v[112:113], v[112:113], v[120:121] op_sel:[1,1] op_sel_hi:[0,0] neg_lo:[1,0] neg_hi:[0,1]
	v_pk_add_f32 v[120:121], v[102:103], v[104:105]
	v_pk_add_f32 v[102:103], v[102:103], v[104:105] neg_lo:[0,1] neg_hi:[0,1]
	v_pk_add_f32 v[104:105], v[114:115], v[4:5]
	v_pk_add_f32 v[4:5], v[114:115], v[4:5] op_sel:[1,1] op_sel_hi:[0,0] neg_lo:[1,0] neg_hi:[0,1]
	v_pk_add_f32 v[114:115], v[116:117], v[118:119]
	v_pk_add_f32 v[116:117], v[116:117], v[118:119] neg_lo:[0,1] neg_hi:[0,1]
	v_pk_add_f32 v[118:119], v[110:111], v[122:123]
	v_pk_add_f32 v[110:111], v[110:111], v[122:123] neg_lo:[0,1] neg_hi:[0,1]
	v_pk_add_f32 v[122:123], v[126:127], v[124:125]
	v_pk_add_f32 v[124:125], v[126:127], v[124:125] neg_lo:[0,1] neg_hi:[0,1]
	v_pk_add_f32 v[126:127], v[106:107], v[108:109]
	v_pk_add_f32 v[106:107], v[106:107], v[108:109] neg_lo:[0,1] neg_hi:[0,1]
	v_pk_add_f32 v[108:109], v[130:131], v[140:141]
	v_pk_add_f32 v[130:131], v[130:131], v[140:141] neg_lo:[0,1] neg_hi:[0,1]
	v_pk_add_f32 v[140:141], v[128:129], v[112:113]
	v_pk_add_f32 v[112:113], v[128:129], v[112:113] neg_lo:[0,1] neg_hi:[0,1]
	v_pk_add_f32 v[128:129], v[120:121], v[104:105]
	v_pk_add_f32 v[104:105], v[120:121], v[104:105] neg_lo:[0,1] neg_hi:[0,1]
	v_pk_add_f32 v[120:121], v[102:103], v[4:5]
	v_pk_add_f32 v[4:5], v[102:103], v[4:5] neg_lo:[0,1] neg_hi:[0,1]
	ds_write2_b64 v133, v[114:115], v[108:109] offset1:72
	ds_write2_b64 v133, v[122:123], v[128:129] offset0:144 offset1:216
	ds_write2_b64 v134, v[118:119], v[140:141] offset0:32 offset1:104
	ds_write2_b64 v134, v[126:127], v[120:121] offset0:176 offset1:248
	ds_write2_b64 v135, v[116:117], v[130:131] offset0:64 offset1:136
	ds_write2_b64 v136, v[124:125], v[104:105] offset0:80 offset1:152
	ds_write2_b64 v137, v[110:111], v[112:113] offset0:96 offset1:168
	ds_write2_b64 v138, v[106:107], v[4:5] offset0:112 offset1:184
	s_cbranch_vccnz .LBB0_778
	s_lshl_b32 s85, s83, 2
	s_add_i32 s85, s85, 0
	s_add_i32 s85, s85, 0x24400
	s_waitcnt lgkmcnt(0)
	s_barrier
	s_cselect_b32 s99, 1, 0
	v_readfirstlane_b32 s98, v0
	s_cmp_lt_u32 s98, 0x100
	s_cbranch_scc1 .Lfft_stg_22863
	s_sleep 8
.Lfft_stg_22863:
	s_cmp_lg_u32 s99, 0
	v_mov_b32_e32 v2, s85
	v_mov_b32_e32 v118, v204
	ds_read_b32 v38, v2
	s_ashr_i32 s85, s84, 31
	v_cvt_f32_i32_e32 v102, v118
	v_and_b32_e32 v2, -8, v118
	v_lshlrev_b32_e32 v119, 3, v118
	v_add3_u32 v116, 0, v2, v119
	v_mul_f32_e32 v102, 0x38800000, v102
	ds_read2st64_b64 v[2:5], v116 offset1:18
	v_cos_f32_e32 v106, v102
	v_sin_f32_e32 v107, v102
	s_waitcnt lgkmcnt(0)
	v_pk_mul_f32 v[102:103], v[4:5], v[106:107] op_sel_hi:[1,0]
	v_add_u32_e32 v122, 0x12000, v116
	v_pk_fma_f32 v[4:5], v[4:5], v[106:107], v[102:103] op_sel:[1,1,0] op_sel_hi:[0,1,1] neg_lo:[1,0,0]
	v_pk_mul_f32 v[102:103], v[106:107], v[106:107] op_sel_hi:[1,0]
	v_add_u32_e32 v124, 0x14400, v116
	v_pk_fma_f32 v[108:109], v[106:107], v[106:107], v[102:103] op_sel:[1,1,0] op_sel_hi:[0,1,1] neg_lo:[1,0,0]
	ds_read2st64_b64 v[102:105], v116 offset0:36 offset1:54
	s_waitcnt lgkmcnt(0)
	v_pk_mul_f32 v[110:111], v[102:103], v[108:109] op_sel_hi:[1,0]
	v_add_u32_e32 v126, 0x16800, v116
	v_pk_fma_f32 v[102:103], v[102:103], v[108:109], v[110:111] op_sel:[1,1,0] op_sel_hi:[0,1,1] neg_lo:[1,0,0]
	v_pk_mul_f32 v[110:111], v[108:109], v[106:107] op_sel_hi:[1,0]
	v_add_u32_e32 v128, 0x18c00, v116
	v_pk_fma_f32 v[108:109], v[108:109], v[106:107], v[110:111] op_sel:[1,1,0] op_sel_hi:[0,1,1] neg_lo:[1,0,0]
	v_add_u32_e32 v130, 0x1b000, v116
	v_pk_mul_f32 v[110:111], v[104:105], v[108:109] op_sel_hi:[1,0]
	v_add_u32_e32 v132, 0x1d400, v116
	v_pk_fma_f32 v[104:105], v[104:105], v[108:109], v[110:111] op_sel:[1,1,0] op_sel_hi:[0,1,1] neg_lo:[1,0,0]
	v_pk_mul_f32 v[110:111], v[108:109], v[106:107] op_sel_hi:[1,0]
	v_add_u32_e32 v134, 0x1f800, v116
	v_pk_fma_f32 v[108:109], v[108:109], v[106:107], v[110:111] op_sel:[1,1,0] op_sel_hi:[0,1,1] neg_lo:[1,0,0]
	ds_read2st64_b64 v[110:113], v116 offset0:72 offset1:90
	s_waitcnt lgkmcnt(0)
	v_pk_mul_f32 v[114:115], v[110:111], v[108:109] op_sel_hi:[1,0]
	v_add_u32_e32 v136, 0x21c00, v116
	v_pk_fma_f32 v[110:111], v[110:111], v[108:109], v[114:115] op_sel:[1,1,0] op_sel_hi:[0,1,1] neg_lo:[1,0,0]
	v_pk_mul_f32 v[114:115], v[108:109], v[106:107] op_sel_hi:[1,0]
	s_lshl_b64 s[84:85], s[84:85], 16
	v_pk_fma_f32 v[108:109], v[108:109], v[106:107], v[114:115] op_sel:[1,1,0] op_sel_hi:[0,1,1] neg_lo:[1,0,0]
	s_add_u32 s84, s88, s84
	v_pk_mul_f32 v[114:115], v[112:113], v[108:109] op_sel_hi:[1,0]
	s_addc_u32 s85, s89, s85
	v_pk_fma_f32 v[112:113], v[112:113], v[108:109], v[114:115] op_sel:[1,1,0] op_sel_hi:[0,1,1] neg_lo:[1,0,0]
	v_pk_mul_f32 v[114:115], v[108:109], v[106:107] op_sel_hi:[1,0]
	s_add_i32 s83, s83, 1
	v_pk_fma_f32 v[108:109], v[108:109], v[106:107], v[114:115] op_sel:[1,1,0] op_sel_hi:[0,1,1] neg_lo:[1,0,0]
	ds_read2st64_b64 v[114:117], v116 offset0:108 offset1:126
	s_waitcnt lgkmcnt(0)
	v_pk_mul_f32 v[120:121], v[114:115], v[108:109] op_sel_hi:[1,0]
	s_cmp_lg_u32 s83, 4
	v_pk_fma_f32 v[114:115], v[114:115], v[108:109], v[120:121] op_sel:[1,1,0] op_sel_hi:[0,1,1] neg_lo:[1,0,0]
	v_pk_mul_f32 v[120:121], v[108:109], v[106:107] op_sel_hi:[1,0]
	s_nop 0
	v_pk_fma_f32 v[108:109], v[108:109], v[106:107], v[120:121] op_sel:[1,1,0] op_sel_hi:[0,1,1] neg_lo:[1,0,0]
	s_nop 0
	v_pk_mul_f32 v[120:121], v[116:117], v[108:109] op_sel_hi:[1,0]
	s_nop 0
	v_pk_fma_f32 v[116:117], v[116:117], v[108:109], v[120:121] op_sel:[1,1,0] op_sel_hi:[0,1,1] neg_lo:[1,0,0]
	v_pk_mul_f32 v[120:121], v[108:109], v[106:107] op_sel_hi:[1,0]
	s_nop 0
	v_pk_fma_f32 v[120:121], v[108:109], v[106:107], v[120:121] op_sel:[1,1,0] op_sel_hi:[0,1,1] neg_lo:[1,0,0]
	ds_read_b64 v[108:109], v122
	s_waitcnt lgkmcnt(0)
	v_pk_mul_f32 v[122:123], v[108:109], v[120:121] op_sel_hi:[1,0]
	s_nop 0
	v_pk_fma_f32 v[108:109], v[108:109], v[120:121], v[122:123] op_sel:[1,1,0] op_sel_hi:[0,1,1] neg_lo:[1,0,0]
	v_pk_mul_f32 v[122:123], v[120:121], v[106:107] op_sel_hi:[1,0]
	s_nop 0
	v_pk_fma_f32 v[120:121], v[120:121], v[106:107], v[122:123] op_sel:[1,1,0] op_sel_hi:[0,1,1] neg_lo:[1,0,0]
	ds_read_b64 v[122:123], v124
	s_waitcnt lgkmcnt(0)
	v_pk_mul_f32 v[124:125], v[122:123], v[120:121] op_sel_hi:[1,0]
	s_nop 0
	v_pk_fma_f32 v[122:123], v[122:123], v[120:121], v[124:125] op_sel:[1,1,0] op_sel_hi:[0,1,1] neg_lo:[1,0,0]
	v_pk_mul_f32 v[124:125], v[120:121], v[106:107] op_sel_hi:[1,0]
	s_nop 0
	v_pk_fma_f32 v[120:121], v[120:121], v[106:107], v[124:125] op_sel:[1,1,0] op_sel_hi:[0,1,1] neg_lo:[1,0,0]
	ds_read_b64 v[124:125], v126
	s_waitcnt lgkmcnt(0)
	v_pk_mul_f32 v[126:127], v[124:125], v[120:121] op_sel_hi:[1,0]
	s_nop 0
	v_pk_fma_f32 v[124:125], v[124:125], v[120:121], v[126:127] op_sel:[1,1,0] op_sel_hi:[0,1,1] neg_lo:[1,0,0]
	v_pk_mul_f32 v[126:127], v[120:121], v[106:107] op_sel_hi:[1,0]
	s_nop 0
	v_pk_fma_f32 v[120:121], v[120:121], v[106:107], v[126:127] op_sel:[1,1,0] op_sel_hi:[0,1,1] neg_lo:[1,0,0]
	ds_read_b64 v[126:127], v128
	s_waitcnt lgkmcnt(0)
	v_pk_mul_f32 v[128:129], v[126:127], v[120:121] op_sel_hi:[1,0]
	s_nop 0
	v_pk_fma_f32 v[126:127], v[126:127], v[120:121], v[128:129] op_sel:[1,1,0] op_sel_hi:[0,1,1] neg_lo:[1,0,0]
	v_pk_mul_f32 v[128:129], v[120:121], v[106:107] op_sel_hi:[1,0]
	s_nop 0
	v_pk_fma_f32 v[120:121], v[120:121], v[106:107], v[128:129] op_sel:[1,1,0] op_sel_hi:[0,1,1] neg_lo:[1,0,0]
	ds_read_b64 v[128:129], v130
	s_waitcnt lgkmcnt(0)
	v_pk_mul_f32 v[130:131], v[128:129], v[120:121] op_sel_hi:[1,0]
	v_pk_add_f32 v[138:139], v[104:105], v[126:127]
	v_pk_fma_f32 v[128:129], v[128:129], v[120:121], v[130:131] op_sel:[1,1,0] op_sel_hi:[0,1,1] neg_lo:[1,0,0]
	v_pk_mul_f32 v[130:131], v[120:121], v[106:107] op_sel_hi:[1,0]
	v_pk_add_f32 v[104:105], v[104:105], v[126:127] neg_lo:[0,1] neg_hi:[0,1]
	v_pk_fma_f32 v[120:121], v[120:121], v[106:107], v[130:131] op_sel:[1,1,0] op_sel_hi:[0,1,1] neg_lo:[1,0,0]
	ds_read_b64 v[130:131], v132
	s_waitcnt lgkmcnt(0)
	v_pk_mul_f32 v[132:133], v[130:131], v[120:121] op_sel_hi:[1,0]
	v_pk_add_f32 v[140:141], v[110:111], v[128:129]
	v_pk_fma_f32 v[130:131], v[130:131], v[120:121], v[132:133] op_sel:[1,1,0] op_sel_hi:[0,1,1] neg_lo:[1,0,0]
	v_pk_mul_f32 v[132:133], v[120:121], v[106:107] op_sel_hi:[1,0]
	v_pk_add_f32 v[128:129], v[110:111], v[128:129] op_sel:[1,1] op_sel_hi:[0,0] neg_lo:[1,0] neg_hi:[0,1]
	v_mov_b64_e32 v[110:111], s[12:13]
	v_pk_fma_f32 v[120:121], v[120:121], v[106:107], v[132:133] op_sel:[1,1,0] op_sel_hi:[0,1,1] neg_lo:[1,0,0]
	ds_read_b64 v[132:133], v134
	s_waitcnt lgkmcnt(0)
	v_pk_mul_f32 v[134:135], v[132:133], v[120:121] op_sel_hi:[1,0]
	v_pk_add_f32 v[142:143], v[112:113], v[130:131]
	v_pk_fma_f32 v[132:133], v[132:133], v[120:121], v[134:135] op_sel:[1,1,0] op_sel_hi:[0,1,1] neg_lo:[1,0,0]
	v_pk_mul_f32 v[134:135], v[120:121], v[106:107] op_sel_hi:[1,0]
	s_nop 0
	v_pk_fma_f32 v[106:107], v[120:121], v[106:107], v[134:135] op_sel:[1,1,0] op_sel_hi:[0,1,1] neg_lo:[1,0,0]
	ds_read_b64 v[120:121], v136
	s_waitcnt lgkmcnt(0)
	v_pk_mul_f32 v[134:135], v[120:121], v[106:107] op_sel_hi:[1,0]
	v_pk_add_f32 v[136:137], v[4:5], v[122:123]
	v_pk_fma_f32 v[120:121], v[120:121], v[106:107], v[134:135] op_sel:[1,1,0] op_sel_hi:[0,1,1] neg_lo:[1,0,0]
	v_pk_add_f32 v[134:135], v[2:3], v[108:109]
	v_pk_add_f32 v[2:3], v[2:3], v[108:109] neg_lo:[0,1] neg_hi:[0,1]
	v_pk_add_f32 v[4:5], v[4:5], v[122:123] neg_lo:[0,1] neg_hi:[0,1]
	v_mov_b64_e32 v[106:107], s[4:5]
	v_pk_mul_f32 v[108:109], v[4:5], v[106:107] op_sel_hi:[1,0]
	v_pk_add_f32 v[122:123], v[102:103], v[124:125]
	v_pk_fma_f32 v[4:5], v[4:5], v[106:107], v[108:109] op_sel:[1,1,0] op_sel_hi:[0,1,1] neg_lo:[1,0,0]
	v_pk_add_f32 v[108:109], v[102:103], v[124:125] neg_lo:[0,1] neg_hi:[0,1]
	v_mov_b64_e32 v[102:103], s[6:7]
	v_pk_mul_f32 v[124:125], v[108:109], v[102:103] op_sel_hi:[1,0]
	v_pk_add_f32 v[144:145], v[114:115], v[132:133]
	v_pk_fma_f32 v[124:125], v[108:109], v[102:103], v[124:125] op_sel:[1,1,0] op_sel_hi:[0,1,1] neg_lo:[1,0,0]
	v_mov_b64_e32 v[108:109], s[10:11]
	v_pk_mul_f32 v[126:127], v[104:105], v[108:109] op_sel_hi:[1,0]
	s_nop 0
	v_pk_fma_f32 v[126:127], v[104:105], v[108:109], v[126:127] op_sel:[1,1,0] op_sel_hi:[0,1,1] neg_lo:[1,0,0]
	v_pk_add_f32 v[104:105], v[112:113], v[130:131] neg_lo:[0,1] neg_hi:[0,1]
	s_nop 0
	v_pk_mul_f32 v[112:113], v[104:105], v[110:111] op_sel_hi:[1,0]
	s_nop 0
	v_pk_fma_f32 v[130:131], v[104:105], v[110:111], v[112:113] op_sel:[1,1,0] op_sel_hi:[0,1,1] neg_lo:[1,0,0]
	v_pk_add_f32 v[112:113], v[114:115], v[132:133] neg_lo:[0,1] neg_hi:[0,1]
	v_mov_b64_e32 v[104:105], s[14:15]
	v_pk_mul_f32 v[114:115], v[112:113], v[104:105] op_sel_hi:[1,0]
	v_pk_add_f32 v[132:133], v[116:117], v[120:121]
	v_pk_fma_f32 v[114:115], v[112:113], v[104:105], v[114:115] op_sel:[1,1,0] op_sel_hi:[0,1,1] neg_lo:[1,0,0]
	v_pk_add_f32 v[116:117], v[116:117], v[120:121] neg_lo:[0,1] neg_hi:[0,1]
	v_mov_b64_e32 v[112:113], s[16:17]
	v_pk_mul_f32 v[120:121], v[116:117], v[112:113] op_sel_hi:[1,0]
	s_nop 0
	v_pk_fma_f32 v[116:117], v[116:117], v[112:113], v[120:121] op_sel:[1,1,0] op_sel_hi:[0,1,1] neg_lo:[1,0,0]
	v_pk_add_f32 v[120:121], v[134:135], v[140:141]
	v_pk_add_f32 v[134:135], v[134:135], v[140:141] neg_lo:[0,1] neg_hi:[0,1]
	v_pk_add_f32 v[140:141], v[136:137], v[142:143]
	v_pk_add_f32 v[136:137], v[136:137], v[142:143] neg_lo:[0,1] neg_hi:[0,1]
	s_nop 0
	v_pk_mul_f32 v[142:143], v[136:137], v[102:103] op_sel_hi:[1,0]
	s_nop 0
	v_pk_fma_f32 v[136:137], v[136:137], v[102:103], v[142:143] op_sel:[1,1,0] op_sel_hi:[0,1,1] neg_lo:[1,0,0]
	v_pk_add_f32 v[142:143], v[122:123], v[144:145]
	v_pk_add_f32 v[122:123], v[122:123], v[144:145] op_sel:[1,1] op_sel_hi:[0,0] neg_lo:[1,0] neg_hi:[0,1]
	v_pk_add_f32 v[144:145], v[138:139], v[132:133]
	v_pk_add_f32 v[132:133], v[138:139], v[132:133] neg_lo:[0,1] neg_hi:[0,1]
	s_nop 0
	v_pk_mul_f32 v[138:139], v[132:133], v[104:105] op_sel_hi:[1,0]
	s_nop 0
	v_pk_fma_f32 v[132:133], v[132:133], v[104:105], v[138:139] op_sel:[1,1,0] op_sel_hi:[0,1,1] neg_lo:[1,0,0]
	v_pk_add_f32 v[138:139], v[2:3], v[128:129]
	v_pk_add_f32 v[2:3], v[2:3], v[128:129] neg_lo:[0,1] neg_hi:[0,1]
	v_pk_add_f32 v[128:129], v[4:5], v[130:131]
	v_pk_add_f32 v[4:5], v[4:5], v[130:131] neg_lo:[0,1] neg_hi:[0,1]
	s_nop 0
	v_pk_mul_f32 v[130:131], v[4:5], v[102:103] op_sel_hi:[1,0]
	s_nop 0
	v_pk_fma_f32 v[4:5], v[4:5], v[102:103], v[130:131] op_sel:[1,1,0] op_sel_hi:[0,1,1] neg_lo:[1,0,0]
	v_pk_add_f32 v[130:131], v[124:125], v[114:115]
	v_pk_add_f32 v[114:115], v[124:125], v[114:115] op_sel:[1,1] op_sel_hi:[0,0] neg_lo:[1,0] neg_hi:[0,1]
	v_pk_add_f32 v[124:125], v[126:127], v[116:117]
	v_pk_add_f32 v[116:117], v[126:127], v[116:117] neg_lo:[0,1] neg_hi:[0,1]
	s_nop 0
	v_pk_mul_f32 v[126:127], v[116:117], v[104:105] op_sel_hi:[1,0]
	s_nop 0
	v_pk_fma_f32 v[116:117], v[116:117], v[104:105], v[126:127] op_sel:[1,1,0] op_sel_hi:[0,1,1] neg_lo:[1,0,0]
	v_pk_add_f32 v[126:127], v[120:121], v[142:143]
	v_pk_add_f32 v[120:121], v[120:121], v[142:143] neg_lo:[0,1] neg_hi:[0,1]
	v_pk_add_f32 v[142:143], v[140:141], v[144:145]
	v_pk_add_f32 v[140:141], v[140:141], v[144:145] op_sel:[1,1] op_sel_hi:[0,0] neg_lo:[1,0] neg_hi:[0,1]
	v_pk_add_f32 v[144:145], v[134:135], v[122:123]
	v_pk_add_f32 v[122:123], v[134:135], v[122:123] neg_lo:[0,1] neg_hi:[0,1]
	v_pk_add_f32 v[134:135], v[136:137], v[132:133]
	v_pk_add_f32 v[132:133], v[136:137], v[132:133] op_sel:[1,1] op_sel_hi:[0,0] neg_lo:[1,0] neg_hi:[0,1]
	v_pk_add_f32 v[136:137], v[138:139], v[130:131]
	v_pk_add_f32 v[130:131], v[138:139], v[130:131] neg_lo:[0,1] neg_hi:[0,1]
	v_pk_add_f32 v[138:139], v[128:129], v[124:125]
	v_pk_add_f32 v[124:125], v[128:129], v[124:125] op_sel:[1,1] op_sel_hi:[0,0] neg_lo:[1,0] neg_hi:[0,1]
	v_pk_add_f32 v[128:129], v[2:3], v[114:115]
	v_pk_add_f32 v[2:3], v[2:3], v[114:115] neg_lo:[0,1] neg_hi:[0,1]
	v_pk_add_f32 v[114:115], v[4:5], v[116:117]
	v_pk_add_f32 v[4:5], v[4:5], v[116:117] op_sel:[1,1] op_sel_hi:[0,0] neg_lo:[1,0] neg_hi:[0,1]
	v_pk_add_f32 v[116:117], v[126:127], v[142:143]
	v_pk_add_f32 v[2:3], v[2:3], v[4:5]
	s_waitcnt vmcnt(47)
	v_pk_mul_f32 v[4:5], v[38:39], v[116:117] op_sel_hi:[0,1]
	v_lshlrev_b32_e32 v116, 1, v118
	v_ashrrev_i32_e32 v117, 31, v116
	v_pk_add_f32 v[114:115], v[128:129], v[114:115]
	v_lshl_add_u64 v[128:129], v[116:117], 2, s[84:85]
	global_store_dwordx2 v[128:129], v[4:5], off
	v_add_u32_e32 v128, 0x800, v116
	v_pk_add_f32 v[122:123], v[122:123], v[132:133]
	v_pk_add_f32 v[132:133], v[136:137], v[138:139]
	v_ashrrev_i32_e32 v129, 31, v128
	v_pk_add_f32 v[126:127], v[144:145], v[134:135]
	v_pk_mul_f32 v[4:5], v[38:39], v[132:133] op_sel_hi:[0,1]
	v_lshl_add_u64 v[128:129], v[128:129], 2, s[84:85]
	global_store_dwordx2 v[128:129], v[4:5], off
	v_pk_mul_f32 v[4:5], v[38:39], v[126:127] op_sel_hi:[0,1]
	v_add_u32_e32 v126, 0x1000, v116
	v_ashrrev_i32_e32 v127, 31, v126
	v_lshl_add_u64 v[126:127], v[126:127], 2, s[84:85]
	global_store_dwordx2 v[126:127], v[4:5], off
	v_pk_mul_f32 v[4:5], v[38:39], v[114:115] op_sel_hi:[0,1]
	v_add_u32_e32 v114, 0x1800, v116
	v_ashrrev_i32_e32 v115, 31, v114
	v_lshl_add_u64 v[114:115], v[114:115], 2, s[84:85]
	global_store_dwordx2 v[114:115], v[4:5], off
	v_add_u32_e32 v114, 0x2000, v116
	v_pk_add_f32 v[120:121], v[120:121], v[140:141]
	v_ashrrev_i32_e32 v115, 31, v114
	v_pk_mul_f32 v[4:5], v[38:39], v[120:121] op_sel_hi:[0,1]
	v_lshl_add_u64 v[114:115], v[114:115], 2, s[84:85]
	global_store_dwordx2 v[114:115], v[4:5], off
	v_add_u32_e32 v114, 0x2800, v116
	v_pk_add_f32 v[124:125], v[130:131], v[124:125]
	v_ashrrev_i32_e32 v115, 31, v114
	v_pk_mul_f32 v[4:5], v[38:39], v[124:125] op_sel_hi:[0,1]
	v_lshl_add_u64 v[114:115], v[114:115], 2, s[84:85]
	global_store_dwordx2 v[114:115], v[4:5], off
	v_add_u32_e32 v114, 0x3000, v116
	v_ashrrev_i32_e32 v115, 31, v114
	v_pk_mul_f32 v[4:5], v[38:39], v[122:123] op_sel_hi:[0,1]
	v_lshl_add_u64 v[114:115], v[114:115], 2, s[84:85]
	v_add_u32_e32 v130, 0x200, v118
	global_store_dwordx2 v[114:115], v[4:5], off
	v_add_u32_e32 v4, 0x3800, v116
	v_cvt_f32_i32_e32 v114, v130
	v_ashrrev_i32_e32 v5, 31, v4
	v_pk_mul_f32 v[2:3], v[38:39], v[2:3] op_sel_hi:[0,1]
	v_lshl_add_u64 v[4:5], v[4:5], 2, s[84:85]
	global_store_dwordx2 v[4:5], v[2:3], off
	v_and_b32_e32 v2, -8, v130
	v_add3_u32 v128, 0, v2, v119
	v_mul_f32_e32 v114, 0x38800000, v114
	ds_read2st64_b64 v[2:5], v128 offset0:8 offset1:26
	v_cos_f32_e32 v118, v114
	v_sin_f32_e32 v119, v114
	s_waitcnt lgkmcnt(0)
	v_pk_mul_f32 v[114:115], v[4:5], v[118:119] op_sel_hi:[1,0]
	ds_read2st64_b64 v[120:123], v128 offset0:44 offset1:62
	v_pk_fma_f32 v[4:5], v[4:5], v[118:119], v[114:115] op_sel:[1,1,0] op_sel_hi:[0,1,1] neg_lo:[1,0,0]
	v_pk_mul_f32 v[114:115], v[118:119], v[118:119] op_sel_hi:[1,0]
	v_add_u32_e32 v131, 0x1000, v128
	v_pk_fma_f32 v[114:115], v[118:119], v[118:119], v[114:115] op_sel:[1,1,0] op_sel_hi:[0,1,1] neg_lo:[1,0,0]
	v_add_u32_e32 v134, 0x13000, v128
	s_waitcnt lgkmcnt(0)
	v_pk_mul_f32 v[116:117], v[120:121], v[114:115] op_sel_hi:[1,0]
	v_add_u32_e32 v136, 0x15400, v128
	v_pk_fma_f32 v[116:117], v[120:121], v[114:115], v[116:117] op_sel:[1,1,0] op_sel_hi:[0,1,1] neg_lo:[1,0,0]
	v_pk_mul_f32 v[120:121], v[114:115], v[118:119] op_sel_hi:[1,0]
	v_add_u32_e32 v138, 0x17800, v128
	v_pk_fma_f32 v[120:121], v[114:115], v[118:119], v[120:121] op_sel:[1,1,0] op_sel_hi:[0,1,1] neg_lo:[1,0,0]
	v_add_u32_e32 v140, 0x19c00, v128
	v_pk_mul_f32 v[114:115], v[122:123], v[120:121] op_sel_hi:[1,0]
	v_add_u32_e32 v142, 0x1c000, v128
	v_pk_fma_f32 v[114:115], v[122:123], v[120:121], v[114:115] op_sel:[1,1,0] op_sel_hi:[0,1,1] neg_lo:[1,0,0]
	v_pk_mul_f32 v[122:123], v[120:121], v[118:119] op_sel_hi:[1,0]
	v_add_u32_e32 v144, 0x1e400, v128
	v_pk_fma_f32 v[124:125], v[120:121], v[118:119], v[122:123] op_sel:[1,1,0] op_sel_hi:[0,1,1] neg_lo:[1,0,0]
	ds_read2st64_b64 v[120:123], v128 offset0:80 offset1:98
	s_waitcnt lgkmcnt(0)
	v_pk_mul_f32 v[126:127], v[120:121], v[124:125] op_sel_hi:[1,0]
	v_add_u32_e32 v146, 0x20800, v128
	v_pk_fma_f32 v[120:121], v[120:121], v[124:125], v[126:127] op_sel:[1,1,0] op_sel_hi:[0,1,1] neg_lo:[1,0,0]
	v_pk_mul_f32 v[126:127], v[124:125], v[118:119] op_sel_hi:[1,0]
	v_add_u32_e32 v148, 0x22c00, v128
	v_pk_fma_f32 v[124:125], v[124:125], v[118:119], v[126:127] op_sel:[1,1,0] op_sel_hi:[0,1,1] neg_lo:[1,0,0]
	s_nop 0
	v_pk_mul_f32 v[126:127], v[122:123], v[124:125] op_sel_hi:[1,0]
	s_nop 0
	v_pk_fma_f32 v[122:123], v[122:123], v[124:125], v[126:127] op_sel:[1,1,0] op_sel_hi:[0,1,1] neg_lo:[1,0,0]
	v_pk_mul_f32 v[126:127], v[124:125], v[118:119] op_sel_hi:[1,0]
	s_nop 0
	v_pk_fma_f32 v[126:127], v[124:125], v[118:119], v[126:127] op_sel:[1,1,0] op_sel_hi:[0,1,1] neg_lo:[1,0,0]
	ds_read_b64 v[124:125], v128 offset:59392
	s_waitcnt lgkmcnt(0)
	v_pk_mul_f32 v[128:129], v[124:125], v[126:127] op_sel_hi:[1,0]
	s_nop 0
	v_pk_fma_f32 v[124:125], v[124:125], v[126:127], v[128:129] op_sel:[1,1,0] op_sel_hi:[0,1,1] neg_lo:[1,0,0]
	v_pk_mul_f32 v[128:129], v[126:127], v[118:119] op_sel_hi:[1,0]
	s_nop 0
	v_pk_fma_f32 v[128:129], v[126:127], v[118:119], v[128:129] op_sel:[1,1,0] op_sel_hi:[0,1,1] neg_lo:[1,0,0]
	ds_read_b64 v[126:127], v131 offset:64512
	s_waitcnt lgkmcnt(0)
	v_pk_mul_f32 v[132:133], v[126:127], v[128:129] op_sel_hi:[1,0]
	s_nop 0
	v_pk_fma_f32 v[126:127], v[126:127], v[128:129], v[132:133] op_sel:[1,1,0] op_sel_hi:[0,1,1] neg_lo:[1,0,0]
	v_pk_mul_f32 v[132:133], v[128:129], v[118:119] op_sel_hi:[1,0]
	s_nop 0
	v_pk_fma_f32 v[132:133], v[128:129], v[118:119], v[132:133] op_sel:[1,1,0] op_sel_hi:[0,1,1] neg_lo:[1,0,0]
	ds_read_b64 v[128:129], v134
	s_waitcnt lgkmcnt(0)
	v_pk_mul_f32 v[134:135], v[128:129], v[132:133] op_sel_hi:[1,0]
	s_nop 0
	v_pk_fma_f32 v[128:129], v[128:129], v[132:133], v[134:135] op_sel:[1,1,0] op_sel_hi:[0,1,1] neg_lo:[1,0,0]
	v_pk_mul_f32 v[134:135], v[132:133], v[118:119] op_sel_hi:[1,0]
	s_nop 0
	v_pk_fma_f32 v[132:133], v[132:133], v[118:119], v[134:135] op_sel:[1,1,0] op_sel_hi:[0,1,1] neg_lo:[1,0,0]
	ds_read_b64 v[134:135], v136
	s_waitcnt lgkmcnt(0)
	v_pk_mul_f32 v[136:137], v[134:135], v[132:133] op_sel_hi:[1,0]
	s_nop 0
	v_pk_fma_f32 v[134:135], v[134:135], v[132:133], v[136:137] op_sel:[1,1,0] op_sel_hi:[0,1,1] neg_lo:[1,0,0]
	v_pk_mul_f32 v[136:137], v[132:133], v[118:119] op_sel_hi:[1,0]
	s_nop 0
	v_pk_fma_f32 v[132:133], v[132:133], v[118:119], v[136:137] op_sel:[1,1,0] op_sel_hi:[0,1,1] neg_lo:[1,0,0]
	ds_read_b64 v[136:137], v138
	s_waitcnt lgkmcnt(0)
	v_pk_mul_f32 v[138:139], v[136:137], v[132:133] op_sel_hi:[1,0]
	s_nop 0
	v_pk_fma_f32 v[136:137], v[136:137], v[132:133], v[138:139] op_sel:[1,1,0] op_sel_hi:[0,1,1] neg_lo:[1,0,0]
	v_pk_mul_f32 v[138:139], v[132:133], v[118:119] op_sel_hi:[1,0]
	s_nop 0
	v_pk_fma_f32 v[132:133], v[132:133], v[118:119], v[138:139] op_sel:[1,1,0] op_sel_hi:[0,1,1] neg_lo:[1,0,0]
	ds_read_b64 v[138:139], v140
	s_waitcnt lgkmcnt(0)
	v_pk_mul_f32 v[140:141], v[138:139], v[132:133] op_sel_hi:[1,0]
	s_nop 0
	v_pk_fma_f32 v[138:139], v[138:139], v[132:133], v[140:141] op_sel:[1,1,0] op_sel_hi:[0,1,1] neg_lo:[1,0,0]
	v_pk_mul_f32 v[140:141], v[132:133], v[118:119] op_sel_hi:[1,0]
	s_nop 0
	v_pk_fma_f32 v[132:133], v[132:133], v[118:119], v[140:141] op_sel:[1,1,0] op_sel_hi:[0,1,1] neg_lo:[1,0,0]
	ds_read_b64 v[140:141], v142
	s_waitcnt lgkmcnt(0)
	v_pk_mul_f32 v[142:143], v[140:141], v[132:133] op_sel_hi:[1,0]
	s_nop 0
	v_pk_fma_f32 v[140:141], v[140:141], v[132:133], v[142:143] op_sel:[1,1,0] op_sel_hi:[0,1,1] neg_lo:[1,0,0]
	v_pk_mul_f32 v[142:143], v[132:133], v[118:119] op_sel_hi:[1,0]
	s_nop 0
	v_pk_fma_f32 v[132:133], v[132:133], v[118:119], v[142:143] op_sel:[1,1,0] op_sel_hi:[0,1,1] neg_lo:[1,0,0]
	ds_read_b64 v[142:143], v144
	s_waitcnt lgkmcnt(0)
	v_pk_mul_f32 v[144:145], v[142:143], v[132:133] op_sel_hi:[1,0]
	s_nop 0
	v_pk_fma_f32 v[142:143], v[142:143], v[132:133], v[144:145] op_sel:[1,1,0] op_sel_hi:[0,1,1] neg_lo:[1,0,0]
	v_pk_mul_f32 v[144:145], v[132:133], v[118:119] op_sel_hi:[1,0]
	s_nop 0
	v_pk_fma_f32 v[132:133], v[132:133], v[118:119], v[144:145] op_sel:[1,1,0] op_sel_hi:[0,1,1] neg_lo:[1,0,0]
	ds_read_b64 v[144:145], v146
	s_waitcnt lgkmcnt(0)
	v_pk_mul_f32 v[146:147], v[144:145], v[132:133] op_sel_hi:[1,0]
	s_nop 0
	v_pk_fma_f32 v[144:145], v[144:145], v[132:133], v[146:147] op_sel:[1,1,0] op_sel_hi:[0,1,1] neg_lo:[1,0,0]
	v_pk_mul_f32 v[146:147], v[132:133], v[118:119] op_sel_hi:[1,0]
	s_nop 0
	v_pk_fma_f32 v[118:119], v[132:133], v[118:119], v[146:147] op_sel:[1,1,0] op_sel_hi:[0,1,1] neg_lo:[1,0,0]
	ds_read_b64 v[132:133], v148
	s_waitcnt lgkmcnt(0)
	v_pk_mul_f32 v[146:147], v[132:133], v[118:119] op_sel_hi:[1,0]
	s_nop 0
	v_pk_fma_f32 v[118:119], v[132:133], v[118:119], v[146:147] op_sel:[1,1,0] op_sel_hi:[0,1,1] neg_lo:[1,0,0]
	v_pk_add_f32 v[132:133], v[2:3], v[128:129]
	v_pk_add_f32 v[2:3], v[2:3], v[128:129] neg_lo:[0,1] neg_hi:[0,1]
	v_pk_add_f32 v[128:129], v[4:5], v[134:135]
	v_pk_add_f32 v[4:5], v[4:5], v[134:135] neg_lo:[0,1] neg_hi:[0,1]
	s_nop 0
	v_pk_mul_f32 v[134:135], v[4:5], v[106:107] op_sel_hi:[1,0]
	s_nop 0
	v_pk_fma_f32 v[4:5], v[4:5], v[106:107], v[134:135] op_sel:[1,1,0] op_sel_hi:[0,1,1] neg_lo:[1,0,0]
	v_pk_add_f32 v[106:107], v[116:117], v[136:137]
	v_pk_add_f32 v[116:117], v[116:117], v[136:137] neg_lo:[0,1] neg_hi:[0,1]
	s_nop 0
	v_pk_mul_f32 v[134:135], v[116:117], v[102:103] op_sel_hi:[1,0]
	s_nop 0
	v_pk_fma_f32 v[116:117], v[116:117], v[102:103], v[134:135] op_sel:[1,1,0] op_sel_hi:[0,1,1] neg_lo:[1,0,0]
	v_pk_add_f32 v[134:135], v[114:115], v[138:139]
	v_pk_add_f32 v[114:115], v[114:115], v[138:139] neg_lo:[0,1] neg_hi:[0,1]
	s_nop 0
	v_pk_mul_f32 v[136:137], v[114:115], v[108:109] op_sel_hi:[1,0]
	s_nop 0
	v_pk_fma_f32 v[108:109], v[114:115], v[108:109], v[136:137] op_sel:[1,1,0] op_sel_hi:[0,1,1] neg_lo:[1,0,0]
	v_pk_add_f32 v[136:137], v[122:123], v[142:143]
	v_pk_add_f32 v[122:123], v[122:123], v[142:143] neg_lo:[0,1] neg_hi:[0,1]
	v_pk_add_f32 v[114:115], v[120:121], v[140:141]
	v_pk_mul_f32 v[138:139], v[122:123], v[110:111] op_sel_hi:[1,0]
	v_pk_add_f32 v[120:121], v[120:121], v[140:141] op_sel:[1,1] op_sel_hi:[0,0] neg_lo:[1,0] neg_hi:[0,1]
	s_nop 0
	v_pk_fma_f32 v[110:111], v[122:123], v[110:111], v[138:139] op_sel:[1,1,0] op_sel_hi:[0,1,1] neg_lo:[1,0,0]
	v_pk_add_f32 v[122:123], v[124:125], v[144:145]
	v_pk_add_f32 v[124:125], v[124:125], v[144:145] neg_lo:[0,1] neg_hi:[0,1]
	s_nop 0
	v_pk_mul_f32 v[138:139], v[124:125], v[104:105] op_sel_hi:[1,0]
	s_nop 0
	v_pk_fma_f32 v[124:125], v[124:125], v[104:105], v[138:139] op_sel:[1,1,0] op_sel_hi:[0,1,1] neg_lo:[1,0,0]
	v_pk_add_f32 v[138:139], v[126:127], v[118:119]
	v_pk_add_f32 v[118:119], v[126:127], v[118:119] neg_lo:[0,1] neg_hi:[0,1]
	s_nop 0
	v_pk_mul_f32 v[126:127], v[118:119], v[112:113] op_sel_hi:[1,0]
	s_nop 0
	v_pk_fma_f32 v[112:113], v[118:119], v[112:113], v[126:127] op_sel:[1,1,0] op_sel_hi:[0,1,1] neg_lo:[1,0,0]
	v_pk_add_f32 v[118:119], v[132:133], v[114:115]
	v_pk_add_f32 v[114:115], v[132:133], v[114:115] neg_lo:[0,1] neg_hi:[0,1]
	v_pk_add_f32 v[126:127], v[128:129], v[136:137]
	v_pk_add_f32 v[128:129], v[128:129], v[136:137] neg_lo:[0,1] neg_hi:[0,1]
	s_nop 0
	v_pk_mul_f32 v[132:133], v[128:129], v[102:103] op_sel_hi:[1,0]
	s_nop 0
	v_pk_fma_f32 v[128:129], v[128:129], v[102:103], v[132:133] op_sel:[1,1,0] op_sel_hi:[0,1,1] neg_lo:[1,0,0]
	v_pk_add_f32 v[132:133], v[106:107], v[122:123]
	v_pk_add_f32 v[106:107], v[106:107], v[122:123] op_sel:[1,1] op_sel_hi:[0,0] neg_lo:[1,0] neg_hi:[0,1]
	v_pk_add_f32 v[122:123], v[134:135], v[138:139]
	v_pk_add_f32 v[134:135], v[134:135], v[138:139] neg_lo:[0,1] neg_hi:[0,1]
	s_nop 0
	v_pk_mul_f32 v[136:137], v[134:135], v[104:105] op_sel_hi:[1,0]
	s_nop 0
	v_pk_fma_f32 v[134:135], v[134:135], v[104:105], v[136:137] op_sel:[1,1,0] op_sel_hi:[0,1,1] neg_lo:[1,0,0]
	v_pk_add_f32 v[136:137], v[2:3], v[120:121]
	v_pk_add_f32 v[2:3], v[2:3], v[120:121] neg_lo:[0,1] neg_hi:[0,1]
	v_pk_add_f32 v[120:121], v[4:5], v[110:111]
	v_pk_add_f32 v[4:5], v[4:5], v[110:111] neg_lo:[0,1] neg_hi:[0,1]
	s_nop 0
	v_pk_mul_f32 v[110:111], v[4:5], v[102:103] op_sel_hi:[1,0]
	s_nop 0
	v_pk_fma_f32 v[4:5], v[4:5], v[102:103], v[110:111] op_sel:[1,1,0] op_sel_hi:[0,1,1] neg_lo:[1,0,0]
	v_pk_add_f32 v[102:103], v[116:117], v[124:125]
	v_pk_add_f32 v[110:111], v[116:117], v[124:125] op_sel:[1,1] op_sel_hi:[0,0] neg_lo:[1,0] neg_hi:[0,1]
	v_pk_add_f32 v[116:117], v[108:109], v[112:113]
	v_pk_add_f32 v[108:109], v[108:109], v[112:113] neg_lo:[0,1] neg_hi:[0,1]
	v_pk_add_f32 v[124:125], v[114:115], v[106:107]
	v_pk_mul_f32 v[112:113], v[108:109], v[104:105] op_sel_hi:[1,0]
	v_pk_add_f32 v[106:107], v[114:115], v[106:107] neg_lo:[0,1] neg_hi:[0,1]
	v_pk_fma_f32 v[104:105], v[108:109], v[104:105], v[112:113] op_sel:[1,1,0] op_sel_hi:[0,1,1] neg_lo:[1,0,0]
	v_pk_add_f32 v[108:109], v[118:119], v[132:133]
	v_pk_add_f32 v[112:113], v[118:119], v[132:133] neg_lo:[0,1] neg_hi:[0,1]
	v_pk_add_f32 v[118:119], v[126:127], v[122:123]
	v_pk_add_f32 v[132:133], v[120:121], v[116:117]
	v_pk_add_f32 v[116:117], v[120:121], v[116:117] op_sel:[1,1] op_sel_hi:[0,0] neg_lo:[1,0] neg_hi:[0,1]
	v_pk_add_f32 v[120:121], v[2:3], v[110:111]
	v_pk_add_f32 v[2:3], v[2:3], v[110:111] neg_lo:[0,1] neg_hi:[0,1]
	v_pk_add_f32 v[110:111], v[4:5], v[104:105]
	v_pk_add_f32 v[4:5], v[4:5], v[104:105] op_sel:[1,1] op_sel_hi:[0,0] neg_lo:[1,0] neg_hi:[0,1]
	v_pk_add_f32 v[104:105], v[108:109], v[118:119]
	v_pk_add_f32 v[2:3], v[2:3], v[4:5]
	v_pk_mul_f32 v[4:5], v[38:39], v[104:105] op_sel_hi:[0,1]
	v_lshlrev_b32_e32 v104, 1, v130
	v_pk_add_f32 v[122:123], v[126:127], v[122:123] op_sel:[1,1] op_sel_hi:[0,0] neg_lo:[1,0] neg_hi:[0,1]
	v_pk_add_f32 v[114:115], v[128:129], v[134:135]
	v_pk_add_f32 v[126:127], v[128:129], v[134:135] op_sel:[1,1] op_sel_hi:[0,0] neg_lo:[1,0] neg_hi:[0,1]
	v_pk_add_f32 v[128:129], v[136:137], v[102:103]
	v_pk_add_f32 v[102:103], v[136:137], v[102:103] neg_lo:[0,1] neg_hi:[0,1]
	v_ashrrev_i32_e32 v105, 31, v104
	v_pk_add_f32 v[108:109], v[112:113], v[122:123]
	v_pk_add_f32 v[112:113], v[124:125], v[114:115]
	v_pk_add_f32 v[114:115], v[128:129], v[132:133]
	v_pk_add_f32 v[102:103], v[102:103], v[116:117]
	v_lshl_add_u64 v[116:117], v[104:105], 2, s[84:85]
	global_store_dwordx2 v[116:117], v[4:5], off
	v_pk_mul_f32 v[4:5], v[38:39], v[114:115] op_sel_hi:[0,1]
	v_add_u32_e32 v114, 0x800, v104
	v_ashrrev_i32_e32 v115, 31, v114
	v_lshl_add_u64 v[114:115], v[114:115], 2, s[84:85]
	global_store_dwordx2 v[114:115], v[4:5], off
	v_pk_mul_f32 v[4:5], v[38:39], v[112:113] op_sel_hi:[0,1]
	v_add_u32_e32 v112, 0x1000, v104
	v_ashrrev_i32_e32 v113, 31, v112
	v_pk_add_f32 v[110:111], v[120:121], v[110:111]
	v_lshl_add_u64 v[112:113], v[112:113], 2, s[84:85]
	global_store_dwordx2 v[112:113], v[4:5], off
	v_pk_mul_f32 v[4:5], v[38:39], v[110:111] op_sel_hi:[0,1]
	v_add_u32_e32 v110, 0x1800, v104
	v_ashrrev_i32_e32 v111, 31, v110
	v_lshl_add_u64 v[110:111], v[110:111], 2, s[84:85]
	global_store_dwordx2 v[110:111], v[4:5], off
	v_pk_mul_f32 v[4:5], v[38:39], v[108:109] op_sel_hi:[0,1]
	v_add_u32_e32 v108, 0x2000, v104
	v_ashrrev_i32_e32 v109, 31, v108
	v_lshl_add_u64 v[108:109], v[108:109], 2, s[84:85]
	global_store_dwordx2 v[108:109], v[4:5], off
	v_pk_mul_f32 v[4:5], v[38:39], v[102:103] op_sel_hi:[0,1]
	v_add_u32_e32 v102, 0x2800, v104
	v_ashrrev_i32_e32 v103, 31, v102
	v_lshl_add_u64 v[102:103], v[102:103], 2, s[84:85]
	global_store_dwordx2 v[102:103], v[4:5], off
	v_add_u32_e32 v102, 0x3000, v104
	v_pk_add_f32 v[106:107], v[106:107], v[126:127]
	v_ashrrev_i32_e32 v103, 31, v102
	v_pk_mul_f32 v[4:5], v[38:39], v[106:107] op_sel_hi:[0,1]
	v_lshl_add_u64 v[102:103], v[102:103], 2, s[84:85]
	global_store_dwordx2 v[102:103], v[4:5], off
	v_add_u32_e32 v4, 0x3800, v104
	v_ashrrev_i32_e32 v5, 31, v4
	v_pk_mul_f32 v[2:3], v[38:39], v[2:3] op_sel_hi:[0,1]
	v_lshl_add_u64 v[4:5], v[4:5], 2, s[84:85]
	global_store_dwordx2 v[4:5], v[2:3], off
	s_waitcnt lgkmcnt(0)
	s_barrier
	s_cbranch_scc1 .LBB0_755
	v_readlane_b32 s86, v253, 12
	s_add_i32 s95, s95, s86
	s_cmpk_lt_i32 s95, 0x100
	s_barrier
	v_readlane_b32 s87, v253, 13
	s_cbranch_scc1 .LBB0_750
	v_readlane_b32 s88, v253, 16
	v_readlane_b32 s84, v253, 31
	v_readlane_b32 s92, v253, 20
	v_readlane_b32 s60, v252, 57
	v_readlane_b32 s64, v252, 41
	v_readlane_b32 s36, v253, 14
	v_readlane_b32 s94, v253, 22
	v_readlane_b32 s95, v253, 23
	s_mov_b32 s92, s84
	v_readlane_b32 s97, v253, 28
	v_readlane_b32 s63, v253, 27
	v_readlane_b32 s61, v252, 58
	v_readlane_b32 s56, v252, 59
	v_readlane_b32 s72, v252, 49
	v_readlane_b32 s73, v252, 50
	s_mov_b32 s62, s86
	v_readlane_b32 s37, v253, 15
	v_readlane_b32 s85, v253, 32
	v_readlane_b32 s89, v253, 17
	v_readlane_b32 s90, v253, 18
	v_readlane_b32 s91, v253, 19
	v_readlane_b32 s93, v253, 21
	v_readlane_b32 s65, v252, 42
	v_readlane_b32 s66, v252, 43
	v_readlane_b32 s67, v252, 44
	v_readlane_b32 s68, v252, 45
	v_readlane_b32 s69, v252, 46
	v_readlane_b32 s70, v252, 47
	v_readlane_b32 s71, v252, 48
	v_readlane_b32 s74, v252, 51
	v_readlane_b32 s75, v252, 52
	v_readlane_b32 s76, v252, 53
	v_readlane_b32 s77, v252, 54
	v_readlane_b32 s78, v252, 55
	v_readlane_b32 s79, v252, 56
